# speedup vs baseline: 1.0045x; 1.0045x over previous
_Z4ln_kPKfS0_S0_S0_PfPDF16_:
	v_lshlrev_b32_e32 v64, 4, v0
	s_getpc_b64 s[92:93]
	s_add_u32 s92, s92, 0xa2f8
	s_addc_u32 s93, s93, 0x0
	global_load_dwordx4 v[60:63], v64, s[92:93]
	v_add_u32_e32 v64, 0x1000, v64
	global_load_dwordx4 v[60:63], v64, s[92:93]
	v_add_u32_e32 v64, 0x1000, v64
	global_load_dwordx4 v[60:63], v64, s[92:93]
	v_add_u32_e32 v64, 0x1000, v64
	global_load_dwordx4 v[60:63], v64, s[92:93]
	v_lshlrev_b32_e32 v64, 4, v0
	s_load_dwordx8 s[4:11], s[0:1], 0x0
	v_lshrrev_b32_e32 v1, 6, v0
	v_lshl_or_b32 v54, s2, 2, v1
	s_movk_i32 s12, 0xc00
	v_and_b32_e32 v55, 63, v0
	s_waitcnt lgkmcnt(0)
	v_mov_b64_e32 v[2:3], s[4:5]
	v_mad_i64_i32 v[4:5], s[2:3], v54, s12, v[2:3]
	v_mov_b64_e32 v[2:3], s[6:7]
	v_mad_i64_i32 v[6:7], s[2:3], v54, s12, v[2:3]
	v_lshlrev_b32_e32 v2, 4, v55
	v_mov_b32_e32 v3, 0
	v_lshl_add_u64 v[30:31], v[6:7], 0, v[2:3]
	v_lshl_add_u64 v[28:29], v[4:5], 0, v[2:3]
	global_load_dwordx4 v[4:7], v[30:31], off
	global_load_dwordx4 v[8:11], v[28:29], off
	global_load_dwordx4 v[12:15], v[28:29], off offset:1024
	global_load_dwordx4 v[16:19], v[30:31], off offset:1024
	global_load_dwordx4 v[20:23], v[28:29], off offset:2048
	global_load_dwordx4 v[24:27], v[30:31], off offset:2048
	s_nop 0
	global_load_dwordx4 v[28:31], v2, s[8:9]
	global_load_dwordx4 v[32:35], v2, s[10:11]
	global_load_dwordx4 v[36:39], v2, s[8:9] offset:1024
	global_load_dwordx4 v[40:43], v2, s[10:11] offset:1024
	s_load_dwordx4 s[4:7], s[0:1], 0x20
	v_and_b32_e32 v50, 16, v0
	v_cmp_eq_u32_e32 vcc, 0, v50
	v_and_b32_e32 v51, 32, v0
	v_mov_b32_e32 v56, 0x2b8cbccc
	s_waitcnt lgkmcnt(0)
	v_mov_b64_e32 v[0:1], s[4:5]
	v_mad_i64_i32 v[0:1], s[0:1], v54, s12, v[0:1]
	v_cmp_eq_u32_e64 s[0:1], 0, v51
	s_mov_b32 s3, 0xf800000
	s_movk_i32 s2, 0x680
	v_mov_b64_e32 v[44:45], s[6:7]
	v_mov_b32_e32 v57, 0x260
	s_waitcnt vmcnt(8)
	v_pk_add_f32 v[46:47], v[8:9], v[4:5]
	v_pk_add_f32 v[48:49], v[10:11], v[6:7]
	global_load_dwordx4 v[4:7], v2, s[8:9] offset:2048
	global_load_dwordx4 v[8:11], v2, s[10:11] offset:2048
	s_waitcnt vmcnt(8)
	v_pk_add_f32 v[12:13], v[12:13], v[16:17]
	s_waitcnt vmcnt(6)
	v_pk_add_f32 v[16:17], v[20:21], v[24:25]
	v_pk_add_f32 v[14:15], v[14:15], v[18:19]
	v_pk_add_f32 v[18:19], v[22:23], v[26:27]
	v_add_f32_e32 v52, v46, v47
	v_mov_b32_e32 v20, v12
	v_mov_b32_e32 v21, v16
	v_mov_b32_e32 v22, v13
	v_mov_b32_e32 v23, v17
	v_mov_b32_e32 v24, v14
	v_mov_b32_e32 v25, v18
	v_add_f32_e32 v52, v52, v48
	v_pk_add_f32 v[20:21], v[20:21], v[22:23]
	v_mov_b32_e32 v26, v15
	v_mov_b32_e32 v27, v19
	v_add_f32_e32 v22, v52, v49
	v_pk_add_f32 v[20:21], v[20:21], v[24:25]
	v_add_f32_e32 v22, 0, v22
	v_pk_add_f32 v[20:21], v[20:21], v[26:27]
	s_nop 0
	v_add_f32_e32 v20, v22, v20
	v_add_f32_e32 v20, v20, v21
	s_nop 1
	v_add_f32_dpp v20, v20, v20 quad_perm:[1,0,3,2] row_mask:0xf bank_mask:0xf bound_ctrl:1
	s_nop 1
	v_add_f32_dpp v20, v20, v20 quad_perm:[2,3,0,1] row_mask:0xf bank_mask:0xf bound_ctrl:1
	s_nop 1
	v_add_f32_dpp v20, v20, v20 row_half_mirror row_mask:0xf bank_mask:0xf bound_ctrl:1
	s_nop 1
	v_add_f32_dpp v20, v20, v20 row_mirror row_mask:0xf bank_mask:0xf bound_ctrl:1
	v_mov_b32_e32 v21, v20
	v_mov_b32_e32 v22, v20
	s_nop 1
	v_permlane16_swap_b32_e32 v21, v22
	v_cndmask_b32_e32 v21, v21, v22, vcc
	v_add_f32_e32 v20, v20, v21
	v_mov_b32_e32 v21, v20
	v_mov_b32_e32 v22, v20
	s_nop 1
	v_permlane32_swap_b32_e32 v21, v22
	v_cndmask_b32_e64 v21, v21, v22, s[0:1]
	v_add_f32_e32 v20, v20, v21
	v_mul_f32_e32 v20, 0x3aaaaaab, v20
	v_pk_add_f32 v[22:23], v[46:47], v[20:21] op_sel_hi:[1,0] neg_lo:[0,1] neg_hi:[0,1]
	v_pk_add_f32 v[16:17], v[16:17], v[20:21] op_sel_hi:[1,0] neg_lo:[0,1] neg_hi:[0,1]
	v_pk_add_f32 v[24:25], v[48:49], v[20:21] op_sel_hi:[1,0] neg_lo:[0,1] neg_hi:[0,1]
	v_pk_add_f32 v[12:13], v[12:13], v[20:21] op_sel_hi:[1,0] neg_lo:[0,1] neg_hi:[0,1]
	v_mov_b32_e32 v48, v17
	v_mov_b32_e32 v49, v23
	v_pk_add_f32 v[14:15], v[14:15], v[20:21] op_sel_hi:[1,0] neg_lo:[0,1] neg_hi:[0,1]
	v_pk_add_f32 v[18:19], v[18:19], v[20:21] op_sel_hi:[1,0] neg_lo:[0,1] neg_hi:[0,1]
	v_pk_mul_f32 v[20:21], v[12:13], v[12:13]
	v_mov_b32_e32 v46, v16
	v_mov_b32_e32 v47, v22
	v_pk_mul_f32 v[48:49], v[48:49], v[48:49]
	v_pk_mul_f32 v[26:27], v[14:15], v[14:15]
	v_mov_b32_e32 v50, v18
	v_mov_b32_e32 v51, v24
	v_add_f32_e32 v58, v20, v21
	v_pk_fma_f32 v[20:21], v[46:47], v[46:47], v[48:49]
	v_mov_b32_e32 v52, v19
	v_mov_b32_e32 v53, v25
	v_add_f32_e32 v26, v26, v58
	v_pk_fma_f32 v[20:21], v[50:51], v[50:51], v[20:21]
	v_add_f32_e32 v26, v27, v26
	v_pk_fma_f32 v[20:21], v[52:53], v[52:53], v[20:21]
	s_nop 0
	v_add_f32_e32 v21, v21, v26
	v_add_f32_e32 v20, v20, v21
	s_nop 1
	v_add_f32_dpp v20, v20, v20 quad_perm:[1,0,3,2] row_mask:0xf bank_mask:0xf bound_ctrl:1
	s_nop 1
	v_add_f32_dpp v20, v20, v20 quad_perm:[2,3,0,1] row_mask:0xf bank_mask:0xf bound_ctrl:1
	s_nop 1
	v_add_f32_dpp v20, v20, v20 row_half_mirror row_mask:0xf bank_mask:0xf bound_ctrl:1
	s_nop 1
	v_add_f32_dpp v20, v20, v20 row_mirror row_mask:0xf bank_mask:0xf bound_ctrl:1
	v_mov_b32_e32 v21, v20
	v_mov_b32_e32 v26, v20
	s_nop 1
	v_permlane16_swap_b32_e32 v21, v26
	v_cndmask_b32_e32 v21, v21, v26, vcc
	v_add_f32_e32 v20, v20, v21
	v_mov_b32_e32 v21, v20
	v_mov_b32_e32 v26, v20
	s_nop 1
	v_permlane32_swap_b32_e32 v21, v26
	v_cndmask_b32_e64 v21, v21, v26, s[0:1]
	v_add_f32_e32 v20, v20, v21
	v_fmac_f32_e32 v56, 0x3aaaaaab, v20
	v_mul_f32_e32 v20, 0x4f800000, v56
	v_cmp_gt_f32_e32 vcc, s3, v56
	v_lshl_add_u64 v[26:27], v[0:1], 0, v[2:3]
	s_nop 0
	v_cndmask_b32_e32 v46, v56, v20, vcc
	v_sqrt_f32_e32 v47, v46
	v_mad_i64_i32 v[20:21], s[0:1], v54, s2, v[44:45]
	v_add_u32_e32 v0, -1, v47
	v_add_u32_e32 v1, 1, v47
	v_fma_f32 v2, -v0, v47, v46
	v_fma_f32 v44, -v1, v47, v46
	v_cmp_ge_f32_e64 s[0:1], 0, v2
	v_lshlrev_b32_e32 v2, 3, v55
	v_lshl_add_u64 v[20:21], v[20:21], 0, v[2:3]
	v_cndmask_b32_e64 v0, v47, v0, s[0:1]
	v_cmp_lt_f32_e64 s[0:1], 0, v44
	s_nop 1
	v_cndmask_b32_e64 v0, v0, v1, s[0:1]
	v_mul_f32_e32 v1, 0x37800000, v0
	v_cndmask_b32_e32 v0, v0, v1, vcc
	v_cmp_class_f32_e32 vcc, v46, v57
	s_nop 1
	v_cndmask_b32_e32 v0, v0, v46, vcc
	v_div_scale_f32 v1, s[0:1], v0, v0, 1.0
	v_rcp_f32_e32 v44, v1
	s_nop 0
	v_fma_f32 v2, -v1, v44, 1.0
	v_fmac_f32_e32 v44, v2, v44
	v_div_scale_f32 v2, vcc, 1.0, v0, 1.0
	v_mul_f32_e32 v3, v2, v44
	v_fma_f32 v45, -v1, v3, v2
	v_fmac_f32_e32 v3, v45, v44
	v_fma_f32 v1, -v1, v3, v2
	v_div_fmas_f32 v1, v1, v44, v3
	v_div_fixup_f32 v44, v1, v0, 1.0
	v_pk_mul_f32 v[0:1], v[22:23], v[44:45] op_sel_hi:[1,0]
	v_pk_mul_f32 v[2:3], v[24:25], v[44:45] op_sel_hi:[1,0]
	v_pk_mul_f32 v[12:13], v[12:13], v[44:45] op_sel_hi:[1,0]
	v_pk_mul_f32 v[14:15], v[14:15], v[44:45] op_sel_hi:[1,0]
	v_pk_mul_f32 v[16:17], v[16:17], v[44:45] op_sel_hi:[1,0]
	s_waitcnt vmcnt(4)
	v_pk_fma_f32 v[0:1], v[28:29], v[0:1], v[32:33]
	v_pk_fma_f32 v[2:3], v[30:31], v[2:3], v[34:35]
	s_waitcnt vmcnt(2)
	v_pk_fma_f32 v[12:13], v[12:13], v[36:37], v[40:41]
	v_pk_fma_f32 v[14:15], v[14:15], v[38:39], v[42:43]
	s_waitcnt vmcnt(0)
	v_pk_fma_f32 v[4:5], v[16:17], v[4:5], v[8:9]
	v_pk_mul_f32 v[8:9], v[18:19], v[44:45] op_sel_hi:[1,0]
	global_store_dwordx4 v[26:27], v[0:3], off
	v_pk_fma_f32 v[6:7], v[8:9], v[6:7], v[10:11]
	s_nop 0
	v_cvt_pk_f16_f32 v3, v2, v3
	v_cvt_pk_f16_f32 v2, v0, v1
	v_cvt_pk_f16_f32 v1, v14, v15
	v_cvt_pk_f16_f32 v0, v12, v13
	global_store_dwordx2 v[20:21], v[2:3], off
	global_store_dwordx4 v[26:27], v[12:15], off offset:1024
	global_store_dwordx2 v[20:21], v[0:1], off offset:512
	global_store_dwordx4 v[26:27], v[4:7], off offset:2048
	v_cvt_pk_f16_f32 v1, v6, v7
	v_cvt_pk_f16_f32 v0, v4, v5
	global_store_dwordx2 v[20:21], v[0:1], off offset:1024
	s_endpgm

	.amdhsa_kernel _Z4ln_kPKfS0_S0_S0_PfPDF16_
		.amdhsa_group_segment_fixed_size 0
		.amdhsa_private_segment_fixed_size 0
		.amdhsa_kernarg_size 48
		.amdhsa_user_sgpr_count 2
		.amdhsa_user_sgpr_dispatch_ptr 0
		.amdhsa_user_sgpr_queue_ptr 0
		.amdhsa_user_sgpr_kernarg_segment_ptr 1
		.amdhsa_user_sgpr_dispatch_id 0
		.amdhsa_user_sgpr_kernarg_preload_length 0
		.amdhsa_user_sgpr_kernarg_preload_offset 0
		.amdhsa_user_sgpr_private_segment_size 0
		.amdhsa_uses_dynamic_stack 0
		.amdhsa_enable_private_segment 0
		.amdhsa_system_sgpr_workgroup_id_x 1
		.amdhsa_system_sgpr_workgroup_id_y 0
		.amdhsa_system_sgpr_workgroup_id_z 0
		.amdhsa_system_sgpr_workgroup_info 0
		.amdhsa_system_vgpr_workitem_id 0
		.amdhsa_next_free_vgpr 65
		.amdhsa_next_free_sgpr 96
		.amdhsa_accum_offset 68
		.amdhsa_reserve_vcc 1
		.amdhsa_float_round_mode_32 0
		.amdhsa_float_round_mode_16_64 0
		.amdhsa_float_denorm_mode_32 3
		.amdhsa_float_denorm_mode_16_64 3
		.amdhsa_dx10_clamp 1
		.amdhsa_ieee_mode 1
		.amdhsa_fp16_overflow 0
		.amdhsa_tg_split 0
		.amdhsa_exception_fp_ieee_invalid_op 0
		.amdhsa_exception_fp_denorm_src 0
		.amdhsa_exception_fp_ieee_div_zero 0
		.amdhsa_exception_fp_ieee_overflow 0
		.amdhsa_exception_fp_ieee_underflow 0
		.amdhsa_exception_fp_ieee_inexact 0
		.amdhsa_exception_int_div_zero 0
	.end_amdhsa_kernel

_Z11ln_router_kPKfS0_S0_S0_S0_PfPDF16_PiS1_i:
	v_lshlrev_b32_e32 v60, 4, v0
	s_getpc_b64 s[92:93]
	s_add_u32 s92, s92, 0xef8
	s_addc_u32 s93, s93, 0x0
	global_load_dwordx4 v[56:59], v60, s[92:93]
	s_getpc_b64 s[92:93]
	s_add_u32 s92, s92, 0x35e0
	s_addc_u32 s93, s93, 0x0
	global_load_dwordx4 v[56:59], v60, s[92:93]
	s_load_dwordx8 s[16:23], s[0:1], 0x0
	v_lshrrev_b32_e32 v1, 6, v0
	v_and_b32_e32 v16, 63, v0
	v_lshl_or_b32 v14, s2, 4, v1
	s_movk_i32 s4, 0xc00
	s_waitcnt lgkmcnt(0)
	v_mov_b64_e32 v[2:3], s[16:17]
	v_mad_i64_i32 v[2:3], s[2:3], v14, s4, v[2:3]
	v_mov_b32_e32 v19, 0
	v_lshlrev_b32_e32 v18, 4, v16
	v_lshl_add_u64 v[20:21], v[2:3], 0, v[18:19]
	global_load_dwordx4 v[10:13], v[20:21], off
	global_load_dwordx4 v[6:9], v[20:21], off offset:1024
	global_load_dwordx4 v[2:5], v[20:21], off offset:2048
	s_load_dwordx2 s[16:17], s[0:1], 0x40
	s_load_dwordx8 s[8:15], s[0:1], 0x20
	v_lshlrev_b32_e32 v18, 4, v0
	v_mad_i64_i32 v[20:21], s[2:3], v14, s4, 0
	v_lshlrev_b32_e32 v17, 1, v0
	v_lshl_add_u64 v[18:19], s[22:23], 0, v[18:19]
	v_ashrrev_i32_e32 v15, 31, v14
	v_or_b32_e32 v1, 0xfffffc00, v0
	v_and_b32_e32 v17, 0x7fc, v17
	v_lshl_add_u64 v[18:19], v[18:19], 0, 8
	v_lshlrev_b32_e32 v22, 2, v0
	s_mov_b64 s[2:3], 0
	s_movk_i32 s6, 0xc10
	s_mov_b64 s[4:5], 0x4000
	s_movk_i32 s7, 0x1ff

	.amdhsa_kernel _Z11ln_router_kPKfS0_S0_S0_S0_PfPDF16_PiS1_i
		.amdhsa_group_segment_fixed_size 24704
		.amdhsa_private_segment_fixed_size 0
		.amdhsa_kernarg_size 76
		.amdhsa_user_sgpr_count 2
		.amdhsa_user_sgpr_dispatch_ptr 0
		.amdhsa_user_sgpr_queue_ptr 0
		.amdhsa_user_sgpr_kernarg_segment_ptr 1
		.amdhsa_user_sgpr_dispatch_id 0
		.amdhsa_user_sgpr_kernarg_preload_length 0
		.amdhsa_user_sgpr_kernarg_preload_offset 0
		.amdhsa_user_sgpr_private_segment_size 0
		.amdhsa_uses_dynamic_stack 0
		.amdhsa_enable_private_segment 0
		.amdhsa_system_sgpr_workgroup_id_x 1
		.amdhsa_system_sgpr_workgroup_id_y 0
		.amdhsa_system_sgpr_workgroup_id_z 0
		.amdhsa_system_sgpr_workgroup_info 0
		.amdhsa_system_vgpr_workitem_id 0
		.amdhsa_next_free_vgpr 61
		.amdhsa_next_free_sgpr 96
		.amdhsa_accum_offset 64
		.amdhsa_reserve_vcc 1
		.amdhsa_float_round_mode_32 0
		.amdhsa_float_round_mode_16_64 0
		.amdhsa_float_denorm_mode_32 3
		.amdhsa_float_denorm_mode_16_64 3
		.amdhsa_dx10_clamp 1
		.amdhsa_ieee_mode 1
		.amdhsa_fp16_overflow 0
		.amdhsa_tg_split 0
		.amdhsa_exception_fp_ieee_invalid_op 0
		.amdhsa_exception_fp_denorm_src 0
		.amdhsa_exception_fp_ieee_div_zero 0
		.amdhsa_exception_fp_ieee_overflow 0
		.amdhsa_exception_fp_ieee_underflow 0
		.amdhsa_exception_fp_ieee_inexact 0
		.amdhsa_exception_int_div_zero 0
	.end_amdhsa_kernel

_Z6sort_kPKiPiS1_:
	v_lshlrev_b32_e32 v52, 4, v0
	s_getpc_b64 s[92:93]
	s_add_u32 s92, s92, 0xdef8
	s_addc_u32 s93, s93, 0x0
	global_load_dwordx4 v[48:51], v52, s[92:93]
	s_load_dwordx4 s[4:7], s[0:1], 0x0
	s_load_dwordx2 s[8:9], s[0:1], 0x10
	v_lshrrev_b32_e32 v1, 6, v0
	v_and_b32_e32 v2, 63, v0
	v_lshl_or_b32 v3, v1, 8, v2
	v_lshlrev_b32_e32 v12, 2, v3
	s_waitcnt lgkmcnt(0)
	global_load_dword v4, v12, s[4:5]
	global_load_dword v5, v12, s[4:5] offset:256
	global_load_dword v6, v12, s[4:5] offset:512
	global_load_dword v7, v12, s[4:5] offset:768
	v_readfirstlane_b32 s2, v1
	v_mov_b32_e32 v8, 0
	v_lshl_or_b32 v9, v1, 5, v2
	v_lshlrev_b32_e32 v9, 2, v9
	v_lshlrev_b32_e32 v10, 5, v2
	v_mov_b32_e32 v32, 0
	v_mov_b32_e32 v33, 0
	v_mov_b32_e32 v34, 0
	v_mov_b32_e32 v35, 0
	s_waitcnt vmcnt(3)
	v_cmp_eq_u32_e64 s[10:11], 0, v4
	v_cmp_eq_u32_e64 s[12:13], 1, v4
	v_cmp_eq_u32_e64 s[14:15], 2, v4
	v_cmp_eq_u32_e64 s[16:17], 3, v4
	v_cmp_eq_u32_e64 s[18:19], 4, v4
	v_cmp_eq_u32_e64 s[20:21], 5, v4
	v_cmp_eq_u32_e64 s[22:23], 6, v4
	v_cmp_eq_u32_e64 s[24:25], 7, v4
	s_waitcnt vmcnt(2)
	v_cmp_eq_u32_e64 s[26:27], 0, v5
	v_cmp_eq_u32_e64 s[28:29], 1, v5
	v_cmp_eq_u32_e64 s[30:31], 2, v5
	v_cmp_eq_u32_e64 s[32:33], 3, v5
	v_cmp_eq_u32_e64 s[34:35], 4, v5
	v_cmp_eq_u32_e64 s[36:37], 5, v5
	v_cmp_eq_u32_e64 s[38:39], 6, v5
	v_cmp_eq_u32_e64 s[40:41], 7, v5
	s_waitcnt vmcnt(1)
	v_cmp_eq_u32_e64 s[42:43], 0, v6
	v_cmp_eq_u32_e64 s[44:45], 1, v6
	v_cmp_eq_u32_e64 s[46:47], 2, v6
	v_cmp_eq_u32_e64 s[48:49], 3, v6
	v_cmp_eq_u32_e64 s[50:51], 4, v6
	v_cmp_eq_u32_e64 s[52:53], 5, v6
	v_cmp_eq_u32_e64 s[54:55], 6, v6
	v_cmp_eq_u32_e64 s[56:57], 7, v6
	s_waitcnt vmcnt(0)
	v_cmp_eq_u32_e64 s[58:59], 0, v7
	v_cmp_eq_u32_e64 s[60:61], 1, v7
	v_cmp_eq_u32_e64 s[62:63], 2, v7
	v_cmp_eq_u32_e64 s[64:65], 3, v7
	v_cmp_eq_u32_e64 s[66:67], 4, v7
	v_cmp_eq_u32_e64 s[68:69], 5, v7
	v_cmp_eq_u32_e64 s[70:71], 6, v7
	v_cmp_eq_u32_e64 s[72:73], 7, v7
	s_bcnt1_i32_b64 s74, s[10:11]
	v_writelane_b32 v8, s74, 0
	s_bcnt1_i32_b64 s74, s[12:13]
	v_writelane_b32 v8, s74, 1
	s_bcnt1_i32_b64 s74, s[14:15]
	v_writelane_b32 v8, s74, 2
	s_bcnt1_i32_b64 s74, s[16:17]
	v_writelane_b32 v8, s74, 3
	s_bcnt1_i32_b64 s74, s[18:19]
	v_writelane_b32 v8, s74, 4
	s_bcnt1_i32_b64 s74, s[20:21]
	v_writelane_b32 v8, s74, 5
	s_bcnt1_i32_b64 s74, s[22:23]
	v_writelane_b32 v8, s74, 6
	s_bcnt1_i32_b64 s74, s[24:25]
	v_writelane_b32 v8, s74, 7
	s_bcnt1_i32_b64 s74, s[26:27]
	v_writelane_b32 v8, s74, 8
	s_bcnt1_i32_b64 s74, s[28:29]
	v_writelane_b32 v8, s74, 9
	s_bcnt1_i32_b64 s74, s[30:31]
	v_writelane_b32 v8, s74, 10
	s_bcnt1_i32_b64 s74, s[32:33]
	v_writelane_b32 v8, s74, 11
	s_bcnt1_i32_b64 s74, s[34:35]
	v_writelane_b32 v8, s74, 12
	s_bcnt1_i32_b64 s74, s[36:37]
	v_writelane_b32 v8, s74, 13
	s_bcnt1_i32_b64 s74, s[38:39]
	v_writelane_b32 v8, s74, 14
	s_bcnt1_i32_b64 s74, s[40:41]
	v_writelane_b32 v8, s74, 15
	s_bcnt1_i32_b64 s74, s[42:43]
	v_writelane_b32 v8, s74, 16
	s_bcnt1_i32_b64 s74, s[44:45]
	v_writelane_b32 v8, s74, 17
	s_bcnt1_i32_b64 s74, s[46:47]
	v_writelane_b32 v8, s74, 18
	s_bcnt1_i32_b64 s74, s[48:49]
	v_writelane_b32 v8, s74, 19
	s_bcnt1_i32_b64 s74, s[50:51]
	v_writelane_b32 v8, s74, 20
	s_bcnt1_i32_b64 s74, s[52:53]
	v_writelane_b32 v8, s74, 21
	s_bcnt1_i32_b64 s74, s[54:55]
	v_writelane_b32 v8, s74, 22
	s_bcnt1_i32_b64 s74, s[56:57]
	v_writelane_b32 v8, s74, 23
	s_bcnt1_i32_b64 s74, s[58:59]
	v_writelane_b32 v8, s74, 24
	s_bcnt1_i32_b64 s74, s[60:61]
	v_writelane_b32 v8, s74, 25
	s_bcnt1_i32_b64 s74, s[62:63]
	v_writelane_b32 v8, s74, 26
	s_bcnt1_i32_b64 s74, s[64:65]
	v_writelane_b32 v8, s74, 27
	s_bcnt1_i32_b64 s74, s[66:67]
	v_writelane_b32 v8, s74, 28
	s_bcnt1_i32_b64 s74, s[68:69]
	v_writelane_b32 v8, s74, 29
	s_bcnt1_i32_b64 s74, s[70:71]
	v_writelane_b32 v8, s74, 30
	s_bcnt1_i32_b64 s74, s[72:73]
	v_writelane_b32 v8, s74, 31
	s_mov_b32 exec_lo, -1
	s_mov_b32 exec_hi, 0
	ds_write_b32 v9, v8
	s_mov_b64 exec, -1
	s_waitcnt lgkmcnt(0)
	s_barrier
	ds_read_b128 v[16:19], v10
	ds_read_b128 v[20:23], v10 offset:16
	s_mov_b64 exec, s[10:11]
	v_mbcnt_lo_u32_b32 v32, s10, 0
	v_mbcnt_hi_u32_b32 v32, s11, v32
	s_mov_b64 exec, s[12:13]
	v_mbcnt_lo_u32_b32 v32, s12, 0
	v_mbcnt_hi_u32_b32 v32, s13, v32
	s_mov_b64 exec, s[14:15]
	v_mbcnt_lo_u32_b32 v32, s14, 0
	v_mbcnt_hi_u32_b32 v32, s15, v32
	s_mov_b64 exec, s[16:17]
	v_mbcnt_lo_u32_b32 v32, s16, 0
	v_mbcnt_hi_u32_b32 v32, s17, v32
	s_mov_b64 exec, s[18:19]
	v_mbcnt_lo_u32_b32 v32, s18, 0
	v_mbcnt_hi_u32_b32 v32, s19, v32
	s_mov_b64 exec, s[20:21]
	v_mbcnt_lo_u32_b32 v32, s20, 0
	v_mbcnt_hi_u32_b32 v32, s21, v32
	s_mov_b64 exec, s[22:23]
	v_mbcnt_lo_u32_b32 v32, s22, 0
	v_mbcnt_hi_u32_b32 v32, s23, v32
	s_mov_b64 exec, s[24:25]
	v_mbcnt_lo_u32_b32 v32, s24, 0
	v_mbcnt_hi_u32_b32 v32, s25, v32
	s_mov_b64 exec, s[26:27]
	v_mbcnt_lo_u32_b32 v33, s26, 0
	v_mbcnt_hi_u32_b32 v33, s27, v33
	s_mov_b64 exec, s[28:29]
	v_mbcnt_lo_u32_b32 v33, s28, 0
	v_mbcnt_hi_u32_b32 v33, s29, v33
	s_mov_b64 exec, s[30:31]
	v_mbcnt_lo_u32_b32 v33, s30, 0
	v_mbcnt_hi_u32_b32 v33, s31, v33
	s_mov_b64 exec, s[32:33]
	v_mbcnt_lo_u32_b32 v33, s32, 0
	v_mbcnt_hi_u32_b32 v33, s33, v33
	s_mov_b64 exec, s[34:35]
	v_mbcnt_lo_u32_b32 v33, s34, 0
	v_mbcnt_hi_u32_b32 v33, s35, v33
	s_mov_b64 exec, s[36:37]
	v_mbcnt_lo_u32_b32 v33, s36, 0
	v_mbcnt_hi_u32_b32 v33, s37, v33
	s_mov_b64 exec, s[38:39]
	v_mbcnt_lo_u32_b32 v33, s38, 0
	v_mbcnt_hi_u32_b32 v33, s39, v33
	s_mov_b64 exec, s[40:41]
	v_mbcnt_lo_u32_b32 v33, s40, 0
	v_mbcnt_hi_u32_b32 v33, s41, v33
	s_mov_b64 exec, s[42:43]
	v_mbcnt_lo_u32_b32 v34, s42, 0
	v_mbcnt_hi_u32_b32 v34, s43, v34
	s_mov_b64 exec, s[44:45]
	v_mbcnt_lo_u32_b32 v34, s44, 0
	v_mbcnt_hi_u32_b32 v34, s45, v34
	s_mov_b64 exec, s[46:47]
	v_mbcnt_lo_u32_b32 v34, s46, 0
	v_mbcnt_hi_u32_b32 v34, s47, v34
	s_mov_b64 exec, s[48:49]
	v_mbcnt_lo_u32_b32 v34, s48, 0
	v_mbcnt_hi_u32_b32 v34, s49, v34
	s_mov_b64 exec, s[50:51]
	v_mbcnt_lo_u32_b32 v34, s50, 0
	v_mbcnt_hi_u32_b32 v34, s51, v34
	s_mov_b64 exec, s[52:53]
	v_mbcnt_lo_u32_b32 v34, s52, 0
	v_mbcnt_hi_u32_b32 v34, s53, v34
	s_mov_b64 exec, s[54:55]
	v_mbcnt_lo_u32_b32 v34, s54, 0
	v_mbcnt_hi_u32_b32 v34, s55, v34
	s_mov_b64 exec, s[56:57]
	v_mbcnt_lo_u32_b32 v34, s56, 0
	v_mbcnt_hi_u32_b32 v34, s57, v34
	s_mov_b64 exec, s[58:59]
	v_mbcnt_lo_u32_b32 v35, s58, 0
	v_mbcnt_hi_u32_b32 v35, s59, v35
	s_mov_b64 exec, s[60:61]
	v_mbcnt_lo_u32_b32 v35, s60, 0
	v_mbcnt_hi_u32_b32 v35, s61, v35
	s_mov_b64 exec, s[62:63]
	v_mbcnt_lo_u32_b32 v35, s62, 0
	v_mbcnt_hi_u32_b32 v35, s63, v35
	s_mov_b64 exec, s[64:65]
	v_mbcnt_lo_u32_b32 v35, s64, 0
	v_mbcnt_hi_u32_b32 v35, s65, v35
	s_mov_b64 exec, s[66:67]
	v_mbcnt_lo_u32_b32 v35, s66, 0
	v_mbcnt_hi_u32_b32 v35, s67, v35
	s_mov_b64 exec, s[68:69]
	v_mbcnt_lo_u32_b32 v35, s68, 0
	v_mbcnt_hi_u32_b32 v35, s69, v35
	s_mov_b64 exec, s[70:71]
	v_mbcnt_lo_u32_b32 v35, s70, 0
	v_mbcnt_hi_u32_b32 v35, s71, v35
	s_mov_b64 exec, s[72:73]
	v_mbcnt_lo_u32_b32 v35, s72, 0
	v_mbcnt_hi_u32_b32 v35, s73, v35
	s_mov_b64 exec, -1
	s_waitcnt lgkmcnt(0)
	v_mov_b32_e32 v24, v16
	v_mov_b32_e32 v25, v17
	v_mov_b32_e32 v26, v18
	v_mov_b32_e32 v27, v19
	v_mov_b32_e32 v28, v20
	v_mov_b32_e32 v29, v21
	v_mov_b32_e32 v30, v22
	v_mov_b32_e32 v31, v23
	v_add_u32_dpp v16, v16, v16 row_shr:1 row_mask:0xf bank_mask:0xf
	v_add_u32_dpp v17, v17, v17 row_shr:1 row_mask:0xf bank_mask:0xf
	v_add_u32_dpp v18, v18, v18 row_shr:1 row_mask:0xf bank_mask:0xf
	v_add_u32_dpp v19, v19, v19 row_shr:1 row_mask:0xf bank_mask:0xf
	v_add_u32_dpp v20, v20, v20 row_shr:1 row_mask:0xf bank_mask:0xf
	v_add_u32_dpp v21, v21, v21 row_shr:1 row_mask:0xf bank_mask:0xf
	v_add_u32_dpp v22, v22, v22 row_shr:1 row_mask:0xf bank_mask:0xf
	v_add_u32_dpp v23, v23, v23 row_shr:1 row_mask:0xf bank_mask:0xf
	v_add_u32_dpp v16, v16, v16 row_shr:2 row_mask:0xf bank_mask:0xf
	v_add_u32_dpp v17, v17, v17 row_shr:2 row_mask:0xf bank_mask:0xf
	v_add_u32_dpp v18, v18, v18 row_shr:2 row_mask:0xf bank_mask:0xf
	v_add_u32_dpp v19, v19, v19 row_shr:2 row_mask:0xf bank_mask:0xf
	v_add_u32_dpp v20, v20, v20 row_shr:2 row_mask:0xf bank_mask:0xf
	v_add_u32_dpp v21, v21, v21 row_shr:2 row_mask:0xf bank_mask:0xf
	v_add_u32_dpp v22, v22, v22 row_shr:2 row_mask:0xf bank_mask:0xf
	v_add_u32_dpp v23, v23, v23 row_shr:2 row_mask:0xf bank_mask:0xf
	v_add_u32_dpp v16, v16, v16 row_shr:4 row_mask:0xf bank_mask:0xf
	v_add_u32_dpp v17, v17, v17 row_shr:4 row_mask:0xf bank_mask:0xf
	v_add_u32_dpp v18, v18, v18 row_shr:4 row_mask:0xf bank_mask:0xf
	v_add_u32_dpp v19, v19, v19 row_shr:4 row_mask:0xf bank_mask:0xf
	v_add_u32_dpp v20, v20, v20 row_shr:4 row_mask:0xf bank_mask:0xf
	v_add_u32_dpp v21, v21, v21 row_shr:4 row_mask:0xf bank_mask:0xf
	v_add_u32_dpp v22, v22, v22 row_shr:4 row_mask:0xf bank_mask:0xf
	v_add_u32_dpp v23, v23, v23 row_shr:4 row_mask:0xf bank_mask:0xf
	v_add_u32_dpp v16, v16, v16 row_shr:8 row_mask:0xf bank_mask:0xf
	v_add_u32_dpp v17, v17, v17 row_shr:8 row_mask:0xf bank_mask:0xf
	v_add_u32_dpp v18, v18, v18 row_shr:8 row_mask:0xf bank_mask:0xf
	v_add_u32_dpp v19, v19, v19 row_shr:8 row_mask:0xf bank_mask:0xf
	v_add_u32_dpp v20, v20, v20 row_shr:8 row_mask:0xf bank_mask:0xf
	v_add_u32_dpp v21, v21, v21 row_shr:8 row_mask:0xf bank_mask:0xf
	v_add_u32_dpp v22, v22, v22 row_shr:8 row_mask:0xf bank_mask:0xf
	v_add_u32_dpp v23, v23, v23 row_shr:8 row_mask:0xf bank_mask:0xf
	v_add_u32_dpp v16, v16, v16 row_bcast:15 row_mask:0xa bank_mask:0xf
	v_add_u32_dpp v17, v17, v17 row_bcast:15 row_mask:0xa bank_mask:0xf
	v_add_u32_dpp v18, v18, v18 row_bcast:15 row_mask:0xa bank_mask:0xf
	v_add_u32_dpp v19, v19, v19 row_bcast:15 row_mask:0xa bank_mask:0xf
	v_add_u32_dpp v20, v20, v20 row_bcast:15 row_mask:0xa bank_mask:0xf
	v_add_u32_dpp v21, v21, v21 row_bcast:15 row_mask:0xa bank_mask:0xf
	v_add_u32_dpp v22, v22, v22 row_bcast:15 row_mask:0xa bank_mask:0xf
	v_add_u32_dpp v23, v23, v23 row_bcast:15 row_mask:0xa bank_mask:0xf
	v_add_u32_dpp v16, v16, v16 row_bcast:31 row_mask:0xc bank_mask:0xf
	v_add_u32_dpp v17, v17, v17 row_bcast:31 row_mask:0xc bank_mask:0xf
	v_add_u32_dpp v18, v18, v18 row_bcast:31 row_mask:0xc bank_mask:0xf
	v_add_u32_dpp v19, v19, v19 row_bcast:31 row_mask:0xc bank_mask:0xf
	v_add_u32_dpp v20, v20, v20 row_bcast:31 row_mask:0xc bank_mask:0xf
	v_add_u32_dpp v21, v21, v21 row_bcast:31 row_mask:0xc bank_mask:0xf
	v_add_u32_dpp v22, v22, v22 row_bcast:31 row_mask:0xc bank_mask:0xf
	v_add_u32_dpp v23, v23, v23 row_bcast:31 row_mask:0xc bank_mask:0xf
	v_sub_u32_e32 v24, v16, v24
	v_sub_u32_e32 v25, v17, v25
	v_sub_u32_e32 v26, v18, v26
	v_sub_u32_e32 v27, v19, v27
	v_sub_u32_e32 v28, v20, v28
	v_sub_u32_e32 v29, v21, v29
	v_sub_u32_e32 v30, v22, v30
	v_sub_u32_e32 v31, v23, v31
	v_readlane_b32 s80, v16, 63
	v_readlane_b32 s81, v17, 63
	v_readlane_b32 s82, v18, 63
	v_readlane_b32 s83, v19, 63
	v_readlane_b32 s84, v20, 63
	v_readlane_b32 s85, v21, 63
	v_readlane_b32 s86, v22, 63
	v_readlane_b32 s87, v23, 63
	s_mov_b32 s88, 0
	s_add_i32 s89, s88, s80
	s_add_i32 s90, s89, s81
	s_add_i32 s91, s90, s82
	s_add_i32 s92, s91, s83
	s_add_i32 s93, s92, s84
	s_add_i32 s94, s93, s85
	s_add_i32 s95, s94, s86
	s_lshl_b32 s3, s2, 2
	s_add_i32 s75, s3, 0
	v_mov_b32_e32 v36, 0
	v_readlane_b32 s76, v24, s75
	v_readlane_b32 s77, v25, s75
	s_add_i32 s76, s76, s88
	s_mov_b64 exec, s[10:11]
	v_add_u32_e32 v36, s76, v32
	v_readlane_b32 s76, v26, s75
	s_add_i32 s77, s77, s89
	s_mov_b64 exec, s[12:13]
	v_add_u32_e32 v36, s77, v32
	v_readlane_b32 s77, v27, s75
	s_add_i32 s76, s76, s90
	s_mov_b64 exec, s[14:15]
	v_add_u32_e32 v36, s76, v32
	v_readlane_b32 s76, v28, s75
	s_add_i32 s77, s77, s91
	s_mov_b64 exec, s[16:17]
	v_add_u32_e32 v36, s77, v32
	v_readlane_b32 s77, v29, s75
	s_add_i32 s76, s76, s92
	s_mov_b64 exec, s[18:19]
	v_add_u32_e32 v36, s76, v32
	v_readlane_b32 s76, v30, s75
	s_add_i32 s77, s77, s93
	s_mov_b64 exec, s[20:21]
	v_add_u32_e32 v36, s77, v32
	v_readlane_b32 s77, v31, s75
	s_add_i32 s76, s76, s94
	s_mov_b64 exec, s[22:23]
	v_add_u32_e32 v36, s76, v32
	s_add_i32 s77, s77, s95
	s_mov_b64 exec, s[24:25]
	v_add_u32_e32 v36, s77, v32
	s_mov_b64 exec, -1
	s_add_i32 s75, s3, 1
	v_mov_b32_e32 v37, 0
	v_readlane_b32 s76, v24, s75
	v_readlane_b32 s77, v25, s75
	s_add_i32 s76, s76, s88
	s_mov_b64 exec, s[26:27]
	v_add_u32_e32 v37, s76, v33
	v_readlane_b32 s76, v26, s75
	s_add_i32 s77, s77, s89
	s_mov_b64 exec, s[28:29]
	v_add_u32_e32 v37, s77, v33
	v_readlane_b32 s77, v27, s75
	s_add_i32 s76, s76, s90
	s_mov_b64 exec, s[30:31]
	v_add_u32_e32 v37, s76, v33
	v_readlane_b32 s76, v28, s75
	s_add_i32 s77, s77, s91
	s_mov_b64 exec, s[32:33]
	v_add_u32_e32 v37, s77, v33
	v_readlane_b32 s77, v29, s75
	s_add_i32 s76, s76, s92
	s_mov_b64 exec, s[34:35]
	v_add_u32_e32 v37, s76, v33
	v_readlane_b32 s76, v30, s75
	s_add_i32 s77, s77, s93
	s_mov_b64 exec, s[36:37]
	v_add_u32_e32 v37, s77, v33
	v_readlane_b32 s77, v31, s75
	s_add_i32 s76, s76, s94
	s_mov_b64 exec, s[38:39]
	v_add_u32_e32 v37, s76, v33
	s_add_i32 s77, s77, s95
	s_mov_b64 exec, s[40:41]
	v_add_u32_e32 v37, s77, v33
	s_mov_b64 exec, -1
	s_add_i32 s75, s3, 2
	v_mov_b32_e32 v38, 0
	v_readlane_b32 s76, v24, s75
	v_readlane_b32 s77, v25, s75
	s_add_i32 s76, s76, s88
	s_mov_b64 exec, s[42:43]
	v_add_u32_e32 v38, s76, v34
	v_readlane_b32 s76, v26, s75
	s_add_i32 s77, s77, s89
	s_mov_b64 exec, s[44:45]
	v_add_u32_e32 v38, s77, v34
	v_readlane_b32 s77, v27, s75
	s_add_i32 s76, s76, s90
	s_mov_b64 exec, s[46:47]
	v_add_u32_e32 v38, s76, v34
	v_readlane_b32 s76, v28, s75
	s_add_i32 s77, s77, s91
	s_mov_b64 exec, s[48:49]
	v_add_u32_e32 v38, s77, v34
	v_readlane_b32 s77, v29, s75
	s_add_i32 s76, s76, s92
	s_mov_b64 exec, s[50:51]
	v_add_u32_e32 v38, s76, v34
	v_readlane_b32 s76, v30, s75
	s_add_i32 s77, s77, s93
	s_mov_b64 exec, s[52:53]
	v_add_u32_e32 v38, s77, v34
	v_readlane_b32 s77, v31, s75
	s_add_i32 s76, s76, s94
	s_mov_b64 exec, s[54:55]
	v_add_u32_e32 v38, s76, v34
	s_add_i32 s77, s77, s95
	s_mov_b64 exec, s[56:57]
	v_add_u32_e32 v38, s77, v34
	s_mov_b64 exec, -1
	s_add_i32 s75, s3, 3
	v_mov_b32_e32 v39, 0
	v_readlane_b32 s76, v24, s75
	v_readlane_b32 s77, v25, s75
	s_add_i32 s76, s76, s88
	s_mov_b64 exec, s[58:59]
	v_add_u32_e32 v39, s76, v35
	v_readlane_b32 s76, v26, s75
	s_add_i32 s77, s77, s89
	s_mov_b64 exec, s[60:61]
	v_add_u32_e32 v39, s77, v35
	v_readlane_b32 s77, v27, s75
	s_add_i32 s76, s76, s90
	s_mov_b64 exec, s[62:63]
	v_add_u32_e32 v39, s76, v35
	v_readlane_b32 s76, v28, s75
	s_add_i32 s77, s77, s91
	s_mov_b64 exec, s[64:65]
	v_add_u32_e32 v39, s77, v35
	v_readlane_b32 s77, v29, s75
	s_add_i32 s76, s76, s92
	s_mov_b64 exec, s[66:67]
	v_add_u32_e32 v39, s76, v35
	v_readlane_b32 s76, v30, s75
	s_add_i32 s77, s77, s93
	s_mov_b64 exec, s[68:69]
	v_add_u32_e32 v39, s77, v35
	v_readlane_b32 s77, v31, s75
	s_add_i32 s76, s76, s94
	s_mov_b64 exec, s[70:71]
	v_add_u32_e32 v39, s76, v35
	s_add_i32 s77, s77, s95
	s_mov_b64 exec, s[72:73]
	v_add_u32_e32 v39, s77, v35
	s_mov_b64 exec, -1
	v_lshlrev_b32_e32 v13, 2, v36
	global_store_dword v13, v3, s[6:7]
	v_lshlrev_b32_e32 v13, 2, v37
	v_add_u32_e32 v14, 64, v3
	global_store_dword v13, v14, s[6:7]
	v_lshlrev_b32_e32 v13, 2, v38
	v_add_u32_e32 v14, 128, v3
	global_store_dword v13, v14, s[6:7]
	v_lshlrev_b32_e32 v13, 2, v39
	v_add_u32_e32 v14, 192, v3
	global_store_dword v13, v14, s[6:7]
	s_cmp_lg_u32 s2, 0
	s_cbranch_scc1 .Lsort_end
	v_mov_b32_e32 v40, -1
	v_mov_b32_e32 v41, 0
	v_mov_b32_e32 v42, 0
	v_mov_b32_e32 v43, 0
	s_mov_b32 s75, 0
	s_add_i32 s76, s80, 0x7f
	s_lshr_b32 s76, s76, 7
	s_add_i32 s77, s75, s76
	s_add_i32 s78, s88, s80
	v_cmp_le_u32_e64 s[10:11], s75, v2
	v_cmp_gt_u32_e64 s[12:13], s77, v2
	v_subrev_u32_e32 v44, s75, v2
	v_lshl_add_u32 v44, v44, 7, s88
	v_add_u32_e32 v45, 0x80, v44
	v_min_i32_e32 v45, s78, v45
	s_and_b64 s[14:15], s[10:11], s[12:13]
	s_mov_b32 s75, s77
	v_cndmask_b32_e64 v40, v40, 0, s[14:15]
	v_cndmask_b32_e64 v41, v41, v44, s[14:15]
	v_cndmask_b32_e64 v42, v42, v45, s[14:15]
	s_add_i32 s76, s81, 0x7f
	s_lshr_b32 s76, s76, 7
	s_add_i32 s77, s75, s76
	s_add_i32 s78, s89, s81
	v_cmp_le_u32_e64 s[10:11], s75, v2
	v_cmp_gt_u32_e64 s[12:13], s77, v2
	v_subrev_u32_e32 v44, s75, v2
	v_lshl_add_u32 v44, v44, 7, s89
	v_add_u32_e32 v45, 0x80, v44
	v_min_i32_e32 v45, s78, v45
	s_and_b64 s[14:15], s[10:11], s[12:13]
	s_mov_b32 s75, s77
	v_cndmask_b32_e64 v40, v40, 1, s[14:15]
	v_cndmask_b32_e64 v41, v41, v44, s[14:15]
	v_cndmask_b32_e64 v42, v42, v45, s[14:15]
	s_add_i32 s76, s82, 0x7f
	s_lshr_b32 s76, s76, 7
	s_add_i32 s77, s75, s76
	s_add_i32 s78, s90, s82
	v_cmp_le_u32_e64 s[10:11], s75, v2
	v_cmp_gt_u32_e64 s[12:13], s77, v2
	v_subrev_u32_e32 v44, s75, v2
	v_lshl_add_u32 v44, v44, 7, s90
	v_add_u32_e32 v45, 0x80, v44
	v_min_i32_e32 v45, s78, v45
	s_and_b64 s[14:15], s[10:11], s[12:13]
	s_mov_b32 s75, s77
	v_cndmask_b32_e64 v40, v40, 2, s[14:15]
	v_cndmask_b32_e64 v41, v41, v44, s[14:15]
	v_cndmask_b32_e64 v42, v42, v45, s[14:15]
	s_add_i32 s76, s83, 0x7f
	s_lshr_b32 s76, s76, 7
	s_add_i32 s77, s75, s76
	s_add_i32 s78, s91, s83
	v_cmp_le_u32_e64 s[10:11], s75, v2
	v_cmp_gt_u32_e64 s[12:13], s77, v2
	v_subrev_u32_e32 v44, s75, v2
	v_lshl_add_u32 v44, v44, 7, s91
	v_add_u32_e32 v45, 0x80, v44
	v_min_i32_e32 v45, s78, v45
	s_and_b64 s[14:15], s[10:11], s[12:13]
	s_mov_b32 s75, s77
	v_cndmask_b32_e64 v40, v40, 3, s[14:15]
	v_cndmask_b32_e64 v41, v41, v44, s[14:15]
	v_cndmask_b32_e64 v42, v42, v45, s[14:15]
	s_add_i32 s76, s84, 0x7f
	s_lshr_b32 s76, s76, 7
	s_add_i32 s77, s75, s76
	s_add_i32 s78, s92, s84
	v_cmp_le_u32_e64 s[10:11], s75, v2
	v_cmp_gt_u32_e64 s[12:13], s77, v2
	v_subrev_u32_e32 v44, s75, v2
	v_lshl_add_u32 v44, v44, 7, s92
	v_add_u32_e32 v45, 0x80, v44
	v_min_i32_e32 v45, s78, v45
	s_and_b64 s[14:15], s[10:11], s[12:13]
	s_mov_b32 s75, s77
	v_cndmask_b32_e64 v40, v40, 4, s[14:15]
	v_cndmask_b32_e64 v41, v41, v44, s[14:15]
	v_cndmask_b32_e64 v42, v42, v45, s[14:15]
	s_add_i32 s76, s85, 0x7f
	s_lshr_b32 s76, s76, 7
	s_add_i32 s77, s75, s76
	s_add_i32 s78, s93, s85
	v_cmp_le_u32_e64 s[10:11], s75, v2
	v_cmp_gt_u32_e64 s[12:13], s77, v2
	v_subrev_u32_e32 v44, s75, v2
	v_lshl_add_u32 v44, v44, 7, s93
	v_add_u32_e32 v45, 0x80, v44
	v_min_i32_e32 v45, s78, v45
	s_and_b64 s[14:15], s[10:11], s[12:13]
	s_mov_b32 s75, s77
	v_cndmask_b32_e64 v40, v40, 5, s[14:15]
	v_cndmask_b32_e64 v41, v41, v44, s[14:15]
	v_cndmask_b32_e64 v42, v42, v45, s[14:15]
	s_add_i32 s76, s86, 0x7f
	s_lshr_b32 s76, s76, 7
	s_add_i32 s77, s75, s76
	s_add_i32 s78, s94, s86
	v_cmp_le_u32_e64 s[10:11], s75, v2
	v_cmp_gt_u32_e64 s[12:13], s77, v2
	v_subrev_u32_e32 v44, s75, v2
	v_lshl_add_u32 v44, v44, 7, s94
	v_add_u32_e32 v45, 0x80, v44
	v_min_i32_e32 v45, s78, v45
	s_and_b64 s[14:15], s[10:11], s[12:13]
	s_mov_b32 s75, s77
	v_cndmask_b32_e64 v40, v40, 6, s[14:15]
	v_cndmask_b32_e64 v41, v41, v44, s[14:15]
	v_cndmask_b32_e64 v42, v42, v45, s[14:15]
	s_add_i32 s76, s87, 0x7f
	s_lshr_b32 s76, s76, 7
	s_add_i32 s77, s75, s76
	s_add_i32 s78, s95, s87
	v_cmp_le_u32_e64 s[10:11], s75, v2
	v_cmp_gt_u32_e64 s[12:13], s77, v2
	v_subrev_u32_e32 v44, s75, v2
	v_lshl_add_u32 v44, v44, 7, s95
	v_add_u32_e32 v45, 0x80, v44
	v_min_i32_e32 v45, s78, v45
	s_and_b64 s[14:15], s[10:11], s[12:13]
	s_mov_b32 s75, s77
	v_cndmask_b32_e64 v40, v40, 7, s[14:15]
	v_cndmask_b32_e64 v41, v41, v44, s[14:15]
	v_cndmask_b32_e64 v42, v42, v45, s[14:15]
	v_lshlrev_b32_e32 v46, 4, v2
	v_mov_b32_e32 v47, s75
	v_cmp_gt_u32_e32 vcc, 40, v2
	s_and_b64 exec, exec, vcc
	global_store_dwordx4 v46, v[40:43], s[8:9]
	v_cmp_eq_u32_e32 vcc, 0, v2
	s_and_b64 exec, exec, vcc
	global_store_dword v46, v47, s[8:9] offset:640

	.amdhsa_kernel _Z6sort_kPKiPiS1_
		.amdhsa_group_segment_fixed_size 4176
		.amdhsa_private_segment_fixed_size 0
		.amdhsa_kernarg_size 24
		.amdhsa_user_sgpr_count 2
		.amdhsa_user_sgpr_dispatch_ptr 0
		.amdhsa_user_sgpr_queue_ptr 0
		.amdhsa_user_sgpr_kernarg_segment_ptr 1
		.amdhsa_user_sgpr_dispatch_id 0
		.amdhsa_user_sgpr_kernarg_preload_length 0
		.amdhsa_user_sgpr_kernarg_preload_offset 0
		.amdhsa_user_sgpr_private_segment_size 0
		.amdhsa_uses_dynamic_stack 0
		.amdhsa_enable_private_segment 0
		.amdhsa_system_sgpr_workgroup_id_x 1
		.amdhsa_system_sgpr_workgroup_id_y 0
		.amdhsa_system_sgpr_workgroup_id_z 0
		.amdhsa_system_sgpr_workgroup_info 0
		.amdhsa_system_vgpr_workitem_id 0
		.amdhsa_next_free_vgpr 53
		.amdhsa_next_free_sgpr 96
		.amdhsa_accum_offset 56
		.amdhsa_reserve_vcc 1
		.amdhsa_float_round_mode_32 0
		.amdhsa_float_round_mode_16_64 0
		.amdhsa_float_denorm_mode_32 3
		.amdhsa_float_denorm_mode_16_64 3
		.amdhsa_dx10_clamp 1
		.amdhsa_ieee_mode 1
		.amdhsa_fp16_overflow 0
		.amdhsa_tg_split 0
		.amdhsa_exception_fp_ieee_invalid_op 0
		.amdhsa_exception_fp_denorm_src 0
		.amdhsa_exception_fp_ieee_div_zero 0
		.amdhsa_exception_fp_ieee_overflow 0
		.amdhsa_exception_fp_ieee_underflow 0
		.amdhsa_exception_fp_ieee_inexact 0
		.amdhsa_exception_int_div_zero 0
	.end_amdhsa_kernel

_Z5pre_k7CvtArgsPKiS1_PKfS3_S3_S3_S3_PfPDF16_S4_:
	v_lshlrev_b32_e32 v72, 4, v0
	s_getpc_b64 s[92:93]
	s_add_u32 s92, s92, 0x7ff8
	s_addc_u32 s93, s93, 0x0
	global_load_dwordx4 v[68:71], v72, s[92:93]
	v_add_u32_e32 v72, 0x1000, v72
	global_load_dwordx4 v[68:71], v72, s[92:93]
	v_add_u32_e32 v72, 0x1000, v72
	global_load_dwordx4 v[68:71], v72, s[92:93]
	v_add_u32_e32 v72, 0x1000, v72
	global_load_dwordx4 v[68:71], v72, s[92:93]
	v_lshlrev_b32_e32 v72, 4, v0
	s_cmpk_gt_u32 s2, 0x3ff
	s_mov_b64 s[4:5], -1
	s_cbranch_scc0 .LBB4_8
	s_add_i32 s10, s2, 0xfffffc00
	s_cmpk_gt_i32 s10, 0x47f
	s_cbranch_scc0 .LBB4_5
	s_cmpk_gt_u32 s10, 0x6bf
	s_cbranch_scc0 .LBB4_12
	s_add_i32 s3, s2, 0xfffff540
	s_mul_hi_u32 s4, s3, 0x38e38e39
	s_lshr_b32 s4, s4, 7
	s_add_i32 s8, s4, 9
	s_mulk_i32 s4, 0x240
	s_sub_i32 s9, s3, s4
	s_cbranch_execz .LBB4_13

	.amdhsa_kernel _Z5pre_k7CvtArgsPKiS1_PKfS3_S3_S3_S3_PfPDF16_S4_
		.amdhsa_group_segment_fixed_size 16640
		.amdhsa_private_segment_fixed_size 0
		.amdhsa_kernarg_size 352
		.amdhsa_user_sgpr_count 2
		.amdhsa_user_sgpr_dispatch_ptr 0
		.amdhsa_user_sgpr_queue_ptr 0
		.amdhsa_user_sgpr_kernarg_segment_ptr 1
		.amdhsa_user_sgpr_dispatch_id 0
		.amdhsa_user_sgpr_kernarg_preload_length 0
		.amdhsa_user_sgpr_kernarg_preload_offset 0
		.amdhsa_user_sgpr_private_segment_size 0
		.amdhsa_uses_dynamic_stack 0
		.amdhsa_enable_private_segment 0
		.amdhsa_system_sgpr_workgroup_id_x 1
		.amdhsa_system_sgpr_workgroup_id_y 0
		.amdhsa_system_sgpr_workgroup_id_z 0
		.amdhsa_system_sgpr_workgroup_info 0
		.amdhsa_system_vgpr_workitem_id 0
		.amdhsa_next_free_vgpr 73
		.amdhsa_next_free_sgpr 96
		.amdhsa_accum_offset 76
		.amdhsa_reserve_vcc 1
		.amdhsa_float_round_mode_32 0
		.amdhsa_float_round_mode_16_64 0
		.amdhsa_float_denorm_mode_32 3
		.amdhsa_float_denorm_mode_16_64 3
		.amdhsa_dx10_clamp 1
		.amdhsa_ieee_mode 1
		.amdhsa_fp16_overflow 0
		.amdhsa_tg_split 0
		.amdhsa_exception_fp_ieee_invalid_op 0
		.amdhsa_exception_fp_denorm_src 0
		.amdhsa_exception_fp_ieee_div_zero 0
		.amdhsa_exception_fp_ieee_overflow 0
		.amdhsa_exception_fp_ieee_underflow 0
		.amdhsa_exception_fp_ieee_inexact 0
		.amdhsa_exception_int_div_zero 0
	.end_amdhsa_kernel

_Z6attn_kPKDF16_S0_S0_PKfPDF16_PK15HIP_vector_typeIfLj4EEiPf:
	v_lshlrev_b32_e32 v176, 4, v0
	s_getpc_b64 s[92:93]
	s_add_u32 s92, s92, 0xacf8
	s_addc_u32 s93, s93, 0x0
	global_load_dwordx4 v[172:175], v176, s[92:93]
	s_cmpk_lt_u32 s2, 0xc0
	s_mov_b64 s[4:5], -1
	s_cbranch_scc0 .LBB5_6
	s_load_dwordx8 s[4:11], s[0:1], 0x0
	s_and_b32 s3, s2, 7
	s_mul_i32 s3, s3, 12
	s_lshr_b32 s12, s2, 4
	s_add_i32 s3, s3, s12
	s_mul_i32 s12, s3, 0xab
	s_bfe_u32 s12, s12, 0x5000b
	s_lshl_b32 s13, s3, 16
	s_waitcnt lgkmcnt(0)
	s_add_u32 s6, s6, s13
	s_addc_u32 s7, s7, 0
	v_lshlrev_b32_e32 v2, 4, v0
	v_mov_b32_e32 v3, 0
	v_lshl_add_u64 v[28:29], s[6:7], 0, v[2:3]
	s_movk_i32 s14, 0x2000
	v_add_co_u32_e32 v12, vcc, s14, v28
	s_movk_i32 s15, 0x6000
	s_nop 0
	v_addc_co_u32_e32 v13, vcc, 0, v29, vcc
	v_add_co_u32_e32 v20, vcc, s15, v28
	s_mov_b32 s16, 0xa000
	s_nop 0
	v_addc_co_u32_e32 v21, vcc, 0, v29, vcc
	v_add_co_u32_e32 v30, vcc, s16, v28
	s_add_u32 s8, s8, s13
	s_nop 0
	v_addc_co_u32_e32 v31, vcc, 0, v29, vcc
	s_mov_b32 s17, 0xe000
	s_addc_u32 s9, s9, 0
	v_add_co_u32_e32 v28, vcc, s17, v28
	v_lshl_add_u64 v[48:49], s[8:9], 0, v[2:3]
	s_nop 0
	v_addc_co_u32_e32 v29, vcc, 0, v29, vcc
	v_add_co_u32_e32 v50, vcc, s14, v48
	v_or_b32_e32 v1, 0x4000, v2
	s_nop 0
	v_addc_co_u32_e32 v51, vcc, 0, v49, vcc
	global_load_dwordx4 v[4:7], v[12:13], off
	global_load_dwordx4 v[8:11], v1, s[6:7]
	v_or_b32_e32 v54, 0x8000, v2
	global_load_dwordx4 v[12:15], v[20:21], off
	global_load_dwordx4 v[16:19], v54, s[6:7]
	v_or_b32_e32 v55, 0xc000, v2
	global_load_dwordx4 v[20:23], v[30:31], off
	global_load_dwordx4 v[24:27], v55, s[6:7]
	v_add_co_u32_e32 v52, vcc, s15, v48
	global_load_dwordx4 v[28:31], v[28:29], off
	s_nop 0
	global_load_dwordx4 v[32:35], v2, s[6:7]
	global_load_dwordx4 v[36:39], v2, s[8:9]
	v_addc_co_u32_e32 v53, vcc, 0, v49, vcc
	global_load_dwordx4 v[40:43], v1, s[8:9]
	global_load_dwordx4 v[44:47], v[50:51], off
	global_load_dwordx4 v[66:69], v[52:53], off
	global_load_dwordx4 v[70:73], v54, s[8:9]
	v_add_co_u32_e32 v50, vcc, s16, v48
	s_add_u32 s4, s4, s13
	s_nop 0
	v_addc_co_u32_e32 v51, vcc, 0, v49, vcc
	s_addc_u32 s5, s5, 0
	global_load_dwordx4 v[74:77], v[50:51], off
	global_load_dwordx4 v[78:81], v55, s[8:9]
	s_lshl_b32 s8, s12, 9
	v_add_co_u32_e32 v48, vcc, s17, v48
	v_or_b32_e32 v1, s8, v0
	s_nop 0
	v_addc_co_u32_e32 v49, vcc, 0, v49, vcc
	v_lshlrev_b32_e32 v1, 2, v1
	global_load_dwordx4 v[84:87], v[48:49], off
	v_and_b32_e32 v49, 63, v0
	global_load_dword v48, v1, s[10:11]
	v_lshrrev_b32_e32 v1, 6, v0
	v_and_or_b32 v1, s2, 8, v1
	v_lshlrev_b32_e32 v83, 4, v49
	v_lshl_or_b32 v49, v1, 12, v83
	global_load_dwordx4 v[50:53], v49, s[4:5]
	global_load_dwordx4 v[54:57], v49, s[4:5] offset:1024
	global_load_dwordx4 v[58:61], v49, s[4:5] offset:2048
	global_load_dwordx4 v[62:65], v49, s[4:5] offset:3072
	s_load_dwordx2 s[6:7], s[0:1], 0x20
	v_bfe_u32 v82, v0, 5, 1
	s_mov_b32 s9, 16
	s_mov_b32 s10, 0x41000000
	s_waitcnt vmcnt(13)
	ds_write_b128 v2, v[32:35]
	ds_write_b128 v2, v[4:7] offset:8192
	ds_write_b128 v2, v[8:11] offset:16384
	ds_write_b128 v2, v[12:15] offset:24576
	ds_write_b128 v2, v[16:19] offset:32768
	ds_write_b128 v2, v[20:23] offset:40960
	ds_write_b128 v2, v[24:27] offset:49152
	ds_write_b128 v2, v[28:31] offset:57344
	v_or_b32_e32 v4, 0x10000, v2
	s_waitcnt vmcnt(12)
	ds_write_b128 v4, v[36:39]
	v_or_b32_e32 v4, 0x12000, v2
	s_waitcnt vmcnt(10)
	ds_write_b128 v4, v[44:47]
	v_or_b32_e32 v4, 0x14000, v2
	ds_write_b128 v4, v[40:43]
	v_or_b32_e32 v4, 0x16000, v2
	s_waitcnt vmcnt(9)
	ds_write_b128 v4, v[66:69]
	v_or_b32_e32 v4, 0x18000, v2
	s_waitcnt vmcnt(8)
	ds_write_b128 v4, v[70:73]
	v_or_b32_e32 v4, 0x1a000, v2
	s_waitcnt vmcnt(7)
	ds_write_b128 v4, v[74:77]
	v_or_b32_e32 v4, 0x1c000, v2
	v_or_b32_e32 v2, 0x1e000, v2
	v_mov_b32_e32 v16, v3
	v_mov_b32_e32 v17, v3
	s_waitcnt vmcnt(6)
	ds_write_b128 v4, v[78:81]
	v_mov_b32_e32 v4, v3
	v_mov_b32_e32 v5, v3
	s_waitcnt vmcnt(5)
	ds_write_b128 v2, v[84:87]
	v_mov_b32_e32 v2, 0x20000
	v_lshl_or_b32 v2, v0, 2, v2
	s_waitcnt vmcnt(4)
	ds_write_b32 v2, v48
	v_and_b32_e32 v2, 32, v0
	v_cmp_eq_u32_e32 vcc, 0, v2
	v_mov_b32_e32 v2, v3
	v_mov_b32_e32 v6, v3
	v_mov_b32_e32 v7, v3
	v_mov_b32_e32 v8, v3
	v_mov_b32_e32 v9, v3
	v_mov_b32_e32 v10, v3
	v_mov_b32_e32 v11, v3
	v_mov_b32_e32 v12, v3
	v_mov_b32_e32 v13, v3
	v_mov_b32_e32 v14, v3
	v_mov_b32_e32 v15, v3
	v_mov_b64_e32 v[32:33], v[16:17]
	v_lshlrev_b32_e32 v84, 4, v82
	v_mov_b32_e32 v86, 0xf149f2ca
	v_mov_b64_e32 v[30:31], v[14:15]
	v_mov_b64_e32 v[28:29], v[12:13]
	v_mov_b64_e32 v[26:27], v[10:11]
	v_mov_b64_e32 v[24:25], v[8:9]
	v_mov_b64_e32 v[22:23], v[6:7]
	v_mov_b64_e32 v[20:21], v[4:5]
	v_mov_b64_e32 v[18:19], v[2:3]
	v_mov_b32_e32 v85, v3
	s_waitcnt lgkmcnt(0)
	s_barrier
	s_branch .LBB5_3

	.amdhsa_kernel _Z6attn_kPKDF16_S0_S0_PKfPDF16_PK15HIP_vector_typeIfLj4EEiPf
		.amdhsa_group_segment_fixed_size 133120
		.amdhsa_private_segment_fixed_size 0
		.amdhsa_kernarg_size 64
		.amdhsa_user_sgpr_count 2
		.amdhsa_user_sgpr_dispatch_ptr 0
		.amdhsa_user_sgpr_queue_ptr 0
		.amdhsa_user_sgpr_kernarg_segment_ptr 1
		.amdhsa_user_sgpr_dispatch_id 0
		.amdhsa_user_sgpr_kernarg_preload_length 0
		.amdhsa_user_sgpr_kernarg_preload_offset 0
		.amdhsa_user_sgpr_private_segment_size 0
		.amdhsa_uses_dynamic_stack 0
		.amdhsa_enable_private_segment 0
		.amdhsa_system_sgpr_workgroup_id_x 1
		.amdhsa_system_sgpr_workgroup_id_y 0
		.amdhsa_system_sgpr_workgroup_id_z 0
		.amdhsa_system_sgpr_workgroup_info 0
		.amdhsa_system_vgpr_workitem_id 0
		.amdhsa_next_free_vgpr 177
		.amdhsa_next_free_sgpr 96
		.amdhsa_accum_offset 180
		.amdhsa_reserve_vcc 1
		.amdhsa_float_round_mode_32 0
		.amdhsa_float_round_mode_16_64 0
		.amdhsa_float_denorm_mode_32 3
		.amdhsa_float_denorm_mode_16_64 3
		.amdhsa_dx10_clamp 1
		.amdhsa_ieee_mode 1
		.amdhsa_fp16_overflow 0
		.amdhsa_tg_split 0
		.amdhsa_exception_fp_ieee_invalid_op 0
		.amdhsa_exception_fp_denorm_src 0
		.amdhsa_exception_fp_ieee_div_zero 0
		.amdhsa_exception_fp_ieee_overflow 0
		.amdhsa_exception_fp_ieee_underflow 0
		.amdhsa_exception_fp_ieee_inexact 0
		.amdhsa_exception_int_div_zero 0
	.end_amdhsa_kernel

_Z9tail_up_kPKfPKiS0_S0_PfS0_S2_S3_PK15HIP_vector_typeIfLj4EEiS7_iS3_:
	v_lshlrev_b32_e32 v116, 4, v0
	s_getpc_b64 s[92:93]
	s_add_u32 s92, s92, 0xfff8
	s_addc_u32 s93, s93, 0x0
	global_load_dwordx4 v[112:115], v116, s[92:93]
	s_load_dwordx2 s[6:7], s[0:1], 0x60
	s_load_dwordx2 s[8:9], s[0:1], 0x50
	s_load_dwordx2 s[14:15], s[0:1], 0x40
	s_load_dwordx8 s[44:51], s[0:1], 0x0
	s_load_dwordx8 s[36:43], s[0:1], 0x20
	s_mov_b64 s[12:13], -1
	s_mov_b64 s[4:5], 0
	s_cmp_lt_i32 s3, 9
	s_mov_b64 s[10:11], 0
	s_cbranch_scc0 .LBB6_5
	s_and_b64 vcc, exec, s[12:13]
	s_cbranch_vccnz .LBB6_30

	.amdhsa_kernel _Z9tail_up_kPKfPKiS0_S0_PfS0_S2_S3_PK15HIP_vector_typeIfLj4EEiS7_iS3_
		.amdhsa_group_segment_fixed_size 7168
		.amdhsa_private_segment_fixed_size 0
		.amdhsa_kernarg_size 104
		.amdhsa_user_sgpr_count 2
		.amdhsa_user_sgpr_dispatch_ptr 0
		.amdhsa_user_sgpr_queue_ptr 0
		.amdhsa_user_sgpr_kernarg_segment_ptr 1
		.amdhsa_user_sgpr_dispatch_id 0
		.amdhsa_user_sgpr_kernarg_preload_length 0
		.amdhsa_user_sgpr_kernarg_preload_offset 0
		.amdhsa_user_sgpr_private_segment_size 0
		.amdhsa_uses_dynamic_stack 0
		.amdhsa_enable_private_segment 0
		.amdhsa_system_sgpr_workgroup_id_x 1
		.amdhsa_system_sgpr_workgroup_id_y 1
		.amdhsa_system_sgpr_workgroup_id_z 0
		.amdhsa_system_sgpr_workgroup_info 0
		.amdhsa_system_vgpr_workitem_id 0
		.amdhsa_next_free_vgpr 117
		.amdhsa_next_free_sgpr 96
		.amdhsa_accum_offset 120
		.amdhsa_reserve_vcc 1
		.amdhsa_float_round_mode_32 0
		.amdhsa_float_round_mode_16_64 0
		.amdhsa_float_denorm_mode_32 3
		.amdhsa_float_denorm_mode_16_64 3
		.amdhsa_dx10_clamp 1
		.amdhsa_ieee_mode 1
		.amdhsa_fp16_overflow 0
		.amdhsa_tg_split 0
		.amdhsa_exception_fp_ieee_invalid_op 0
		.amdhsa_exception_fp_denorm_src 0
		.amdhsa_exception_fp_ieee_div_zero 0
		.amdhsa_exception_fp_ieee_overflow 0
		.amdhsa_exception_fp_ieee_underflow 0
		.amdhsa_exception_fp_ieee_inexact 0
		.amdhsa_exception_int_div_zero 0
	.end_amdhsa_kernel

_Z6pool_kPKfS0_S0_S0_S0_S0_PfS1_:
	v_lshlrev_b32_e32 v224, 4, v0
	s_getpc_b64 s[92:93]
	s_add_u32 s92, s92, 0x17f8
	s_addc_u32 s93, s93, 0x0
	global_load_dwordx4 v[220:223], v224, s[92:93]
	s_load_dwordx2 s[12:13], s[0:1], 0x18
	s_load_dwordx2 s[8:9], s[0:1], 0x28
	s_load_dwordx2 s[10:11], s[0:1], 0x38
	s_movk_i32 s4, 0x300
	v_cmp_gt_u32_e32 vcc, s4, v0
	s_mul_i32 s20, s3, 0x60
	s_and_saveexec_b64 s[14:15], vcc
	s_cbranch_execz .LBB8_3
	s_load_dwordx4 s[4:7], s[0:1], 0x0
	s_load_dwordx2 s[16:17], s[0:1], 0x10
	s_mov_b64 s[18:19], 0
	s_mov_b32 s21, 0xaaab
	v_mov_b32_e32 v3, 0
	s_movk_i32 s22, 0x6000
	s_mov_b32 s23, 0xc000
	s_mov_b32 s24, 0x12000
	s_mov_b32 s25, 0x18000
	s_mov_b32 s26, 0x1e000
	s_mov_b32 s27, 0x24000
	s_mov_b32 s28, 0x2a000
	s_mov_b32 s29, 0x30000
	s_mov_b32 s30, 0x36000
	s_mov_b32 s31, 0x3c000
	s_mov_b32 s33, 0x42000
	s_mov_b32 s34, 0x48000
	s_mov_b32 s35, 0x4e000
	s_mov_b32 s36, 0x54000
	s_mov_b32 s37, 0x5a000
	s_movk_i32 s38, 0x180
	s_movk_i32 s39, 0x1ff
	v_mov_b32_e32 v1, v0

	.amdhsa_kernel _Z6pool_kPKfS0_S0_S0_S0_S0_PfS1_
		.amdhsa_group_segment_fixed_size 47872
		.amdhsa_private_segment_fixed_size 0
		.amdhsa_kernarg_size 64
		.amdhsa_user_sgpr_count 2
		.amdhsa_user_sgpr_dispatch_ptr 0
		.amdhsa_user_sgpr_queue_ptr 0
		.amdhsa_user_sgpr_kernarg_segment_ptr 1
		.amdhsa_user_sgpr_dispatch_id 0
		.amdhsa_user_sgpr_kernarg_preload_length 0
		.amdhsa_user_sgpr_kernarg_preload_offset 0
		.amdhsa_user_sgpr_private_segment_size 0
		.amdhsa_uses_dynamic_stack 0
		.amdhsa_enable_private_segment 0
		.amdhsa_system_sgpr_workgroup_id_x 1
		.amdhsa_system_sgpr_workgroup_id_y 1
		.amdhsa_system_sgpr_workgroup_id_z 0
		.amdhsa_system_sgpr_workgroup_info 0
		.amdhsa_system_vgpr_workitem_id 0
		.amdhsa_next_free_vgpr 225
		.amdhsa_next_free_sgpr 96
		.amdhsa_accum_offset 228
		.amdhsa_reserve_vcc 1
		.amdhsa_float_round_mode_32 0
		.amdhsa_float_round_mode_16_64 0
		.amdhsa_float_denorm_mode_32 3
		.amdhsa_float_denorm_mode_16_64 3
		.amdhsa_dx10_clamp 1
		.amdhsa_ieee_mode 1
		.amdhsa_fp16_overflow 0
		.amdhsa_tg_split 0
		.amdhsa_exception_fp_ieee_invalid_op 0
		.amdhsa_exception_fp_denorm_src 0
		.amdhsa_exception_fp_ieee_div_zero 0
		.amdhsa_exception_fp_ieee_overflow 0
		.amdhsa_exception_fp_ieee_underflow 0
		.amdhsa_exception_fp_ieee_inexact 0
		.amdhsa_exception_int_div_zero 0
	.end_amdhsa_kernel

_Z7gemm2_kILi0ELi3ELi1EEv5GArgs:
	v_lshlrev_b32_e32 v192, 4, v0
	s_getpc_b64 s[92:93]
	s_add_u32 s92, s92, 0xffff89f8
	s_addc_u32 s93, s93, 0xffffffff
	global_load_dwordx4 v[188:191], v192, s[92:93]
	s_load_dwordx8 s[8:15], s[0:1], 0x68
	s_cmpk_lt_u32 s2, 0xc0
	s_mov_b64 s[4:5], -1
	s_cbranch_scc0 .LBB11_26
	v_lshrrev_b32_e32 v149, 6, v0
	s_lshl_b32 s3, s2, 8
	v_bfe_u32 v1, v0, 3, 3
	s_load_dwordx4 s[4:7], s[0:1], 0x0
	s_load_dwordx4 s[16:19], s[0:1], 0x18
	s_and_b32 s20, s3, 0xf00
	v_lshl_or_b32 v6, v149, 5, v1
	v_or_b32_e32 v8, s20, v6
	v_mul_u32_u24_e32 v2, 0x340, v8
	v_bfe_u32 v4, v0, 4, 2
	v_lshlrev_b32_e32 v146, 1, v2
	v_mov_b32_e32 v147, 0
	v_bitop3_b32 v4, v4, v0, 7 bitop3:0x78
	s_waitcnt lgkmcnt(0)
	v_lshl_add_u64 v[2:3], s[4:5], 0, v[146:147]
	v_lshlrev_b32_e32 v146, 4, v4
	v_or_b32_e32 v4, 8, v6
	v_lshl_add_u64 v[98:99], v[2:3], 0, v[146:147]
	v_or_b32_e32 v2, s20, v4
	v_lshrrev_b32_e32 v4, 1, v4
	v_xor_b32_e32 v4, v4, v0
	v_mul_u32_u24_e32 v2, 0x340, v2
	v_mov_b32_e32 v3, v147
	v_lshlrev_b32_e32 v4, 4, v4
	v_lshl_add_u64 v[2:3], v[2:3], 1, s[4:5]
	v_and_b32_e32 v4, 0x70, v4
	v_mov_b32_e32 v5, v147
	v_lshl_add_u64 v[100:101], v[2:3], 0, v[4:5]
	v_or_b32_e32 v2, 16, v8
	v_mul_u32_u24_e32 v2, 0x340, v2
	v_mov_b32_e32 v3, v147
	v_lshl_add_u64 v[2:3], v[2:3], 1, s[4:5]
	v_xor_b32_e32 v146, 16, v146
	v_or_b32_e32 v4, 24, v6
	v_lshl_add_u64 v[102:103], v[2:3], 0, v[146:147]
	v_or_b32_e32 v2, s20, v4
	v_lshrrev_b32_e32 v4, 1, v4
	v_xor_b32_e32 v4, v4, v0
	v_lshlrev_b32_e32 v4, 3, v4
	v_mul_u32_u24_e32 v146, 0x340, v2
	v_bitop3_b32 v4, v4, 8, 56 bitop3:0x6c
	s_lshr_b32 s36, s2, 6
	s_bfe_u32 s21, s2, 0x20004
	v_lshl_add_u64 v[2:3], v[146:147], 1, s[4:5]
	v_lshlrev_b32_e32 v146, 1, v4
	v_lshl_add_u64 v[104:105], v[2:3], 0, v[146:147]
	s_mul_i32 s20, s21, 0xc0
	s_mul_i32 s4, s36, 0x300
	v_mul_u32_u24_e32 v2, 24, v149
	v_mul_u32_u24_e32 v4, 3, v149
	s_add_i32 s21, s20, s4
	v_or_b32_e32 v5, v2, v1
	v_add_u32_e32 v2, s21, v5
	v_bfe_u32 v5, v5, 1, 3
	v_lshrrev_b32_e32 v4, 1, v4
	v_and_b32_e32 v7, 7, v0
	s_movk_i32 s22, 0x680
	v_bitop3_b32 v4, v4, v5, 1 bitop3:0x6c
	v_mad_u32_u24 v6, v149, 3, 1
	v_mul_lo_u32 v146, v2, s22
	v_xor_b32_e32 v4, v4, v7
	v_lshl_or_b32 v8, v6, 3, v1
	v_lshl_add_u64 v[2:3], s[6:7], 0, v[146:147]
	v_lshlrev_b32_e32 v146, 4, v4
	v_add_u32_e32 v4, s21, v8
	v_bfe_u32 v8, v8, 1, 3
	v_lshrrev_b32_e32 v9, 1, v6
	v_bitop3_b32 v8, v9, v8, 1 bitop3:0x6c
	v_lshl_add_u64 v[106:107], v[2:3], 0, v[146:147]
	v_mov_b64_e32 v[2:3], s[6:7]
	v_xor_b32_e32 v8, v8, v7
	v_mad_u64_u32 v[4:5], s[4:5], v4, s22, v[2:3]
	v_lshlrev_b32_e32 v146, 4, v8
	v_lshl_add_u64 v[108:109], v[4:5], 0, v[146:147]
	v_mad_u32_u24 v4, v149, 3, 2
	v_lshl_or_b32 v1, v4, 3, v1
	v_add_u32_e32 v5, s21, v1
	v_mad_u64_u32 v[2:3], s[4:5], v5, s22, v[2:3]
	v_bfe_u32 v1, v1, 1, 3
	v_lshrrev_b32_e32 v5, 1, v4
	v_lshlrev_b32_e32 v141, 12, v149
	v_bitop3_b32 v1, v5, v1, 1 bitop3:0x6c
	v_readfirstlane_b32 s33, v141
	v_or_b32_e32 v142, 0x400, v141
	v_xor_b32_e32 v1, v1, v7
	s_mov_b32 m0, s33
	v_readfirstlane_b32 s28, v142
	v_or_b32_e32 v143, 0x800, v141
	v_lshlrev_b32_e32 v146, 4, v1
	global_load_lds_dwordx4 v[98:99], off
	s_mov_b32 m0, s28
	v_readfirstlane_b32 s29, v143
	v_or_b32_e32 v144, 0xc00, v141
	v_mul_u32_u24_e32 v1, 0xc00, v149
	global_load_lds_dwordx4 v[100:101], off
	s_mov_b32 m0, s29
	v_readfirstlane_b32 s30, v144
	v_or_b32_e32 v145, 0x10000, v1
	v_lshlrev_b32_e32 v1, 10, v6
	v_lshl_add_u64 v[110:111], v[2:3], 0, v[146:147]
	global_load_lds_dwordx4 v[102:103], off
	s_mov_b32 m0, s30
	v_readfirstlane_b32 s31, v145
	v_or_b32_e32 v146, 0x10000, v1
	v_lshlrev_b32_e32 v4, 10, v4
	global_load_lds_dwordx4 v[104:105], off
	s_mov_b32 m0, s31
	v_readfirstlane_b32 s34, v146
	v_or_b32_e32 v148, 0x10000, v4
	global_load_lds_dwordx4 v[106:107], off
	s_mov_b32 m0, s34
	v_readfirstlane_b32 s35, v148
	v_or_b32_e32 v134, 0x8000, v141
	global_load_lds_dwordx4 v[108:109], off
	s_mov_b32 m0, s35
	s_mov_b64 s[4:5], 0x80
	v_readfirstlane_b32 s24, v134
	v_or_b32_e32 v135, 0x8400, v141
	global_load_lds_dwordx4 v[110:111], off
	v_lshl_add_u64 v[2:3], v[98:99], 0, s[4:5]
	s_mov_b32 m0, s24
	v_readfirstlane_b32 s21, v135
	v_or_b32_e32 v136, 0x8800, v141
	s_movk_i32 s6, 0xc00
	s_waitcnt vmcnt(0)
	s_waitcnt vmcnt(0) lgkmcnt(0)
	s_barrier
	global_load_lds_dwordx4 v[2:3], off
	v_lshl_add_u64 v[2:3], v[100:101], 0, s[4:5]
	s_mov_b32 m0, s21
	v_readfirstlane_b32 s22, v136
	v_or_b32_e32 v137, 0x8c00, v141
	v_mov_b32_e32 v5, 0x16000
	global_load_lds_dwordx4 v[2:3], off
	v_lshl_add_u64 v[2:3], v[102:103], 0, s[4:5]
	s_mov_b32 m0, s22
	v_readfirstlane_b32 s23, v137
	v_mad_u32_u24 v138, v149, s6, v5
	global_load_lds_dwordx4 v[2:3], off
	v_lshl_add_u64 v[2:3], v[104:105], 0, s[4:5]
	s_mov_b32 m0, s23
	v_readfirstlane_b32 s25, v138
	v_add_u32_e32 v139, 0x16000, v1
	global_load_lds_dwordx4 v[2:3], off
	v_lshl_add_u64 v[2:3], v[106:107], 0, s[4:5]
	s_mov_b32 m0, s25
	v_readfirstlane_b32 s26, v139
	v_add_u32_e32 v140, 0x16000, v4
	global_load_lds_dwordx4 v[2:3], off
	v_lshl_add_u64 v[2:3], v[108:109], 0, s[4:5]
	s_mov_b32 m0, s26
	v_readfirstlane_b32 s27, v140
	global_load_lds_dwordx4 v[2:3], off
	v_lshl_add_u64 v[2:3], v[110:111], 0, s[4:5]
	s_mov_b32 m0, s27
	v_and_b32_e32 v156, 31, v0
	global_load_lds_dwordx4 v[2:3], off
	v_and_b32_e32 v2, 64, v0
	v_mov_b32_e32 v3, 0x60
	v_cmp_ne_u32_e32 vcc, 0, v2
	v_bfe_u32 v153, v0, 5, 1
	v_lshrrev_b32_e32 v157, 1, v0
	v_cndmask_b32_e32 v151, 0, v3, vcc
	v_lshlrev_b32_e32 v3, 6, v0
	v_or_b32_e32 v2, v151, v156
	v_and_b32_e32 v115, 0x6000, v3
	v_bfe_u32 v3, v0, 4, 1
	v_lshlrev_b32_e32 v152, 7, v2
	v_or_b32_e32 v2, 6, v153
	v_bitop3_b32 v3, v157, v3, 7 bitop3:0x6c
	s_load_dwordx2 s[6:7], s[0:1], 0x28
	v_xor_b32_e32 v2, v2, v3
	v_lshlrev_b32_e32 v154, 4, v2
	v_or_b32_e32 v2, 4, v153
	v_xor_b32_e32 v2, v2, v3
	v_lshlrev_b32_e32 v155, 4, v2
	v_or_b32_e32 v2, 2, v153
	s_cmp_lt_u32 s2, 64
	v_xor_b32_e32 v2, v2, v3
	s_cselect_b64 s[4:5], -1, 0
	s_cmp_eq_u32 s36, 1
	v_lshlrev_b32_e32 v18, 4, v2
	v_xor_b32_e32 v2, v3, v153
	s_waitcnt lgkmcnt(0)
	s_cselect_b32 s18, s18, s6
	s_cselect_b32 s19, s19, s7
	s_and_b64 s[6:7], s[4:5], exec
	v_and_b32_e32 v1, 63, v0
	v_lshlrev_b32_e32 v150, 7, v156
	v_lshlrev_b32_e32 v2, 4, v2
	s_cselect_b32 s7, s17, s19
	s_cselect_b32 s6, s16, s18
	v_or_b32_e32 v182, v2, v152
	v_or_b32_e32 v2, v2, v115
	v_add_u32_e32 v112, v2, v150
	ds_read_b128 v[2:5], v112
	v_or_b32_e32 v116, 0x10000, v182
	v_add_u32_e32 v117, 0x11000, v182
	v_add_u32_e32 v118, 0x12000, v182
	ds_read_b128 v[6:9], v116
	ds_read_b128 v[10:13], v117
	ds_read_b128 v[14:17], v112 offset:4096
	ds_read_b128 v[122:125], v118
	v_or_b32_e32 v19, v18, v115
	v_add_u32_e32 v113, v19, v150
	s_waitcnt lgkmcnt(0)
	v_mfma_f32_32x32x16_f16 v[82:97], v[2:5], v[6:9], 0
	ds_read_b128 v[126:129], v113
	v_or_b32_e32 v183, v18, v152
	v_add_u32_e32 v120, 0x11000, v183
	v_or_b32_e32 v119, 0x10000, v183
	ds_read_b128 v[130:133], v113 offset:4096
	ds_read_b128 v[158:161], v119
	v_add_u32_e32 v121, 0x12000, v183
	ds_read_b128 v[162:165], v120
	ds_read_b128 v[166:169], v121
	v_mfma_f32_32x32x16_f16 v[66:81], v[2:5], v[10:13], 0
	v_mfma_f32_32x32x16_f16 v[50:65], v[2:5], v[122:125], 0
	v_mfma_f32_32x32x16_f16 v[34:49], v[14:17], v[6:9], 0
	v_mfma_f32_32x32x16_f16 v[18:33], v[14:17], v[10:13], 0
	v_mfma_f32_32x32x16_f16 v[2:17], v[14:17], v[122:125], 0
	s_waitcnt lgkmcnt(0)
	v_mfma_f32_32x32x16_f16 v[82:97], v[126:129], v[158:161], v[82:97]
	v_or_b32_e32 v114, v155, v115
	v_or_b32_e32 v155, v155, v152
	v_add_u32_e32 v114, v114, v150
	v_or_b32_e32 v122, 0x10000, v155
	v_add_u32_e32 v123, 0x11000, v155
	v_add_u32_e32 v124, 0x12000, v155
	v_mfma_f32_32x32x16_f16 v[66:81], v[126:129], v[162:165], v[66:81]
	v_mfma_f32_32x32x16_f16 v[50:65], v[126:129], v[166:169], v[50:65]
	v_mfma_f32_32x32x16_f16 v[34:49], v[130:133], v[158:161], v[34:49]
	ds_read_b128 v[126:129], v114
	ds_read_b128 v[158:161], v114 offset:4096
	v_mfma_f32_32x32x16_f16 v[18:33], v[130:133], v[162:165], v[18:33]
	ds_read_b128 v[162:165], v122
	ds_read_b128 v[170:173], v123
	ds_read_b128 v[174:177], v124
	v_mfma_f32_32x32x16_f16 v[2:17], v[130:133], v[166:169], v[2:17]
	s_waitcnt lgkmcnt(0)
	v_mfma_f32_32x32x16_f16 v[82:97], v[126:129], v[162:165], v[82:97]
	v_or_b32_e32 v115, v154, v115
	v_or_b32_e32 v133, v154, v152
	v_add_u32_e32 v115, v115, v150
	v_or_b32_e32 v125, 0x10000, v133
	v_mfma_f32_32x32x16_f16 v[66:81], v[126:129], v[170:173], v[66:81]
	v_mfma_f32_32x32x16_f16 v[50:65], v[126:129], v[174:177], v[50:65]
	v_add_u32_e32 v126, 0x11000, v133
	v_add_u32_e32 v127, 0x12000, v133
	v_mfma_f32_32x32x16_f16 v[34:49], v[158:161], v[162:165], v[34:49]
	ds_read_b128 v[128:131], v115
	ds_read_b128 v[162:165], v115 offset:4096
	v_mfma_f32_32x32x16_f16 v[18:33], v[158:161], v[170:173], v[18:33]
	ds_read_b128 v[166:169], v125
	ds_read_b128 v[170:173], v126
	ds_read_b128 v[178:181], v127
	v_mfma_f32_32x32x16_f16 v[2:17], v[158:161], v[174:177], v[2:17]
	s_waitcnt lgkmcnt(0)
	v_mfma_f32_32x32x16_f16 v[82:97], v[128:131], v[166:169], v[82:97]
	v_mfma_f32_32x32x16_f16 v[66:81], v[128:131], v[170:173], v[66:81]
	v_mfma_f32_32x32x16_f16 v[50:65], v[128:131], v[178:181], v[50:65]
	v_mfma_f32_32x32x16_f16 v[34:49], v[162:165], v[166:169], v[34:49]
	v_mfma_f32_32x32x16_f16 v[18:33], v[162:165], v[170:173], v[18:33]
	v_mfma_f32_32x32x16_f16 v[2:17], v[162:165], v[178:181], v[2:17]
	s_mov_b64 s[16:17], 0x100
	s_mov_b32 m0, s33
	v_lshl_add_u64 v[128:129], v[98:99], 0, s[16:17]
	s_waitcnt vmcnt(0)
	s_waitcnt vmcnt(0)
	s_barrier
	global_load_lds_dwordx4 v[128:129], off
	v_lshl_add_u64 v[128:129], v[100:101], 0, s[16:17]
	s_mov_b32 m0, s28
	s_nop 0
	global_load_lds_dwordx4 v[128:129], off
	v_lshl_add_u64 v[128:129], v[102:103], 0, s[16:17]
	s_mov_b32 m0, s29
	s_nop 0
	global_load_lds_dwordx4 v[128:129], off
	v_lshl_add_u64 v[128:129], v[104:105], 0, s[16:17]
	s_mov_b32 m0, s30
	s_nop 0
	global_load_lds_dwordx4 v[128:129], off
	v_lshl_add_u64 v[128:129], v[106:107], 0, s[16:17]
	s_mov_b32 m0, s31
	s_nop 0
	global_load_lds_dwordx4 v[128:129], off
	v_lshl_add_u64 v[128:129], v[108:109], 0, s[16:17]
	s_mov_b32 m0, s34
	s_nop 0
	global_load_lds_dwordx4 v[128:129], off
	v_lshl_add_u64 v[128:129], v[110:111], 0, s[16:17]
	s_mov_b32 m0, s35
	s_nop 0
	global_load_lds_dwordx4 v[128:129], off
	ds_read_b128 v[158:161], v112 offset:32768
	v_add_u32_e32 v129, 0x16000, v182
	v_add_u32_e32 v130, 0x17000, v182
	v_or_b32_e32 v131, 0x18000, v182
	ds_read_b128 v[162:165], v129
	ds_read_b128 v[166:169], v112 offset:36864
	ds_read_b128 v[170:173], v130
	ds_read_b128 v[174:177], v131
	v_add_u32_e32 v128, 0x16000, v183
	ds_read_b128 v[178:181], v128
	s_waitcnt lgkmcnt(0)
	v_mfma_f32_32x32x16_f16 v[82:97], v[158:161], v[162:165], v[82:97]
	v_mfma_f32_32x32x16_f16 v[66:81], v[158:161], v[170:173], v[66:81]
	v_mfma_f32_32x32x16_f16 v[50:65], v[158:161], v[174:177], v[50:65]
	v_mfma_f32_32x32x16_f16 v[34:49], v[166:169], v[162:165], v[34:49]
	v_mfma_f32_32x32x16_f16 v[18:33], v[166:169], v[170:173], v[18:33]
	ds_read_b128 v[158:161], v113 offset:32768
	ds_read_b128 v[162:165], v113 offset:36864
	ds_read_b128 v[170:173], v128 offset:4096
	ds_read_b128 v[182:185], v128 offset:8192
	v_mfma_f32_32x32x16_f16 v[2:17], v[166:169], v[174:177], v[2:17]
	s_waitcnt lgkmcnt(0)
	v_mfma_f32_32x32x16_f16 v[82:97], v[158:161], v[178:181], v[82:97]
	v_add_u32_e32 v132, 0x16000, v155
	v_mfma_f32_32x32x16_f16 v[66:81], v[158:161], v[170:173], v[66:81]
	v_mfma_f32_32x32x16_f16 v[50:65], v[158:161], v[182:185], v[50:65]
	ds_read_b128 v[158:161], v114 offset:32768
	ds_read_b128 v[166:169], v114 offset:36864
	v_mfma_f32_32x32x16_f16 v[34:49], v[162:165], v[178:181], v[34:49]
	v_mfma_f32_32x32x16_f16 v[18:33], v[162:165], v[170:173], v[18:33]
	ds_read_b128 v[170:173], v132
	ds_read_b128 v[174:177], v132 offset:4096
	ds_read_b128 v[178:181], v132 offset:8192
	v_mfma_f32_32x32x16_f16 v[2:17], v[162:165], v[182:185], v[2:17]
	s_waitcnt lgkmcnt(0)
	v_mfma_f32_32x32x16_f16 v[82:97], v[158:161], v[170:173], v[82:97]
	v_add_u32_e32 v133, 0x16000, v133
	v_mfma_f32_32x32x16_f16 v[66:81], v[158:161], v[174:177], v[66:81]
	v_mfma_f32_32x32x16_f16 v[50:65], v[158:161], v[178:181], v[50:65]
	ds_read_b128 v[158:161], v115 offset:32768
	ds_read_b128 v[162:165], v115 offset:36864
	v_mfma_f32_32x32x16_f16 v[34:49], v[166:169], v[170:173], v[34:49]
	v_mfma_f32_32x32x16_f16 v[18:33], v[166:169], v[174:177], v[18:33]
	ds_read_b128 v[170:173], v133
	ds_read_b128 v[174:177], v133 offset:4096
	ds_read_b128 v[182:185], v133 offset:8192
	v_mfma_f32_32x32x16_f16 v[2:17], v[166:169], v[178:181], v[2:17]
	s_waitcnt lgkmcnt(0)
	v_mfma_f32_32x32x16_f16 v[82:97], v[158:161], v[170:173], v[82:97]
	v_mfma_f32_32x32x16_f16 v[66:81], v[158:161], v[174:177], v[66:81]
	v_mfma_f32_32x32x16_f16 v[50:65], v[158:161], v[182:185], v[50:65]
	v_mfma_f32_32x32x16_f16 v[34:49], v[162:165], v[170:173], v[34:49]
	v_mfma_f32_32x32x16_f16 v[18:33], v[162:165], v[174:177], v[18:33]
	v_mfma_f32_32x32x16_f16 v[2:17], v[162:165], v[182:185], v[2:17]
	s_mov_b64 s[16:17], 0x180
	s_mov_b32 m0, s24
	v_lshl_add_u64 v[154:155], v[98:99], 0, s[16:17]
	s_waitcnt vmcnt(0)
	s_waitcnt vmcnt(0)
	s_barrier
	global_load_lds_dwordx4 v[154:155], off
	v_lshl_add_u64 v[154:155], v[100:101], 0, s[16:17]
	s_mov_b32 m0, s21
	s_nop 0
	global_load_lds_dwordx4 v[154:155], off
	v_lshl_add_u64 v[154:155], v[102:103], 0, s[16:17]
	s_mov_b32 m0, s22
	s_nop 0
	global_load_lds_dwordx4 v[154:155], off
	v_lshl_add_u64 v[154:155], v[104:105], 0, s[16:17]
	s_mov_b32 m0, s23
	s_nop 0
	global_load_lds_dwordx4 v[154:155], off
	v_lshl_add_u64 v[154:155], v[106:107], 0, s[16:17]
	s_mov_b32 m0, s25
	s_nop 0
	global_load_lds_dwordx4 v[154:155], off
	v_lshl_add_u64 v[154:155], v[108:109], 0, s[16:17]
	s_mov_b32 m0, s26
	s_nop 0
	global_load_lds_dwordx4 v[154:155], off
	v_lshl_add_u64 v[154:155], v[110:111], 0, s[16:17]
	s_mov_b32 m0, s27
	s_nop 0
	global_load_lds_dwordx4 v[154:155], off
	ds_read_b128 v[158:161], v112
	ds_read_b128 v[162:165], v116
	ds_read_b128 v[166:169], v112 offset:4096
	ds_read_b128 v[170:173], v117
	ds_read_b128 v[174:177], v118
	ds_read_b128 v[178:181], v113
	s_waitcnt lgkmcnt(0)
	v_mfma_f32_32x32x16_f16 v[82:97], v[158:161], v[162:165], v[82:97]
	v_mfma_f32_32x32x16_f16 v[66:81], v[158:161], v[170:173], v[66:81]
	v_mfma_f32_32x32x16_f16 v[50:65], v[158:161], v[174:177], v[50:65]
	v_mfma_f32_32x32x16_f16 v[34:49], v[166:169], v[162:165], v[34:49]
	v_mfma_f32_32x32x16_f16 v[18:33], v[166:169], v[170:173], v[18:33]
	ds_read_b128 v[158:161], v113 offset:4096
	ds_read_b128 v[162:165], v119
	ds_read_b128 v[170:173], v120
	ds_read_b128 v[182:185], v121
	v_mfma_f32_32x32x16_f16 v[2:17], v[166:169], v[174:177], v[2:17]
	s_waitcnt lgkmcnt(0)
	v_mfma_f32_32x32x16_f16 v[82:97], v[178:181], v[162:165], v[82:97]
	v_mfma_f32_32x32x16_f16 v[66:81], v[178:181], v[170:173], v[66:81]
	v_mfma_f32_32x32x16_f16 v[50:65], v[178:181], v[182:185], v[50:65]
	v_mfma_f32_32x32x16_f16 v[34:49], v[158:161], v[162:165], v[34:49]
	v_mfma_f32_32x32x16_f16 v[18:33], v[158:161], v[170:173], v[18:33]
	ds_read_b128 v[162:165], v114
	ds_read_b128 v[166:169], v114 offset:4096
	ds_read_b128 v[170:173], v122
	ds_read_b128 v[174:177], v123
	ds_read_b128 v[178:181], v124
	v_mfma_f32_32x32x16_f16 v[2:17], v[158:161], v[182:185], v[2:17]
	s_waitcnt lgkmcnt(0)
	v_mfma_f32_32x32x16_f16 v[82:97], v[162:165], v[170:173], v[82:97]
	v_mfma_f32_32x32x16_f16 v[66:81], v[162:165], v[174:177], v[66:81]
	v_mfma_f32_32x32x16_f16 v[50:65], v[162:165], v[178:181], v[50:65]
	v_mfma_f32_32x32x16_f16 v[34:49], v[166:169], v[170:173], v[34:49]
	v_mfma_f32_32x32x16_f16 v[18:33], v[166:169], v[174:177], v[18:33]
	ds_read_b128 v[158:161], v115
	ds_read_b128 v[162:165], v115 offset:4096
	ds_read_b128 v[170:173], v125
	ds_read_b128 v[174:177], v126
	ds_read_b128 v[182:185], v127
	v_mfma_f32_32x32x16_f16 v[2:17], v[166:169], v[178:181], v[2:17]
	s_waitcnt lgkmcnt(0)
	v_mfma_f32_32x32x16_f16 v[82:97], v[158:161], v[170:173], v[82:97]
	v_mfma_f32_32x32x16_f16 v[66:81], v[158:161], v[174:177], v[66:81]
	v_mfma_f32_32x32x16_f16 v[50:65], v[158:161], v[182:185], v[50:65]
	v_mfma_f32_32x32x16_f16 v[34:49], v[162:165], v[170:173], v[34:49]
	v_mfma_f32_32x32x16_f16 v[18:33], v[162:165], v[174:177], v[18:33]
	v_mfma_f32_32x32x16_f16 v[2:17], v[162:165], v[182:185], v[2:17]
	s_mov_b64 s[16:17], 0x200
	s_mov_b32 m0, s33
	v_lshl_add_u64 v[154:155], v[98:99], 0, s[16:17]
	s_waitcnt vmcnt(0)
	s_waitcnt vmcnt(0)
	s_barrier
	global_load_lds_dwordx4 v[154:155], off
	v_lshl_add_u64 v[154:155], v[100:101], 0, s[16:17]
	s_mov_b32 m0, s28
	s_nop 0
	global_load_lds_dwordx4 v[154:155], off
	v_lshl_add_u64 v[154:155], v[102:103], 0, s[16:17]
	s_mov_b32 m0, s29
	s_nop 0
	global_load_lds_dwordx4 v[154:155], off
	v_lshl_add_u64 v[154:155], v[104:105], 0, s[16:17]
	s_mov_b32 m0, s30
	s_nop 0
	global_load_lds_dwordx4 v[154:155], off
	v_lshl_add_u64 v[154:155], v[106:107], 0, s[16:17]
	s_mov_b32 m0, s31
	s_nop 0
	global_load_lds_dwordx4 v[154:155], off
	v_lshl_add_u64 v[154:155], v[108:109], 0, s[16:17]
	s_mov_b32 m0, s34
	s_nop 0
	global_load_lds_dwordx4 v[154:155], off
	v_lshl_add_u64 v[154:155], v[110:111], 0, s[16:17]
	s_mov_b32 m0, s35
	s_nop 0
	global_load_lds_dwordx4 v[154:155], off
	ds_read_b128 v[158:161], v112 offset:32768
	ds_read_b128 v[162:165], v129
	ds_read_b128 v[166:169], v112 offset:36864
	ds_read_b128 v[170:173], v130
	ds_read_b128 v[174:177], v131
	ds_read_b128 v[178:181], v128
	s_waitcnt lgkmcnt(0)
	v_mfma_f32_32x32x16_f16 v[82:97], v[158:161], v[162:165], v[82:97]
	v_mfma_f32_32x32x16_f16 v[66:81], v[158:161], v[170:173], v[66:81]
	v_mfma_f32_32x32x16_f16 v[50:65], v[158:161], v[174:177], v[50:65]
	v_mfma_f32_32x32x16_f16 v[34:49], v[166:169], v[162:165], v[34:49]
	v_mfma_f32_32x32x16_f16 v[18:33], v[166:169], v[170:173], v[18:33]
	ds_read_b128 v[158:161], v113 offset:32768
	ds_read_b128 v[162:165], v113 offset:36864
	ds_read_b128 v[170:173], v128 offset:4096
	ds_read_b128 v[182:185], v128 offset:8192
	v_mfma_f32_32x32x16_f16 v[2:17], v[166:169], v[174:177], v[2:17]
	s_waitcnt lgkmcnt(0)
	v_mfma_f32_32x32x16_f16 v[82:97], v[158:161], v[178:181], v[82:97]
	v_mfma_f32_32x32x16_f16 v[66:81], v[158:161], v[170:173], v[66:81]
	v_mfma_f32_32x32x16_f16 v[50:65], v[158:161], v[182:185], v[50:65]
	v_mfma_f32_32x32x16_f16 v[34:49], v[162:165], v[178:181], v[34:49]
	v_mfma_f32_32x32x16_f16 v[18:33], v[162:165], v[170:173], v[18:33]
	ds_read_b128 v[158:161], v114 offset:32768
	ds_read_b128 v[166:169], v114 offset:36864
	ds_read_b128 v[170:173], v132
	ds_read_b128 v[174:177], v132 offset:4096
	ds_read_b128 v[178:181], v132 offset:8192
	v_mfma_f32_32x32x16_f16 v[2:17], v[162:165], v[182:185], v[2:17]
	s_waitcnt lgkmcnt(0)
	v_mfma_f32_32x32x16_f16 v[82:97], v[158:161], v[170:173], v[82:97]
	v_mfma_f32_32x32x16_f16 v[66:81], v[158:161], v[174:177], v[66:81]
	v_mfma_f32_32x32x16_f16 v[50:65], v[158:161], v[178:181], v[50:65]
	v_mfma_f32_32x32x16_f16 v[34:49], v[166:169], v[170:173], v[34:49]
	v_mfma_f32_32x32x16_f16 v[18:33], v[166:169], v[174:177], v[18:33]
	ds_read_b128 v[158:161], v115 offset:32768
	ds_read_b128 v[162:165], v115 offset:36864
	ds_read_b128 v[170:173], v133
	ds_read_b128 v[174:177], v133 offset:4096
	ds_read_b128 v[182:185], v133 offset:8192
	v_mfma_f32_32x32x16_f16 v[2:17], v[166:169], v[178:181], v[2:17]
	s_waitcnt lgkmcnt(0)
	v_mfma_f32_32x32x16_f16 v[82:97], v[158:161], v[170:173], v[82:97]
	v_mfma_f32_32x32x16_f16 v[66:81], v[158:161], v[174:177], v[66:81]
	v_mfma_f32_32x32x16_f16 v[50:65], v[158:161], v[182:185], v[50:65]
	v_mfma_f32_32x32x16_f16 v[34:49], v[162:165], v[170:173], v[34:49]
	v_mfma_f32_32x32x16_f16 v[18:33], v[162:165], v[174:177], v[18:33]
	v_mfma_f32_32x32x16_f16 v[2:17], v[162:165], v[182:185], v[2:17]
	s_mov_b64 s[16:17], 0x280
	s_mov_b32 m0, s24
	v_lshl_add_u64 v[154:155], v[98:99], 0, s[16:17]
	s_waitcnt vmcnt(0)
	s_waitcnt vmcnt(0)
	s_barrier
	global_load_lds_dwordx4 v[154:155], off
	v_lshl_add_u64 v[154:155], v[100:101], 0, s[16:17]
	s_mov_b32 m0, s21
	s_nop 0
	global_load_lds_dwordx4 v[154:155], off
	v_lshl_add_u64 v[154:155], v[102:103], 0, s[16:17]
	s_mov_b32 m0, s22
	s_nop 0
	global_load_lds_dwordx4 v[154:155], off
	v_lshl_add_u64 v[154:155], v[104:105], 0, s[16:17]
	s_mov_b32 m0, s23
	s_nop 0
	global_load_lds_dwordx4 v[154:155], off
	v_lshl_add_u64 v[154:155], v[106:107], 0, s[16:17]
	s_mov_b32 m0, s25
	s_nop 0
	global_load_lds_dwordx4 v[154:155], off
	v_lshl_add_u64 v[154:155], v[108:109], 0, s[16:17]
	s_mov_b32 m0, s26
	s_nop 0
	global_load_lds_dwordx4 v[154:155], off
	v_lshl_add_u64 v[154:155], v[110:111], 0, s[16:17]
	s_mov_b32 m0, s27
	s_nop 0
	global_load_lds_dwordx4 v[154:155], off
	ds_read_b128 v[158:161], v112
	ds_read_b128 v[162:165], v116
	ds_read_b128 v[166:169], v112 offset:4096
	ds_read_b128 v[170:173], v117
	ds_read_b128 v[174:177], v118
	ds_read_b128 v[178:181], v113
	s_waitcnt lgkmcnt(0)
	v_mfma_f32_32x32x16_f16 v[82:97], v[158:161], v[162:165], v[82:97]
	v_mfma_f32_32x32x16_f16 v[66:81], v[158:161], v[170:173], v[66:81]
	v_mfma_f32_32x32x16_f16 v[50:65], v[158:161], v[174:177], v[50:65]
	v_mfma_f32_32x32x16_f16 v[34:49], v[166:169], v[162:165], v[34:49]
	v_mfma_f32_32x32x16_f16 v[18:33], v[166:169], v[170:173], v[18:33]
	ds_read_b128 v[158:161], v113 offset:4096
	ds_read_b128 v[162:165], v119
	ds_read_b128 v[170:173], v120
	ds_read_b128 v[182:185], v121
	v_mfma_f32_32x32x16_f16 v[2:17], v[166:169], v[174:177], v[2:17]
	s_waitcnt lgkmcnt(0)
	v_mfma_f32_32x32x16_f16 v[82:97], v[178:181], v[162:165], v[82:97]
	v_mfma_f32_32x32x16_f16 v[66:81], v[178:181], v[170:173], v[66:81]
	v_mfma_f32_32x32x16_f16 v[50:65], v[178:181], v[182:185], v[50:65]
	v_mfma_f32_32x32x16_f16 v[34:49], v[158:161], v[162:165], v[34:49]
	v_mfma_f32_32x32x16_f16 v[18:33], v[158:161], v[170:173], v[18:33]
	ds_read_b128 v[162:165], v114
	ds_read_b128 v[166:169], v114 offset:4096
	ds_read_b128 v[170:173], v122
	ds_read_b128 v[174:177], v123
	ds_read_b128 v[178:181], v124
	v_mfma_f32_32x32x16_f16 v[2:17], v[158:161], v[182:185], v[2:17]
	s_waitcnt lgkmcnt(0)
	v_mfma_f32_32x32x16_f16 v[82:97], v[162:165], v[170:173], v[82:97]
	v_mfma_f32_32x32x16_f16 v[66:81], v[162:165], v[174:177], v[66:81]
	v_mfma_f32_32x32x16_f16 v[50:65], v[162:165], v[178:181], v[50:65]
	v_mfma_f32_32x32x16_f16 v[34:49], v[166:169], v[170:173], v[34:49]
	v_mfma_f32_32x32x16_f16 v[18:33], v[166:169], v[174:177], v[18:33]
	ds_read_b128 v[158:161], v115
	ds_read_b128 v[162:165], v115 offset:4096
	ds_read_b128 v[170:173], v125
	ds_read_b128 v[174:177], v126
	ds_read_b128 v[182:185], v127
	v_mfma_f32_32x32x16_f16 v[2:17], v[166:169], v[178:181], v[2:17]
	s_waitcnt lgkmcnt(0)
	v_mfma_f32_32x32x16_f16 v[82:97], v[158:161], v[170:173], v[82:97]
	v_mfma_f32_32x32x16_f16 v[66:81], v[158:161], v[174:177], v[66:81]
	v_mfma_f32_32x32x16_f16 v[50:65], v[158:161], v[182:185], v[50:65]
	v_mfma_f32_32x32x16_f16 v[34:49], v[162:165], v[170:173], v[34:49]
	v_mfma_f32_32x32x16_f16 v[18:33], v[162:165], v[174:177], v[18:33]
	v_mfma_f32_32x32x16_f16 v[2:17], v[162:165], v[182:185], v[2:17]
	s_mov_b64 s[22:23], 0x300
	v_readfirstlane_b32 s24, v141
	v_lshl_add_u64 v[154:155], v[98:99], 0, s[22:23]
	s_mov_b32 m0, s24
	v_readfirstlane_b32 s16, v142
	s_waitcnt vmcnt(0)
	s_waitcnt vmcnt(0)
	s_barrier
	global_load_lds_dwordx4 v[154:155], off
	v_lshl_add_u64 v[154:155], v[100:101], 0, s[22:23]
	s_mov_b32 m0, s16
	v_readfirstlane_b32 s17, v143
	global_load_lds_dwordx4 v[154:155], off
	v_lshl_add_u64 v[154:155], v[102:103], 0, s[22:23]
	s_mov_b32 m0, s17
	v_readfirstlane_b32 s18, v144
	global_load_lds_dwordx4 v[154:155], off
	v_lshl_add_u64 v[142:143], v[104:105], 0, s[22:23]
	s_mov_b32 m0, s18
	v_readfirstlane_b32 s19, v145
	global_load_lds_dwordx4 v[142:143], off
	v_lshl_add_u64 v[142:143], v[106:107], 0, s[22:23]
	s_mov_b32 m0, s19
	v_readfirstlane_b32 s21, v146
	global_load_lds_dwordx4 v[142:143], off
	v_lshl_add_u64 v[142:143], v[108:109], 0, s[22:23]
	s_mov_b32 m0, s21
	s_nop 0
	global_load_lds_dwordx4 v[142:143], off
	v_lshl_add_u64 v[142:143], v[110:111], 0, s[22:23]
	v_readfirstlane_b32 s22, v148
	s_mov_b32 m0, s22
	s_nop 0
	global_load_lds_dwordx4 v[142:143], off
	ds_read_b128 v[142:145], v112 offset:32768
	ds_read_b128 v[158:161], v129
	ds_read_b128 v[162:165], v112 offset:36864
	ds_read_b128 v[166:169], v130
	ds_read_b128 v[170:173], v131
	ds_read_b128 v[174:177], v128
	s_waitcnt lgkmcnt(0)
	v_mfma_f32_32x32x16_f16 v[82:97], v[142:145], v[158:161], v[82:97]
	v_mfma_f32_32x32x16_f16 v[66:81], v[142:145], v[166:169], v[66:81]
	v_mfma_f32_32x32x16_f16 v[50:65], v[142:145], v[170:173], v[50:65]
	v_mfma_f32_32x32x16_f16 v[34:49], v[162:165], v[158:161], v[34:49]
	v_mfma_f32_32x32x16_f16 v[18:33], v[162:165], v[166:169], v[18:33]
	ds_read_b128 v[142:145], v113 offset:32768
	ds_read_b128 v[158:161], v113 offset:36864
	ds_read_b128 v[166:169], v128 offset:4096
	ds_read_b128 v[178:181], v128 offset:8192
	v_mfma_f32_32x32x16_f16 v[2:17], v[162:165], v[170:173], v[2:17]
	s_waitcnt lgkmcnt(0)
	v_mfma_f32_32x32x16_f16 v[82:97], v[142:145], v[174:177], v[82:97]
	v_mfma_f32_32x32x16_f16 v[66:81], v[142:145], v[166:169], v[66:81]
	v_mfma_f32_32x32x16_f16 v[50:65], v[142:145], v[178:181], v[50:65]
	v_mfma_f32_32x32x16_f16 v[34:49], v[158:161], v[174:177], v[34:49]
	v_mfma_f32_32x32x16_f16 v[18:33], v[158:161], v[166:169], v[18:33]
	ds_read_b128 v[142:145], v114 offset:32768
	ds_read_b128 v[162:165], v114 offset:36864
	ds_read_b128 v[166:169], v132
	ds_read_b128 v[170:173], v132 offset:4096
	ds_read_b128 v[174:177], v132 offset:8192
	v_mfma_f32_32x32x16_f16 v[2:17], v[158:161], v[178:181], v[2:17]
	s_waitcnt lgkmcnt(0)
	v_mfma_f32_32x32x16_f16 v[82:97], v[142:145], v[166:169], v[82:97]
	v_mfma_f32_32x32x16_f16 v[66:81], v[142:145], v[170:173], v[66:81]
	v_mfma_f32_32x32x16_f16 v[50:65], v[142:145], v[174:177], v[50:65]
	v_mfma_f32_32x32x16_f16 v[34:49], v[162:165], v[166:169], v[34:49]
	v_mfma_f32_32x32x16_f16 v[18:33], v[162:165], v[170:173], v[18:33]
	ds_read_b128 v[142:145], v115 offset:32768
	ds_read_b128 v[158:161], v115 offset:36864
	ds_read_b128 v[166:169], v133
	ds_read_b128 v[170:173], v133 offset:4096
	ds_read_b128 v[178:181], v133 offset:8192
	v_mfma_f32_32x32x16_f16 v[2:17], v[162:165], v[174:177], v[2:17]
	s_waitcnt lgkmcnt(0)
	v_mfma_f32_32x32x16_f16 v[82:97], v[142:145], v[166:169], v[82:97]
	v_mfma_f32_32x32x16_f16 v[66:81], v[142:145], v[170:173], v[66:81]
	v_mfma_f32_32x32x16_f16 v[50:65], v[142:145], v[178:181], v[50:65]
	v_mfma_f32_32x32x16_f16 v[34:49], v[158:161], v[166:169], v[34:49]
	v_mfma_f32_32x32x16_f16 v[18:33], v[158:161], v[170:173], v[18:33]
	v_mfma_f32_32x32x16_f16 v[2:17], v[158:161], v[178:181], v[2:17]
	s_mov_b64 s[34:35], 0x380
	v_readfirstlane_b32 s30, v134
	v_lshl_add_u64 v[142:143], v[98:99], 0, s[34:35]
	s_mov_b32 m0, s30
	v_readfirstlane_b32 s23, v135
	s_waitcnt vmcnt(0)
	s_waitcnt vmcnt(0)
	s_barrier
	global_load_lds_dwordx4 v[142:143], off
	v_lshl_add_u64 v[142:143], v[100:101], 0, s[34:35]
	s_mov_b32 m0, s23
	v_readfirstlane_b32 s25, v136
	global_load_lds_dwordx4 v[142:143], off
	v_lshl_add_u64 v[134:135], v[102:103], 0, s[34:35]
	s_mov_b32 m0, s25
	v_readfirstlane_b32 s26, v137
	global_load_lds_dwordx4 v[134:135], off
	v_lshl_add_u64 v[134:135], v[104:105], 0, s[34:35]
	s_mov_b32 m0, s26
	v_readfirstlane_b32 s27, v138
	global_load_lds_dwordx4 v[134:135], off
	v_lshl_add_u64 v[134:135], v[106:107], 0, s[34:35]
	s_mov_b32 m0, s27
	v_readfirstlane_b32 s28, v139
	global_load_lds_dwordx4 v[134:135], off
	v_lshl_add_u64 v[134:135], v[108:109], 0, s[34:35]
	s_mov_b32 m0, s28
	v_readfirstlane_b32 s29, v140
	global_load_lds_dwordx4 v[134:135], off
	v_lshl_add_u64 v[134:135], v[110:111], 0, s[34:35]
	s_mov_b32 m0, s29
	s_nop 0
	global_load_lds_dwordx4 v[134:135], off
	ds_read_b128 v[134:137], v112
	ds_read_b128 v[138:141], v116
	ds_read_b128 v[142:145], v112 offset:4096
	ds_read_b128 v[158:161], v117
	ds_read_b128 v[162:165], v118
	ds_read_b128 v[166:169], v113
	s_waitcnt lgkmcnt(0)
	v_mfma_f32_32x32x16_f16 v[82:97], v[134:137], v[138:141], v[82:97]
	v_mfma_f32_32x32x16_f16 v[66:81], v[134:137], v[158:161], v[66:81]
	v_mfma_f32_32x32x16_f16 v[50:65], v[134:137], v[162:165], v[50:65]
	v_mfma_f32_32x32x16_f16 v[34:49], v[142:145], v[138:141], v[34:49]
	v_mfma_f32_32x32x16_f16 v[18:33], v[142:145], v[158:161], v[18:33]
	ds_read_b128 v[134:137], v113 offset:4096
	ds_read_b128 v[138:141], v119
	ds_read_b128 v[158:161], v120
	ds_read_b128 v[170:173], v121
	v_mfma_f32_32x32x16_f16 v[2:17], v[142:145], v[162:165], v[2:17]
	s_waitcnt lgkmcnt(0)
	v_mfma_f32_32x32x16_f16 v[82:97], v[166:169], v[138:141], v[82:97]
	v_mfma_f32_32x32x16_f16 v[66:81], v[166:169], v[158:161], v[66:81]
	v_mfma_f32_32x32x16_f16 v[50:65], v[166:169], v[170:173], v[50:65]
	v_mfma_f32_32x32x16_f16 v[34:49], v[134:137], v[138:141], v[34:49]
	v_mfma_f32_32x32x16_f16 v[18:33], v[134:137], v[158:161], v[18:33]
	ds_read_b128 v[138:141], v114
	ds_read_b128 v[142:145], v114 offset:4096
	ds_read_b128 v[158:161], v122
	ds_read_b128 v[162:165], v123
	ds_read_b128 v[166:169], v124
	v_mfma_f32_32x32x16_f16 v[2:17], v[134:137], v[170:173], v[2:17]
	s_waitcnt lgkmcnt(0)
	v_mfma_f32_32x32x16_f16 v[82:97], v[138:141], v[158:161], v[82:97]
	v_mfma_f32_32x32x16_f16 v[66:81], v[138:141], v[162:165], v[66:81]
	v_mfma_f32_32x32x16_f16 v[50:65], v[138:141], v[166:169], v[50:65]
	v_mfma_f32_32x32x16_f16 v[34:49], v[142:145], v[158:161], v[34:49]
	v_mfma_f32_32x32x16_f16 v[18:33], v[142:145], v[162:165], v[18:33]
	ds_read_b128 v[134:137], v115
	ds_read_b128 v[138:141], v115 offset:4096
	ds_read_b128 v[158:161], v125
	ds_read_b128 v[162:165], v126
	ds_read_b128 v[170:173], v127
	v_mfma_f32_32x32x16_f16 v[2:17], v[142:145], v[166:169], v[2:17]
	s_waitcnt lgkmcnt(0)
	v_mfma_f32_32x32x16_f16 v[82:97], v[134:137], v[158:161], v[82:97]
	v_mfma_f32_32x32x16_f16 v[66:81], v[134:137], v[162:165], v[66:81]
	v_mfma_f32_32x32x16_f16 v[50:65], v[134:137], v[170:173], v[50:65]
	v_mfma_f32_32x32x16_f16 v[34:49], v[138:141], v[158:161], v[34:49]
	v_mfma_f32_32x32x16_f16 v[18:33], v[138:141], v[162:165], v[18:33]
	v_mfma_f32_32x32x16_f16 v[2:17], v[138:141], v[170:173], v[2:17]
	s_mov_b64 s[34:35], 0x400
	s_mov_b32 m0, s24
	v_lshl_add_u64 v[134:135], v[98:99], 0, s[34:35]
	s_waitcnt vmcnt(0)
	s_waitcnt vmcnt(0)
	s_barrier
	global_load_lds_dwordx4 v[134:135], off
	v_lshl_add_u64 v[134:135], v[100:101], 0, s[34:35]
	s_mov_b32 m0, s16
	s_nop 0
	global_load_lds_dwordx4 v[134:135], off
	v_lshl_add_u64 v[134:135], v[102:103], 0, s[34:35]
	s_mov_b32 m0, s17
	s_nop 0
	global_load_lds_dwordx4 v[134:135], off
	v_lshl_add_u64 v[134:135], v[104:105], 0, s[34:35]
	s_mov_b32 m0, s18
	s_nop 0
	global_load_lds_dwordx4 v[134:135], off
	v_lshl_add_u64 v[134:135], v[106:107], 0, s[34:35]
	s_mov_b32 m0, s19
	s_nop 0
	global_load_lds_dwordx4 v[134:135], off
	v_lshl_add_u64 v[134:135], v[108:109], 0, s[34:35]
	s_mov_b32 m0, s21
	s_nop 0
	global_load_lds_dwordx4 v[134:135], off
	v_lshl_add_u64 v[134:135], v[110:111], 0, s[34:35]
	s_mov_b32 m0, s22
	s_nop 0
	global_load_lds_dwordx4 v[134:135], off
	ds_read_b128 v[134:137], v112 offset:32768
	ds_read_b128 v[138:141], v129
	ds_read_b128 v[142:145], v112 offset:36864
	ds_read_b128 v[158:161], v130
	ds_read_b128 v[162:165], v131
	ds_read_b128 v[166:169], v128
	s_waitcnt lgkmcnt(0)
	v_mfma_f32_32x32x16_f16 v[82:97], v[134:137], v[138:141], v[82:97]
	v_mfma_f32_32x32x16_f16 v[66:81], v[134:137], v[158:161], v[66:81]
	v_mfma_f32_32x32x16_f16 v[50:65], v[134:137], v[162:165], v[50:65]
	v_mfma_f32_32x32x16_f16 v[34:49], v[142:145], v[138:141], v[34:49]
	v_mfma_f32_32x32x16_f16 v[18:33], v[142:145], v[158:161], v[18:33]
	ds_read_b128 v[134:137], v113 offset:32768
	ds_read_b128 v[138:141], v113 offset:36864
	ds_read_b128 v[158:161], v128 offset:4096
	ds_read_b128 v[170:173], v128 offset:8192
	v_mfma_f32_32x32x16_f16 v[2:17], v[142:145], v[162:165], v[2:17]
	s_waitcnt lgkmcnt(0)
	v_mfma_f32_32x32x16_f16 v[82:97], v[134:137], v[166:169], v[82:97]
	v_mfma_f32_32x32x16_f16 v[66:81], v[134:137], v[158:161], v[66:81]
	v_mfma_f32_32x32x16_f16 v[50:65], v[134:137], v[170:173], v[50:65]
	v_mfma_f32_32x32x16_f16 v[34:49], v[138:141], v[166:169], v[34:49]
	v_mfma_f32_32x32x16_f16 v[18:33], v[138:141], v[158:161], v[18:33]
	ds_read_b128 v[134:137], v114 offset:32768
	ds_read_b128 v[142:145], v114 offset:36864
	ds_read_b128 v[158:161], v132
	ds_read_b128 v[162:165], v132 offset:4096
	ds_read_b128 v[166:169], v132 offset:8192
	v_mfma_f32_32x32x16_f16 v[2:17], v[138:141], v[170:173], v[2:17]
	s_waitcnt lgkmcnt(0)
	v_mfma_f32_32x32x16_f16 v[82:97], v[134:137], v[158:161], v[82:97]
	v_mfma_f32_32x32x16_f16 v[66:81], v[134:137], v[162:165], v[66:81]
	v_mfma_f32_32x32x16_f16 v[50:65], v[134:137], v[166:169], v[50:65]
	v_mfma_f32_32x32x16_f16 v[34:49], v[142:145], v[158:161], v[34:49]
	v_mfma_f32_32x32x16_f16 v[18:33], v[142:145], v[162:165], v[18:33]
	ds_read_b128 v[134:137], v115 offset:32768
	ds_read_b128 v[138:141], v115 offset:36864
	ds_read_b128 v[158:161], v133
	ds_read_b128 v[162:165], v133 offset:4096
	ds_read_b128 v[170:173], v133 offset:8192
	v_mfma_f32_32x32x16_f16 v[2:17], v[142:145], v[166:169], v[2:17]
	s_waitcnt lgkmcnt(0)
	v_mfma_f32_32x32x16_f16 v[82:97], v[134:137], v[158:161], v[82:97]
	v_mfma_f32_32x32x16_f16 v[66:81], v[134:137], v[162:165], v[66:81]
	v_mfma_f32_32x32x16_f16 v[50:65], v[134:137], v[170:173], v[50:65]
	v_mfma_f32_32x32x16_f16 v[34:49], v[138:141], v[158:161], v[34:49]
	v_mfma_f32_32x32x16_f16 v[18:33], v[138:141], v[162:165], v[18:33]
	v_mfma_f32_32x32x16_f16 v[2:17], v[138:141], v[170:173], v[2:17]
	s_mov_b64 s[34:35], 0x480
	s_mov_b32 m0, s30
	v_lshl_add_u64 v[134:135], v[98:99], 0, s[34:35]
	s_waitcnt vmcnt(0)
	s_waitcnt vmcnt(0)
	s_barrier
	global_load_lds_dwordx4 v[134:135], off
	v_lshl_add_u64 v[134:135], v[100:101], 0, s[34:35]
	s_mov_b32 m0, s23
	s_nop 0
	global_load_lds_dwordx4 v[134:135], off
	v_lshl_add_u64 v[134:135], v[102:103], 0, s[34:35]
	s_mov_b32 m0, s25
	s_nop 0
	global_load_lds_dwordx4 v[134:135], off
	v_lshl_add_u64 v[134:135], v[104:105], 0, s[34:35]
	s_mov_b32 m0, s26
	s_nop 0
	global_load_lds_dwordx4 v[134:135], off
	v_lshl_add_u64 v[134:135], v[106:107], 0, s[34:35]
	s_mov_b32 m0, s27
	s_nop 0
	global_load_lds_dwordx4 v[134:135], off
	v_lshl_add_u64 v[134:135], v[108:109], 0, s[34:35]
	s_mov_b32 m0, s28
	s_nop 0
	global_load_lds_dwordx4 v[134:135], off
	v_lshl_add_u64 v[134:135], v[110:111], 0, s[34:35]
	s_mov_b32 m0, s29
	s_nop 0
	global_load_lds_dwordx4 v[134:135], off
	ds_read_b128 v[134:137], v112
	ds_read_b128 v[138:141], v116
	ds_read_b128 v[142:145], v112 offset:4096
	ds_read_b128 v[158:161], v117
	ds_read_b128 v[162:165], v118
	ds_read_b128 v[166:169], v113
	s_waitcnt lgkmcnt(0)
	v_mfma_f32_32x32x16_f16 v[82:97], v[134:137], v[138:141], v[82:97]
	v_mfma_f32_32x32x16_f16 v[66:81], v[134:137], v[158:161], v[66:81]
	v_mfma_f32_32x32x16_f16 v[50:65], v[134:137], v[162:165], v[50:65]
	v_mfma_f32_32x32x16_f16 v[34:49], v[142:145], v[138:141], v[34:49]
	v_mfma_f32_32x32x16_f16 v[18:33], v[142:145], v[158:161], v[18:33]
	ds_read_b128 v[134:137], v113 offset:4096
	ds_read_b128 v[138:141], v119
	ds_read_b128 v[158:161], v120
	ds_read_b128 v[170:173], v121
	v_mfma_f32_32x32x16_f16 v[2:17], v[142:145], v[162:165], v[2:17]
	s_waitcnt lgkmcnt(0)
	v_mfma_f32_32x32x16_f16 v[82:97], v[166:169], v[138:141], v[82:97]
	v_mfma_f32_32x32x16_f16 v[66:81], v[166:169], v[158:161], v[66:81]
	v_mfma_f32_32x32x16_f16 v[50:65], v[166:169], v[170:173], v[50:65]
	v_mfma_f32_32x32x16_f16 v[34:49], v[134:137], v[138:141], v[34:49]
	v_mfma_f32_32x32x16_f16 v[18:33], v[134:137], v[158:161], v[18:33]
	ds_read_b128 v[138:141], v114
	ds_read_b128 v[142:145], v114 offset:4096
	ds_read_b128 v[158:161], v122
	ds_read_b128 v[162:165], v123
	ds_read_b128 v[166:169], v124
	v_mfma_f32_32x32x16_f16 v[2:17], v[134:137], v[170:173], v[2:17]
	s_waitcnt lgkmcnt(0)
	v_mfma_f32_32x32x16_f16 v[82:97], v[138:141], v[158:161], v[82:97]
	v_mfma_f32_32x32x16_f16 v[66:81], v[138:141], v[162:165], v[66:81]
	v_mfma_f32_32x32x16_f16 v[50:65], v[138:141], v[166:169], v[50:65]
	v_mfma_f32_32x32x16_f16 v[34:49], v[142:145], v[158:161], v[34:49]
	v_mfma_f32_32x32x16_f16 v[18:33], v[142:145], v[162:165], v[18:33]
	ds_read_b128 v[134:137], v115
	ds_read_b128 v[138:141], v115 offset:4096
	ds_read_b128 v[158:161], v125
	ds_read_b128 v[162:165], v126
	ds_read_b128 v[170:173], v127
	v_mfma_f32_32x32x16_f16 v[2:17], v[142:145], v[166:169], v[2:17]
	s_waitcnt lgkmcnt(0)
	v_mfma_f32_32x32x16_f16 v[82:97], v[134:137], v[158:161], v[82:97]
	v_mfma_f32_32x32x16_f16 v[66:81], v[134:137], v[162:165], v[66:81]
	v_mfma_f32_32x32x16_f16 v[50:65], v[134:137], v[170:173], v[50:65]
	v_mfma_f32_32x32x16_f16 v[34:49], v[138:141], v[158:161], v[34:49]
	v_mfma_f32_32x32x16_f16 v[18:33], v[138:141], v[162:165], v[18:33]
	v_mfma_f32_32x32x16_f16 v[2:17], v[138:141], v[170:173], v[2:17]
	s_mov_b64 s[34:35], 0x500
	s_mov_b32 m0, s24
	v_lshl_add_u64 v[134:135], v[98:99], 0, s[34:35]
	s_waitcnt vmcnt(0)
	s_waitcnt vmcnt(0)
	s_barrier
	global_load_lds_dwordx4 v[134:135], off
	v_lshl_add_u64 v[134:135], v[100:101], 0, s[34:35]
	s_mov_b32 m0, s16
	s_nop 0
	global_load_lds_dwordx4 v[134:135], off
	v_lshl_add_u64 v[134:135], v[102:103], 0, s[34:35]
	s_mov_b32 m0, s17
	s_nop 0
	global_load_lds_dwordx4 v[134:135], off
	v_lshl_add_u64 v[134:135], v[104:105], 0, s[34:35]
	s_mov_b32 m0, s18
	s_nop 0
	global_load_lds_dwordx4 v[134:135], off
	v_lshl_add_u64 v[134:135], v[106:107], 0, s[34:35]
	s_mov_b32 m0, s19
	s_nop 0
	global_load_lds_dwordx4 v[134:135], off
	v_lshl_add_u64 v[134:135], v[108:109], 0, s[34:35]
	s_mov_b32 m0, s21
	s_nop 0
	global_load_lds_dwordx4 v[134:135], off
	v_lshl_add_u64 v[134:135], v[110:111], 0, s[34:35]
	s_mov_b32 m0, s22
	s_nop 0
	global_load_lds_dwordx4 v[134:135], off
	ds_read_b128 v[134:137], v112 offset:32768
	ds_read_b128 v[138:141], v129
	ds_read_b128 v[142:145], v112 offset:36864
	ds_read_b128 v[158:161], v130
	ds_read_b128 v[162:165], v131
	ds_read_b128 v[166:169], v128
	s_waitcnt lgkmcnt(0)
	v_mfma_f32_32x32x16_f16 v[82:97], v[134:137], v[138:141], v[82:97]
	v_mfma_f32_32x32x16_f16 v[66:81], v[134:137], v[158:161], v[66:81]
	v_mfma_f32_32x32x16_f16 v[50:65], v[134:137], v[162:165], v[50:65]
	v_mfma_f32_32x32x16_f16 v[34:49], v[142:145], v[138:141], v[34:49]
	v_mfma_f32_32x32x16_f16 v[18:33], v[142:145], v[158:161], v[18:33]
	ds_read_b128 v[134:137], v113 offset:32768
	ds_read_b128 v[138:141], v113 offset:36864
	ds_read_b128 v[158:161], v128 offset:4096
	ds_read_b128 v[170:173], v128 offset:8192
	v_mfma_f32_32x32x16_f16 v[2:17], v[142:145], v[162:165], v[2:17]
	s_waitcnt lgkmcnt(0)
	v_mfma_f32_32x32x16_f16 v[82:97], v[134:137], v[166:169], v[82:97]
	v_mfma_f32_32x32x16_f16 v[66:81], v[134:137], v[158:161], v[66:81]
	v_mfma_f32_32x32x16_f16 v[50:65], v[134:137], v[170:173], v[50:65]
	v_mfma_f32_32x32x16_f16 v[34:49], v[138:141], v[166:169], v[34:49]
	v_mfma_f32_32x32x16_f16 v[18:33], v[138:141], v[158:161], v[18:33]
	ds_read_b128 v[134:137], v114 offset:32768
	ds_read_b128 v[142:145], v114 offset:36864
	ds_read_b128 v[158:161], v132
	ds_read_b128 v[162:165], v132 offset:4096
	ds_read_b128 v[166:169], v132 offset:8192
	v_mfma_f32_32x32x16_f16 v[2:17], v[138:141], v[170:173], v[2:17]
	s_waitcnt lgkmcnt(0)
	v_mfma_f32_32x32x16_f16 v[82:97], v[134:137], v[158:161], v[82:97]
	v_mfma_f32_32x32x16_f16 v[66:81], v[134:137], v[162:165], v[66:81]
	v_mfma_f32_32x32x16_f16 v[50:65], v[134:137], v[166:169], v[50:65]
	v_mfma_f32_32x32x16_f16 v[34:49], v[142:145], v[158:161], v[34:49]
	v_mfma_f32_32x32x16_f16 v[18:33], v[142:145], v[162:165], v[18:33]
	ds_read_b128 v[134:137], v115 offset:32768
	ds_read_b128 v[138:141], v115 offset:36864
	ds_read_b128 v[158:161], v133
	ds_read_b128 v[162:165], v133 offset:4096
	ds_read_b128 v[170:173], v133 offset:8192
	v_mfma_f32_32x32x16_f16 v[2:17], v[142:145], v[166:169], v[2:17]
	s_waitcnt lgkmcnt(0)
	v_mfma_f32_32x32x16_f16 v[82:97], v[134:137], v[158:161], v[82:97]
	v_mfma_f32_32x32x16_f16 v[66:81], v[134:137], v[162:165], v[66:81]
	v_mfma_f32_32x32x16_f16 v[50:65], v[134:137], v[170:173], v[50:65]
	v_mfma_f32_32x32x16_f16 v[34:49], v[138:141], v[158:161], v[34:49]
	v_mfma_f32_32x32x16_f16 v[18:33], v[138:141], v[162:165], v[18:33]
	v_mfma_f32_32x32x16_f16 v[2:17], v[138:141], v[170:173], v[2:17]
	s_mov_b64 s[16:17], 0x580
	s_mov_b32 m0, s30
	v_lshl_add_u64 v[98:99], v[98:99], 0, s[16:17]
	s_waitcnt vmcnt(0)
	s_waitcnt vmcnt(0)
	s_barrier
	global_load_lds_dwordx4 v[98:99], off
	v_lshl_add_u64 v[98:99], v[100:101], 0, s[16:17]
	s_mov_b32 m0, s23
	s_nop 0
	global_load_lds_dwordx4 v[98:99], off
	v_lshl_add_u64 v[98:99], v[102:103], 0, s[16:17]
	s_mov_b32 m0, s25
	s_nop 0
	global_load_lds_dwordx4 v[98:99], off
	v_lshl_add_u64 v[98:99], v[104:105], 0, s[16:17]
	s_mov_b32 m0, s26
	s_nop 0
	global_load_lds_dwordx4 v[98:99], off
	v_lshl_add_u64 v[98:99], v[106:107], 0, s[16:17]
	s_mov_b32 m0, s27
	s_nop 0
	global_load_lds_dwordx4 v[98:99], off
	v_lshl_add_u64 v[98:99], v[108:109], 0, s[16:17]
	s_mov_b32 m0, s28
	s_nop 0
	global_load_lds_dwordx4 v[98:99], off
	v_lshl_add_u64 v[98:99], v[110:111], 0, s[16:17]
	s_mov_b32 m0, s29
	s_nop 0
	global_load_lds_dwordx4 v[98:99], off
	ds_read_b128 v[98:101], v112
	ds_read_b128 v[102:105], v116
	ds_read_b128 v[106:109], v112 offset:4096
	ds_read_b128 v[134:137], v117
	ds_read_b128 v[138:141], v118
	ds_read_b128 v[142:145], v113
	s_waitcnt lgkmcnt(0)
	v_mfma_f32_32x32x16_f16 v[82:97], v[98:101], v[102:105], v[82:97]
	v_mfma_f32_32x32x16_f16 v[66:81], v[98:101], v[134:137], v[66:81]
	v_mfma_f32_32x32x16_f16 v[50:65], v[98:101], v[138:141], v[50:65]
	v_mfma_f32_32x32x16_f16 v[34:49], v[106:109], v[102:105], v[34:49]
	v_mfma_f32_32x32x16_f16 v[18:33], v[106:109], v[134:137], v[18:33]
	ds_read_b128 v[98:101], v113 offset:4096
	ds_read_b128 v[102:105], v119
	ds_read_b128 v[116:119], v120
	ds_read_b128 v[134:137], v121
	v_mfma_f32_32x32x16_f16 v[2:17], v[106:109], v[138:141], v[2:17]
	s_waitcnt lgkmcnt(0)
	v_mfma_f32_32x32x16_f16 v[82:97], v[142:145], v[102:105], v[82:97]
	v_mfma_f32_32x32x16_f16 v[66:81], v[142:145], v[116:119], v[66:81]
	v_mfma_f32_32x32x16_f16 v[50:65], v[142:145], v[134:137], v[50:65]
	v_mfma_f32_32x32x16_f16 v[34:49], v[98:101], v[102:105], v[34:49]
	v_mfma_f32_32x32x16_f16 v[18:33], v[98:101], v[116:119], v[18:33]
	ds_read_b128 v[102:105], v114
	ds_read_b128 v[106:109], v114 offset:4096
	ds_read_b128 v[116:119], v122
	ds_read_b128 v[120:123], v123
	ds_read_b128 v[138:141], v124
	v_mfma_f32_32x32x16_f16 v[2:17], v[98:101], v[134:137], v[2:17]
	s_waitcnt lgkmcnt(0)
	v_mfma_f32_32x32x16_f16 v[82:97], v[102:105], v[116:119], v[82:97]
	v_mfma_f32_32x32x16_f16 v[66:81], v[102:105], v[120:123], v[66:81]
	v_mfma_f32_32x32x16_f16 v[50:65], v[102:105], v[138:141], v[50:65]
	v_mfma_f32_32x32x16_f16 v[34:49], v[106:109], v[116:119], v[34:49]
	v_mfma_f32_32x32x16_f16 v[18:33], v[106:109], v[120:123], v[18:33]
	ds_read_b128 v[98:101], v115
	ds_read_b128 v[102:105], v115 offset:4096
	ds_read_b128 v[116:119], v125
	ds_read_b128 v[120:123], v126
	ds_read_b128 v[124:127], v127
	v_mfma_f32_32x32x16_f16 v[2:17], v[106:109], v[138:141], v[2:17]
	s_waitcnt lgkmcnt(0)
	v_mfma_f32_32x32x16_f16 v[82:97], v[98:101], v[116:119], v[82:97]
	v_mfma_f32_32x32x16_f16 v[66:81], v[98:101], v[120:123], v[66:81]
	v_mfma_f32_32x32x16_f16 v[50:65], v[98:101], v[124:127], v[50:65]
	v_mfma_f32_32x32x16_f16 v[34:49], v[102:105], v[116:119], v[34:49]
	v_mfma_f32_32x32x16_f16 v[18:33], v[102:105], v[120:123], v[18:33]
	v_mfma_f32_32x32x16_f16 v[2:17], v[102:105], v[124:127], v[2:17]
	s_waitcnt vmcnt(0)
	s_waitcnt vmcnt(0)
	s_barrier
	ds_read_b128 v[98:101], v112 offset:32768
	ds_read_b128 v[102:105], v129
	ds_read_b128 v[106:109], v112 offset:36864
	ds_read_b128 v[116:119], v130
	ds_read_b128 v[120:123], v131
	ds_read_b128 v[124:127], v128
	s_waitcnt lgkmcnt(4)
	v_mfma_f32_32x32x16_f16 v[82:97], v[98:101], v[102:105], v[82:97]
	s_waitcnt lgkmcnt(2)
	v_mfma_f32_32x32x16_f16 v[66:81], v[98:101], v[116:119], v[66:81]
	s_waitcnt lgkmcnt(1)
	v_mfma_f32_32x32x16_f16 v[50:65], v[98:101], v[120:123], v[50:65]
	v_mfma_f32_32x32x16_f16 v[34:49], v[106:109], v[102:105], v[34:49]
	v_mfma_f32_32x32x16_f16 v[18:33], v[106:109], v[116:119], v[18:33]
	ds_read_b128 v[98:101], v113 offset:32768
	ds_read_b128 v[102:105], v113 offset:36864
	ds_read_b128 v[110:113], v128 offset:4096
	ds_read_b128 v[116:119], v128 offset:8192
	v_mfma_f32_32x32x16_f16 v[2:17], v[106:109], v[120:123], v[2:17]
	s_waitcnt lgkmcnt(3)
	v_mfma_f32_32x32x16_f16 v[82:97], v[98:101], v[124:127], v[82:97]
	s_waitcnt lgkmcnt(1)
	v_mfma_f32_32x32x16_f16 v[66:81], v[98:101], v[110:113], v[66:81]
	s_waitcnt lgkmcnt(0)
	v_mfma_f32_32x32x16_f16 v[50:65], v[98:101], v[116:119], v[50:65]
	v_mfma_f32_32x32x16_f16 v[34:49], v[102:105], v[124:127], v[34:49]
	v_mfma_f32_32x32x16_f16 v[18:33], v[102:105], v[110:113], v[18:33]
	ds_read_b128 v[98:101], v114 offset:32768
	ds_read_b128 v[106:109], v114 offset:36864
	ds_read_b128 v[110:113], v132
	ds_read_b128 v[120:123], v132 offset:4096
	ds_read_b128 v[124:127], v132 offset:8192
	v_mfma_f32_32x32x16_f16 v[2:17], v[102:105], v[116:119], v[2:17]
	s_waitcnt lgkmcnt(2)
	v_mfma_f32_32x32x16_f16 v[82:97], v[98:101], v[110:113], v[82:97]
	s_waitcnt lgkmcnt(1)
	v_mfma_f32_32x32x16_f16 v[66:81], v[98:101], v[120:123], v[66:81]
	s_waitcnt lgkmcnt(0)
	v_mfma_f32_32x32x16_f16 v[50:65], v[98:101], v[124:127], v[50:65]
	v_mfma_f32_32x32x16_f16 v[34:49], v[106:109], v[110:113], v[34:49]
	v_mfma_f32_32x32x16_f16 v[18:33], v[106:109], v[120:123], v[18:33]
	ds_read_b128 v[98:101], v115 offset:32768
	ds_read_b128 v[102:105], v115 offset:36864
	ds_read_b128 v[110:113], v133
	ds_read_b128 v[114:117], v133 offset:4096
	ds_read_b128 v[118:121], v133 offset:8192
	v_mfma_f32_32x32x16_f16 v[2:17], v[106:109], v[124:127], v[2:17]
	s_waitcnt lgkmcnt(2)
	v_mfma_f32_32x32x16_f16 v[82:97], v[98:101], v[110:113], v[82:97]
	s_waitcnt lgkmcnt(1)
	v_mfma_f32_32x32x16_f16 v[66:81], v[98:101], v[114:117], v[66:81]
	s_waitcnt lgkmcnt(0)
	v_mfma_f32_32x32x16_f16 v[50:65], v[98:101], v[118:121], v[50:65]
	v_mfma_f32_32x32x16_f16 v[34:49], v[102:105], v[110:113], v[34:49]
	v_mfma_f32_32x32x16_f16 v[18:33], v[102:105], v[114:117], v[18:33]
	v_mfma_f32_32x32x16_f16 v[2:17], v[102:105], v[118:121], v[2:17]
	v_add_u32_e32 v158, s20, v151
	v_and_b32_e32 v154, 32, v0
	v_mov_b32_e32 v155, v147
	v_lshl_add_u64 v[98:99], s[6:7], 0, v[154:155]
	v_or_b32_e32 v100, v158, v156
	v_lshlrev_b32_e32 v146, 2, v158
	v_lshlrev_b32_e32 v100, 2, v100
	v_lshl_add_u64 v[102:103], v[98:99], 0, v[146:147]
	s_waitcnt vmcnt(0)
	s_barrier
	global_load_dwordx4 v[138:141], v[102:103], off offset:16
	global_load_dwordx4 v[134:137], v[102:103], off offset:64
	global_load_dwordx4 v[130:133], v[102:103], off offset:80
	global_load_dwordx4 v[126:129], v[102:103], off offset:128
	global_load_dwordx4 v[122:125], v[102:103], off offset:144
	global_load_dwordx4 v[118:121], v[102:103], off offset:192
	global_load_dword v152, v100, s[6:7]
	global_load_dwordx4 v[142:145], v[102:103], off
	global_load_dword v150, v100, s[6:7] offset:128
	global_load_dword v148, v100, s[6:7] offset:256
	global_load_dwordx4 v[114:117], v[102:103], off offset:208
	global_load_dwordx4 v[110:113], v[102:103], off offset:256
	s_nop 0
	global_load_dwordx4 v[98:101], v[102:103], off offset:336
	global_load_dwordx4 v[106:109], v[102:103], off offset:272
	s_nop 0
	global_load_dwordx4 v[102:105], v[102:103], off offset:320
	v_mul_u32_u24_e32 v146, 0x1200, v149
	v_mov_b32_e32 v155, 0x1c0
	s_movk_i32 s18, 0x1200
	v_lshl_or_b32 v146, v156, 2, v146
	s_bfe_u32 s6, s3, 0x30009
	v_bitop3_b32 v155, s3, v155, v157 bitop3:0xc8
	v_mul_u32_u24_e32 v156, 0x90, v156
	s_movk_i32 s3, 0x240
	v_mad_u32_u24 v156, v149, s18, v156
	v_mad_u32_u24 v149, v153, s3, v146
	v_mul_u32_u24_e64 v157, s6, 12
	s_cmpk_gt_u32 s2, 0x7f
	ds_write2_b32 v149, v82, v83 offset1:36
	ds_write2_b32 v149, v84, v85 offset0:72 offset1:108
	v_add_u32_e32 v153, 0x400, v149
	v_lshrrev_b32_e32 v83, 6, v158
	s_cselect_b64 s[16:17], -1, 0
	s_and_b64 s[6:7], s[4:5], exec
	ds_write2_b32 v153, v86, v87 offset0:32 offset1:68
	ds_write2_b32 v153, v88, v89 offset0:104 offset1:140
	v_add_u32_e32 v86, 0x800, v149
	v_and_b32_e32 v89, 32, v151
	v_add_lshl_u32 v146, v83, v157, 15
	s_cselect_b32 s7, s11, s13
	s_cselect_b32 s6, s10, s12
	v_mov_b32_e32 v159, 0x3e000000
	ds_write2_b32 v86, v90, v91 offset0:64 offset1:100
	ds_write2_b32 v86, v92, v93 offset0:136 offset1:172
	v_add_u32_e32 v82, 0xc00, v149
	s_mov_b64 s[10:11], -1
	s_and_b64 vcc, exec, s[16:17]
	v_lshl_add_u64 v[84:85], v[146:147], 1, s[14:15]
	v_lshlrev_b32_e32 v83, 1, v89
	v_lshlrev_b32_e32 v91, 3, v155
	ds_write2_b32 v82, v94, v95 offset0:96 offset1:132
	ds_write2_b32 v82, v96, v97 offset0:168 offset1:204
	s_cbranch_vccz .LBB11_3
	ds_read2_b32 v[92:93], v149 offset1:36
	ds_read2_b32 v[94:95], v149 offset0:72 offset1:108
	ds_read2_b32 v[96:97], v153 offset0:32 offset1:68
	ds_read2_b32 v[160:161], v153 offset0:104 offset1:140
	s_mov_b64 s[10:11], 0
	s_waitcnt vmcnt(8) lgkmcnt(3)
	v_add_f32_e32 v87, v152, v92
	v_cvt_f16_f32_e32 v87, v87
	v_mov_b32_e32 v92, v93
	s_waitcnt lgkmcnt(2)
	v_mov_b32_e32 v93, v94
	v_mov_b32_e32 v94, v95
	v_pk_add_f32 v[92:93], v[152:153], v[92:93] op_sel_hi:[0,1]
	s_waitcnt lgkmcnt(1)
	v_mov_b32_e32 v95, v96
	v_cvt_pk_f16_f32 v88, v92, v93
	v_pk_add_f32 v[94:95], v[152:153], v[94:95] op_sel_hi:[0,1]
	v_pack_b32_f16 v92, v87, v88
	v_cvt_pk_f16_f32 v87, v94, v95
	v_mov_b32_e32 v94, v97
	s_waitcnt lgkmcnt(0)
	v_mov_b32_e32 v95, v160
	v_alignbit_b32 v93, v87, v88, 16
	v_add_f32_e32 v88, v152, v161
	v_pk_add_f32 v[94:95], v[152:153], v[94:95] op_sel_hi:[0,1]
	v_cvt_f16_f32_e32 v88, v88
	v_cvt_pk_f16_f32 v90, v94, v95
	ds_read2_b32 v[160:161], v86 offset0:64 offset1:100
	v_alignbit_b32 v94, v90, v87, 16
	v_or3_b32 v87, v83, v91, v1
	v_lshlrev_b32_e32 v96, 4, v87
	ds_read2_b32 v[86:87], v86 offset0:136 offset1:172
	v_mov_b32_e32 v97, v147
	v_alignbit_b32 v95, v88, v90, 16
	v_lshl_add_u64 v[162:163], v[84:85], 0, v[96:97]
	global_store_dwordx4 v[162:163], v[92:95], off
	s_waitcnt lgkmcnt(1)
	v_add_f32_e32 v88, v152, v160
	ds_read2_b32 v[94:95], v82 offset0:96 offset1:132
	v_mov_b32_e32 v92, v161
	ds_read2_b32 v[160:161], v82 offset0:168 offset1:204
	v_cvt_f16_f32_e32 v88, v88
	s_waitcnt lgkmcnt(2)
	v_mov_b32_e32 v93, v86
	v_pk_add_f32 v[92:93], v[152:153], v[92:93] op_sel_hi:[0,1]
	v_cvt_pk_f16_f32 v90, v92, v93
	v_pack_b32_f16 v92, v88, v90
	v_mov_b32_e32 v86, v87
	s_waitcnt lgkmcnt(1)
	v_mov_b32_e32 v87, v94
	s_waitcnt lgkmcnt(0)
	v_add_f32_e32 v88, v152, v161
	v_pk_add_f32 v[86:87], v[152:153], v[86:87] op_sel_hi:[0,1]
	v_cvt_f16_f32_e32 v88, v88
	v_cvt_pk_f16_f32 v82, v86, v87
	v_mov_b32_e32 v86, v95
	v_mov_b32_e32 v87, v160
	v_pk_add_f32 v[86:87], v[152:153], v[86:87] op_sel_hi:[0,1]
	v_cvt_pk_f16_f32 v86, v86, v87
	v_alignbit_b32 v94, v86, v82, 16
	v_alignbit_b32 v95, v88, v86, 16
	v_or_b32_e32 v86, 0x800, v96
	v_mov_b32_e32 v87, v147
	v_alignbit_b32 v93, v82, v90, 16
	v_lshl_add_u64 v[86:87], v[84:85], 0, v[86:87]
	global_store_dwordx4 v[86:87], v[92:95], off

.LBB11_38:
	s_endpgm
	s_nop 0
	s_nop 0
	s_nop 0
	s_nop 0
	s_nop 0
	s_nop 0
	s_nop 0
	s_nop 0
	s_nop 0
	s_nop 0
	s_nop 0
	s_nop 0
	s_nop 0
	s_nop 0
	s_nop 0
	s_nop 0
	s_nop 0
	s_nop 0
	s_nop 0
	s_nop 0
	s_nop 0
	s_nop 0
	s_nop 0
	s_nop 0
	s_nop 0
	s_nop 0
	s_nop 0
	s_nop 0
	s_nop 0
	s_nop 0
	s_nop 0
	s_nop 0
	s_nop 0
	s_nop 0
	s_nop 0
	s_nop 0
	s_nop 0
	s_nop 0
	s_nop 0
	s_nop 0
	s_nop 0
	s_nop 0
	s_nop 0
	s_nop 0
	s_nop 0
	s_nop 0
	s_nop 0
	s_nop 0
	s_nop 0
	s_nop 0
	s_nop 0
	s_nop 0
	s_nop 0
	s_nop 0
	s_nop 0
	s_nop 0
	s_nop 0
	s_nop 0
	s_endpgm

	.amdhsa_kernel _Z7gemm2_kILi0ELi3ELi1EEv5GArgs
		.amdhsa_group_segment_fixed_size 114688
		.amdhsa_private_segment_fixed_size 0
		.amdhsa_kernarg_size 136
		.amdhsa_user_sgpr_count 2
		.amdhsa_user_sgpr_dispatch_ptr 0
		.amdhsa_user_sgpr_queue_ptr 0
		.amdhsa_user_sgpr_kernarg_segment_ptr 1
		.amdhsa_user_sgpr_dispatch_id 0
		.amdhsa_user_sgpr_kernarg_preload_length 0
		.amdhsa_user_sgpr_kernarg_preload_offset 0
		.amdhsa_user_sgpr_private_segment_size 0
		.amdhsa_uses_dynamic_stack 0
		.amdhsa_enable_private_segment 0
		.amdhsa_system_sgpr_workgroup_id_x 1
		.amdhsa_system_sgpr_workgroup_id_y 0
		.amdhsa_system_sgpr_workgroup_id_z 0
		.amdhsa_system_sgpr_workgroup_info 0
		.amdhsa_system_vgpr_workitem_id 0
		.amdhsa_next_free_vgpr 193
		.amdhsa_next_free_sgpr 96
		.amdhsa_accum_offset 196
		.amdhsa_reserve_vcc 1
		.amdhsa_float_round_mode_32 0
		.amdhsa_float_round_mode_16_64 0
		.amdhsa_float_denorm_mode_32 3
		.amdhsa_float_denorm_mode_16_64 3
		.amdhsa_dx10_clamp 1
		.amdhsa_ieee_mode 1
		.amdhsa_fp16_overflow 0
		.amdhsa_tg_split 0
		.amdhsa_exception_fp_ieee_invalid_op 0
		.amdhsa_exception_fp_denorm_src 0
		.amdhsa_exception_fp_ieee_div_zero 0
		.amdhsa_exception_fp_ieee_overflow 0
		.amdhsa_exception_fp_ieee_underflow 0
		.amdhsa_exception_fp_ieee_inexact 0
		.amdhsa_exception_int_div_zero 0
	.end_amdhsa_kernel

_Z6gemm_kILi1ELi128ELi4ELi8EEv5GArgs:
	v_lshlrev_b32_e32 v176, 4, v0
	s_getpc_b64 s[92:93]
	s_add_u32 s92, s92, 0xffff2af8
	s_addc_u32 s93, s93, 0xffffffff
	global_load_dwordx4 v[172:175], v176, s[92:93]
	s_cmpk_lt_u32 s2, 0xc0
	s_mov_b64 s[4:5], -1
	s_cbranch_scc0 .LBB12_2
	s_load_dwordx4 s[4:7], s[0:1], 0x0
	v_lshrrev_b32_e32 v44, 6, v0
	s_lshl_b32 s3, s2, 7
	v_bfe_u32 v1, v0, 3, 3
	s_and_b32 s3, s3, 0xf80
	v_lshl_or_b32 v6, v44, 4, v1
	v_and_b32_e32 v2, 7, v0
	v_bitop3_b32 v4, v44, v2, 1 bitop3:0x6c
	v_or_b32_e32 v2, s3, v6
	v_mul_u32_u24_e32 v2, 0x340, v2
	v_bfe_u32 v5, v0, 4, 2
	v_lshlrev_b32_e32 v34, 1, v2
	v_mov_b32_e32 v35, 0
	v_xor_b32_e32 v5, v4, v5
	s_waitcnt lgkmcnt(0)
	v_lshl_add_u64 v[2:3], s[4:5], 0, v[34:35]
	v_lshlrev_b32_e32 v34, 4, v5
	v_or_b32_e32 v7, 8, v6
	v_lshl_add_u64 v[36:37], v[2:3], 0, v[34:35]
	v_or_b32_e32 v2, s3, v7
	v_bfe_u32 v5, v7, 1, 3
	s_lshl_b32 s8, s2, 2
	v_mul_u32_u24_e32 v2, 0x340, v2
	v_mov_b32_e32 v3, v35
	v_xor_b32_e32 v4, v4, v5
	v_lshl_add_u64 v[2:3], v[2:3], 1, s[4:5]
	v_lshlrev_b32_e32 v4, 4, v4
	v_mov_b32_e32 v5, v35
	s_and_b32 s10, s8, 0x380
	v_lshl_add_u64 v[38:39], v[2:3], 0, v[4:5]
	v_or_b32_e32 v2, s10, v6
	v_mul_u32_u24_e32 v2, 0x680, v2
	v_mov_b32_e32 v3, v35
	v_lshl_add_u64 v[2:3], s[6:7], 0, v[2:3]
	v_lshl_add_u64 v[40:41], v[2:3], 0, v[34:35]
	v_or_b32_e32 v2, s10, v7
	v_mul_u32_u24_e32 v34, 0x680, v2
	v_lshl_add_u64 v[2:3], s[6:7], 0, v[34:35]
	v_lshl_add_u64 v[42:43], v[2:3], 0, v[4:5]
	v_lshlrev_b32_e32 v4, 11, v44
	v_or_b32_e32 v2, 0x400, v4
	v_readfirstlane_b32 s19, v4
	s_mov_b32 m0, s19
	v_readfirstlane_b32 s20, v2
	v_or_b32_e32 v2, 0x10000, v4
	global_load_lds_dwordx4 v[36:37], off
	s_mov_b32 m0, s20
	v_readfirstlane_b32 s21, v2
	v_or_b32_e32 v2, 0x10400, v4
	global_load_lds_dwordx4 v[38:39], off
	s_mov_b32 m0, s21
	v_readfirstlane_b32 s22, v2
	v_or_b32_e32 v5, 0x4000, v4
	global_load_lds_dwordx4 v[40:41], off
	s_mov_b32 m0, s22
	s_mov_b64 s[4:5], 0x80
	v_readfirstlane_b32 s15, v5
	v_or_b32_e32 v5, 0x4400, v4
	global_load_lds_dwordx4 v[42:43], off
	v_lshl_add_u64 v[2:3], v[36:37], 0, s[4:5]
	s_mov_b32 m0, s15
	v_readfirstlane_b32 s16, v5
	v_or_b32_e32 v5, 0x14000, v4
	global_load_lds_dwordx4 v[2:3], off
	v_lshl_add_u64 v[2:3], v[38:39], 0, s[4:5]
	s_mov_b32 m0, s16
	v_readfirstlane_b32 s17, v5
	v_or_b32_e32 v5, 0x14400, v4
	global_load_lds_dwordx4 v[2:3], off
	v_lshl_add_u64 v[2:3], v[40:41], 0, s[4:5]
	s_mov_b32 m0, s17
	v_readfirstlane_b32 s18, v5
	v_or_b32_e32 v5, 0x8000, v4
	global_load_lds_dwordx4 v[2:3], off
	v_lshl_add_u64 v[2:3], v[42:43], 0, s[4:5]
	s_mov_b32 m0, s18
	s_mov_b64 s[4:5], 0x100
	v_readfirstlane_b32 s11, v5
	v_or_b32_e32 v5, 0x8400, v4
	global_load_lds_dwordx4 v[2:3], off
	v_lshl_add_u64 v[2:3], v[36:37], 0, s[4:5]
	s_mov_b32 m0, s11
	v_readfirstlane_b32 s12, v5
	v_or_b32_e32 v5, 0x18000, v4
	global_load_lds_dwordx4 v[2:3], off
	v_lshl_add_u64 v[2:3], v[38:39], 0, s[4:5]
	s_mov_b32 m0, s12
	v_readfirstlane_b32 s13, v5
	v_or_b32_e32 v5, 0x18400, v4
	global_load_lds_dwordx4 v[2:3], off
	v_lshl_add_u64 v[2:3], v[40:41], 0, s[4:5]
	s_mov_b32 m0, s13
	v_readfirstlane_b32 s14, v5
	v_or_b32_e32 v5, 0xc000, v4
	global_load_lds_dwordx4 v[2:3], off
	v_lshl_add_u64 v[2:3], v[42:43], 0, s[4:5]
	s_mov_b32 m0, s14
	s_mov_b64 s[4:5], 0x180
	v_readfirstlane_b32 s25, v5
	v_or_b32_e32 v5, 0xc400, v4
	global_load_lds_dwordx4 v[2:3], off
	v_lshl_add_u64 v[2:3], v[36:37], 0, s[4:5]
	s_mov_b32 m0, s25
	v_readfirstlane_b32 s23, v5
	v_or_b32_e32 v5, 0x1c000, v4
	s_waitcnt vmcnt(8)
	s_waitcnt vmcnt(0) lgkmcnt(0)
	s_barrier
	global_load_lds_dwordx4 v[2:3], off
	v_lshl_add_u64 v[2:3], v[38:39], 0, s[4:5]
	s_mov_b32 m0, s23
	v_readfirstlane_b32 s24, v5
	v_or_b32_e32 v4, 0x1c400, v4
	global_load_lds_dwordx4 v[2:3], off
	v_lshl_add_u64 v[2:3], v[40:41], 0, s[4:5]
	s_mov_b32 m0, s24
	v_readfirstlane_b32 s26, v4
	global_load_lds_dwordx4 v[2:3], off
	v_lshl_add_u64 v[2:3], v[42:43], 0, s[4:5]
	s_mov_b32 m0, s26
	v_bfe_u32 v46, v0, 5, 1
	global_load_lds_dwordx4 v[2:3], off
	v_lshrrev_b32_e32 v2, 1, v0
	v_bfe_u32 v3, v0, 4, 1
	v_bitop3_b32 v2, v2, v3, 7 bitop3:0x6c
	v_or_b32_e32 v3, 6, v46
	s_load_dwordx2 s[8:9], s[0:1], 0x18
	s_load_dwordx2 s[6:7], s[0:1], 0x30
	s_load_dwordx2 s[4:5], s[0:1], 0x48
	v_xor_b32_e32 v3, v2, v3
	v_lshlrev_b32_e32 v72, 4, v3
	v_or_b32_e32 v3, 4, v46
	v_xor_b32_e32 v3, v2, v3
	v_lshlrev_b32_e32 v62, 4, v3
	v_or_b32_e32 v3, 2, v46
	v_and_b32_e32 v47, 31, v0
	v_xor_b32_e32 v3, v2, v3
	v_xor_b32_e32 v2, v2, v46
	v_bfe_u32 v45, v0, 6, 2
	v_lshrrev_b32_e32 v34, 8, v0
	s_mov_b32 s27, 0x10000
	v_lshlrev_b32_e32 v50, 7, v47
	v_lshlrev_b32_e32 v6, 4, v2
	v_lshlrev_b32_e32 v2, 12, v45
	v_lshlrev_b32_e32 v68, 13, v34
	v_lshlrev_b32_e32 v52, 4, v3
	v_or3_b32 v73, v2, v50, s27
	v_or3_b32 v49, v6, v68, v50
	ds_read_b128 v[2:5], v49
	v_or_b32_e32 v51, v73, v6
	ds_read_b128 v[6:9], v51
	v_or_b32_e32 v14, v52, v68
	v_add_u32_e32 v48, v14, v50
	ds_read_b128 v[54:57], v48
	v_or_b32_e32 v53, v73, v52
	ds_read_b128 v[10:13], v49 offset:4096
	ds_read_b128 v[58:61], v53
	s_waitcnt lgkmcnt(0)
	v_mfma_f32_32x32x16_f16 v[18:33], v[2:5], v[6:9], 0
	v_or_b32_e32 v52, v62, v68
	v_add_u32_e32 v52, v52, v50
	v_mfma_f32_32x32x16_f16 v[18:33], v[54:57], v[58:61], v[18:33]
	ds_read_b128 v[54:57], v48 offset:4096
	v_mfma_f32_32x32x16_f16 v[2:17], v[10:13], v[6:9], 0
	s_waitcnt lgkmcnt(0)
	v_mfma_f32_32x32x16_f16 v[2:17], v[54:57], v[58:61], v[2:17]
	ds_read_b128 v[56:59], v52
	v_or_b32_e32 v54, v73, v62
	ds_read_b128 v[60:63], v54
	ds_read_b128 v[64:67], v52 offset:4096
	v_or_b32_e32 v55, v72, v68
	v_add_u32_e32 v50, v55, v50
	ds_read_b128 v[68:71], v50
	v_or_b32_e32 v55, v73, v72
	s_waitcnt lgkmcnt(0)
	v_mfma_f32_32x32x16_f16 v[18:33], v[56:59], v[60:63], v[18:33]
	ds_read_b128 v[56:59], v55
	v_mfma_f32_32x32x16_f16 v[2:17], v[64:67], v[60:63], v[2:17]
	ds_read_b128 v[60:63], v50 offset:4096
	s_waitcnt lgkmcnt(0)
	v_mfma_f32_32x32x16_f16 v[18:33], v[68:71], v[56:59], v[18:33]
	v_mfma_f32_32x32x16_f16 v[2:17], v[60:63], v[56:59], v[2:17]
	s_mov_b64 s[28:29], 0x200
	s_mov_b32 m0, s19
	v_lshl_add_u64 v[56:57], v[36:37], 0, s[28:29]
	s_waitcnt vmcnt(8)
	s_barrier
	global_load_lds_dwordx4 v[56:57], off
	v_lshl_add_u64 v[56:57], v[38:39], 0, s[28:29]
	s_mov_b32 m0, s20
	s_nop 0
	global_load_lds_dwordx4 v[56:57], off
	v_lshl_add_u64 v[56:57], v[40:41], 0, s[28:29]
	s_mov_b32 m0, s21
	s_nop 0
	global_load_lds_dwordx4 v[56:57], off
	v_lshl_add_u64 v[56:57], v[42:43], 0, s[28:29]
	s_mov_b32 m0, s22
	s_nop 0
	global_load_lds_dwordx4 v[56:57], off
	ds_read_b128 v[56:59], v49 offset:16384
	ds_read_b128 v[60:63], v51 offset:16384
	ds_read_b128 v[64:67], v49 offset:20480
	ds_read_b128 v[68:71], v48 offset:16384
	s_waitcnt lgkmcnt(0)
	v_mfma_f32_32x32x16_f16 v[18:33], v[56:59], v[60:63], v[18:33]
	ds_read_b128 v[56:59], v53 offset:16384
	v_mfma_f32_32x32x16_f16 v[2:17], v[64:67], v[60:63], v[2:17]
	ds_read_b128 v[60:63], v48 offset:20480
	s_waitcnt lgkmcnt(0)
	v_mfma_f32_32x32x16_f16 v[18:33], v[68:71], v[56:59], v[18:33]
	v_mfma_f32_32x32x16_f16 v[2:17], v[60:63], v[56:59], v[2:17]
	ds_read_b128 v[56:59], v52 offset:16384
	ds_read_b128 v[60:63], v54 offset:16384
	ds_read_b128 v[64:67], v52 offset:20480
	ds_read_b128 v[68:71], v50 offset:16384
	s_waitcnt lgkmcnt(0)
	v_mfma_f32_32x32x16_f16 v[18:33], v[56:59], v[60:63], v[18:33]
	ds_read_b128 v[56:59], v55 offset:16384
	v_mfma_f32_32x32x16_f16 v[2:17], v[64:67], v[60:63], v[2:17]
	ds_read_b128 v[60:63], v50 offset:20480
	s_waitcnt lgkmcnt(0)
	v_mfma_f32_32x32x16_f16 v[18:33], v[68:71], v[56:59], v[18:33]
	v_mfma_f32_32x32x16_f16 v[2:17], v[60:63], v[56:59], v[2:17]
	s_mov_b64 s[28:29], 0x280
	s_mov_b32 m0, s15
	v_lshl_add_u64 v[56:57], v[36:37], 0, s[28:29]
	s_waitcnt vmcnt(8)
	s_barrier
	global_load_lds_dwordx4 v[56:57], off
	v_lshl_add_u64 v[56:57], v[38:39], 0, s[28:29]
	s_mov_b32 m0, s16
	s_nop 0
	global_load_lds_dwordx4 v[56:57], off
	v_lshl_add_u64 v[56:57], v[40:41], 0, s[28:29]
	s_mov_b32 m0, s17
	s_nop 0
	global_load_lds_dwordx4 v[56:57], off
	v_lshl_add_u64 v[56:57], v[42:43], 0, s[28:29]
	s_mov_b32 m0, s18
	s_nop 0
	global_load_lds_dwordx4 v[56:57], off
	ds_read_b128 v[56:59], v49 offset:32768
	ds_read_b128 v[60:63], v51 offset:32768
	ds_read_b128 v[64:67], v49 offset:36864
	ds_read_b128 v[68:71], v48 offset:32768
	s_waitcnt lgkmcnt(0)
	v_mfma_f32_32x32x16_f16 v[18:33], v[56:59], v[60:63], v[18:33]
	ds_read_b128 v[56:59], v53 offset:32768
	v_mfma_f32_32x32x16_f16 v[2:17], v[64:67], v[60:63], v[2:17]
	ds_read_b128 v[60:63], v48 offset:36864
	s_waitcnt lgkmcnt(0)
	v_mfma_f32_32x32x16_f16 v[18:33], v[68:71], v[56:59], v[18:33]
	v_mfma_f32_32x32x16_f16 v[2:17], v[60:63], v[56:59], v[2:17]
	ds_read_b128 v[56:59], v52 offset:32768
	ds_read_b128 v[60:63], v54 offset:32768
	ds_read_b128 v[64:67], v52 offset:36864
	ds_read_b128 v[68:71], v50 offset:32768
	s_waitcnt lgkmcnt(0)
	v_mfma_f32_32x32x16_f16 v[18:33], v[56:59], v[60:63], v[18:33]
	ds_read_b128 v[56:59], v55 offset:32768
	v_mfma_f32_32x32x16_f16 v[2:17], v[64:67], v[60:63], v[2:17]
	ds_read_b128 v[60:63], v50 offset:36864
	s_waitcnt lgkmcnt(0)
	v_mfma_f32_32x32x16_f16 v[18:33], v[68:71], v[56:59], v[18:33]
	v_mfma_f32_32x32x16_f16 v[2:17], v[60:63], v[56:59], v[2:17]
	s_mov_b64 s[28:29], 0x300
	s_mov_b32 m0, s11
	v_lshl_add_u64 v[56:57], v[36:37], 0, s[28:29]
	s_waitcnt vmcnt(8)
	s_barrier
	global_load_lds_dwordx4 v[56:57], off
	v_lshl_add_u64 v[56:57], v[38:39], 0, s[28:29]
	s_mov_b32 m0, s12
	s_nop 0
	global_load_lds_dwordx4 v[56:57], off
	v_lshl_add_u64 v[56:57], v[40:41], 0, s[28:29]
	s_mov_b32 m0, s13
	s_nop 0
	global_load_lds_dwordx4 v[56:57], off
	v_lshl_add_u64 v[56:57], v[42:43], 0, s[28:29]
	s_mov_b32 m0, s14
	s_nop 0
	global_load_lds_dwordx4 v[56:57], off
	ds_read_b128 v[56:59], v49 offset:49152
	ds_read_b128 v[60:63], v51 offset:49152
	ds_read_b128 v[64:67], v49 offset:53248
	ds_read_b128 v[68:71], v48 offset:49152
	s_waitcnt lgkmcnt(0)
	v_mfma_f32_32x32x16_f16 v[18:33], v[56:59], v[60:63], v[18:33]
	ds_read_b128 v[56:59], v53 offset:49152
	v_mfma_f32_32x32x16_f16 v[2:17], v[64:67], v[60:63], v[2:17]
	ds_read_b128 v[60:63], v48 offset:53248
	s_waitcnt lgkmcnt(0)
	v_mfma_f32_32x32x16_f16 v[18:33], v[68:71], v[56:59], v[18:33]
	v_mfma_f32_32x32x16_f16 v[2:17], v[60:63], v[56:59], v[2:17]
	ds_read_b128 v[56:59], v52 offset:49152
	ds_read_b128 v[60:63], v54 offset:49152
	ds_read_b128 v[64:67], v52 offset:53248
	ds_read_b128 v[68:71], v50 offset:49152
	s_waitcnt lgkmcnt(0)
	v_mfma_f32_32x32x16_f16 v[18:33], v[56:59], v[60:63], v[18:33]
	ds_read_b128 v[56:59], v55 offset:49152
	v_mfma_f32_32x32x16_f16 v[2:17], v[64:67], v[60:63], v[2:17]
	ds_read_b128 v[60:63], v50 offset:53248
	s_waitcnt lgkmcnt(0)
	v_mfma_f32_32x32x16_f16 v[18:33], v[68:71], v[56:59], v[18:33]
	v_mfma_f32_32x32x16_f16 v[2:17], v[60:63], v[56:59], v[2:17]
	s_mov_b64 s[28:29], 0x380
	s_mov_b32 m0, s25
	v_lshl_add_u64 v[56:57], v[36:37], 0, s[28:29]
	s_waitcnt vmcnt(8)
	s_barrier
	global_load_lds_dwordx4 v[56:57], off
	v_lshl_add_u64 v[56:57], v[38:39], 0, s[28:29]
	s_mov_b32 m0, s23
	s_nop 0
	global_load_lds_dwordx4 v[56:57], off
	v_lshl_add_u64 v[56:57], v[40:41], 0, s[28:29]
	s_mov_b32 m0, s24
	s_nop 0
	global_load_lds_dwordx4 v[56:57], off
	v_lshl_add_u64 v[56:57], v[42:43], 0, s[28:29]
	s_mov_b32 m0, s26
	s_nop 0
	global_load_lds_dwordx4 v[56:57], off
	ds_read_b128 v[56:59], v49
	ds_read_b128 v[60:63], v51
	ds_read_b128 v[64:67], v49 offset:4096
	ds_read_b128 v[68:71], v48
	s_waitcnt lgkmcnt(0)
	v_mfma_f32_32x32x16_f16 v[18:33], v[56:59], v[60:63], v[18:33]
	ds_read_b128 v[56:59], v53
	v_mfma_f32_32x32x16_f16 v[2:17], v[64:67], v[60:63], v[2:17]
	ds_read_b128 v[60:63], v48 offset:4096
	s_waitcnt lgkmcnt(0)
	v_mfma_f32_32x32x16_f16 v[18:33], v[68:71], v[56:59], v[18:33]
	v_mfma_f32_32x32x16_f16 v[2:17], v[60:63], v[56:59], v[2:17]
	ds_read_b128 v[56:59], v52
	ds_read_b128 v[60:63], v54
	ds_read_b128 v[64:67], v52 offset:4096
	ds_read_b128 v[68:71], v50
	s_waitcnt lgkmcnt(0)
	v_mfma_f32_32x32x16_f16 v[18:33], v[56:59], v[60:63], v[18:33]
	ds_read_b128 v[56:59], v55
	v_mfma_f32_32x32x16_f16 v[2:17], v[64:67], v[60:63], v[2:17]
	ds_read_b128 v[60:63], v50 offset:4096
	s_waitcnt lgkmcnt(0)
	v_mfma_f32_32x32x16_f16 v[18:33], v[68:71], v[56:59], v[18:33]
	v_mfma_f32_32x32x16_f16 v[2:17], v[60:63], v[56:59], v[2:17]
	s_mov_b64 s[28:29], 0x400
	s_mov_b32 m0, s19
	v_lshl_add_u64 v[56:57], v[36:37], 0, s[28:29]
	s_waitcnt vmcnt(8)
	s_barrier
	global_load_lds_dwordx4 v[56:57], off
	v_lshl_add_u64 v[56:57], v[38:39], 0, s[28:29]
	s_mov_b32 m0, s20
	s_nop 0
	global_load_lds_dwordx4 v[56:57], off
	v_lshl_add_u64 v[56:57], v[40:41], 0, s[28:29]
	s_mov_b32 m0, s21
	s_nop 0
	global_load_lds_dwordx4 v[56:57], off
	v_lshl_add_u64 v[56:57], v[42:43], 0, s[28:29]
	s_mov_b32 m0, s22
	s_nop 0
	global_load_lds_dwordx4 v[56:57], off
	ds_read_b128 v[56:59], v49 offset:16384
	ds_read_b128 v[60:63], v51 offset:16384
	ds_read_b128 v[64:67], v49 offset:20480
	ds_read_b128 v[68:71], v48 offset:16384
	s_waitcnt lgkmcnt(0)
	v_mfma_f32_32x32x16_f16 v[18:33], v[56:59], v[60:63], v[18:33]
	ds_read_b128 v[56:59], v53 offset:16384
	v_mfma_f32_32x32x16_f16 v[2:17], v[64:67], v[60:63], v[2:17]
	ds_read_b128 v[60:63], v48 offset:20480
	s_waitcnt lgkmcnt(0)
	v_mfma_f32_32x32x16_f16 v[18:33], v[68:71], v[56:59], v[18:33]
	v_mfma_f32_32x32x16_f16 v[2:17], v[60:63], v[56:59], v[2:17]
	ds_read_b128 v[56:59], v52 offset:16384
	ds_read_b128 v[60:63], v54 offset:16384
	ds_read_b128 v[64:67], v52 offset:20480
	ds_read_b128 v[68:71], v50 offset:16384
	s_waitcnt lgkmcnt(0)
	v_mfma_f32_32x32x16_f16 v[18:33], v[56:59], v[60:63], v[18:33]
	ds_read_b128 v[56:59], v55 offset:16384
	v_mfma_f32_32x32x16_f16 v[2:17], v[64:67], v[60:63], v[2:17]
	ds_read_b128 v[60:63], v50 offset:20480
	s_waitcnt lgkmcnt(0)
	v_mfma_f32_32x32x16_f16 v[18:33], v[68:71], v[56:59], v[18:33]
	v_mfma_f32_32x32x16_f16 v[2:17], v[60:63], v[56:59], v[2:17]
	s_mov_b64 s[28:29], 0x480
	s_mov_b32 m0, s15
	v_lshl_add_u64 v[56:57], v[36:37], 0, s[28:29]
	s_waitcnt vmcnt(8)
	s_barrier
	global_load_lds_dwordx4 v[56:57], off
	v_lshl_add_u64 v[56:57], v[38:39], 0, s[28:29]
	s_mov_b32 m0, s16
	s_nop 0
	global_load_lds_dwordx4 v[56:57], off
	v_lshl_add_u64 v[56:57], v[40:41], 0, s[28:29]
	s_mov_b32 m0, s17
	s_nop 0
	global_load_lds_dwordx4 v[56:57], off
	v_lshl_add_u64 v[56:57], v[42:43], 0, s[28:29]
	s_mov_b32 m0, s18
	s_nop 0
	global_load_lds_dwordx4 v[56:57], off
	ds_read_b128 v[56:59], v49 offset:32768
	ds_read_b128 v[60:63], v51 offset:32768
	ds_read_b128 v[64:67], v49 offset:36864
	ds_read_b128 v[68:71], v48 offset:32768
	s_waitcnt lgkmcnt(0)
	v_mfma_f32_32x32x16_f16 v[18:33], v[56:59], v[60:63], v[18:33]
	ds_read_b128 v[56:59], v53 offset:32768
	v_mfma_f32_32x32x16_f16 v[2:17], v[64:67], v[60:63], v[2:17]
	ds_read_b128 v[60:63], v48 offset:36864
	s_waitcnt lgkmcnt(0)
	v_mfma_f32_32x32x16_f16 v[18:33], v[68:71], v[56:59], v[18:33]
	v_mfma_f32_32x32x16_f16 v[2:17], v[60:63], v[56:59], v[2:17]
	ds_read_b128 v[56:59], v52 offset:32768
	ds_read_b128 v[60:63], v54 offset:32768
	ds_read_b128 v[64:67], v52 offset:36864
	ds_read_b128 v[68:71], v50 offset:32768
	s_waitcnt lgkmcnt(0)
	v_mfma_f32_32x32x16_f16 v[18:33], v[56:59], v[60:63], v[18:33]
	ds_read_b128 v[56:59], v55 offset:32768
	v_mfma_f32_32x32x16_f16 v[2:17], v[64:67], v[60:63], v[2:17]
	ds_read_b128 v[60:63], v50 offset:36864
	s_waitcnt lgkmcnt(0)
	v_mfma_f32_32x32x16_f16 v[18:33], v[68:71], v[56:59], v[18:33]
	v_mfma_f32_32x32x16_f16 v[2:17], v[60:63], v[56:59], v[2:17]
	s_mov_b64 s[28:29], 0x500
	s_mov_b32 m0, s11
	v_lshl_add_u64 v[56:57], v[36:37], 0, s[28:29]
	s_waitcnt vmcnt(8)
	s_barrier
	global_load_lds_dwordx4 v[56:57], off
	v_lshl_add_u64 v[56:57], v[38:39], 0, s[28:29]
	s_mov_b32 m0, s12
	s_nop 0
	global_load_lds_dwordx4 v[56:57], off
	v_lshl_add_u64 v[56:57], v[40:41], 0, s[28:29]
	s_mov_b32 m0, s13
	s_nop 0
	global_load_lds_dwordx4 v[56:57], off
	v_lshl_add_u64 v[56:57], v[42:43], 0, s[28:29]
	s_mov_b32 m0, s14
	s_nop 0
	global_load_lds_dwordx4 v[56:57], off
	ds_read_b128 v[56:59], v49 offset:49152
	ds_read_b128 v[60:63], v51 offset:49152
	ds_read_b128 v[64:67], v49 offset:53248
	ds_read_b128 v[68:71], v48 offset:49152
	s_waitcnt lgkmcnt(0)
	v_mfma_f32_32x32x16_f16 v[18:33], v[56:59], v[60:63], v[18:33]
	ds_read_b128 v[56:59], v53 offset:49152
	v_mfma_f32_32x32x16_f16 v[2:17], v[64:67], v[60:63], v[2:17]
	ds_read_b128 v[60:63], v48 offset:53248
	s_waitcnt lgkmcnt(0)
	v_mfma_f32_32x32x16_f16 v[18:33], v[68:71], v[56:59], v[18:33]
	v_mfma_f32_32x32x16_f16 v[2:17], v[60:63], v[56:59], v[2:17]
	ds_read_b128 v[56:59], v52 offset:49152
	ds_read_b128 v[60:63], v54 offset:49152
	ds_read_b128 v[64:67], v52 offset:53248
	ds_read_b128 v[68:71], v50 offset:49152
	s_waitcnt lgkmcnt(0)
	v_mfma_f32_32x32x16_f16 v[18:33], v[56:59], v[60:63], v[18:33]
	ds_read_b128 v[56:59], v55 offset:49152
	v_mfma_f32_32x32x16_f16 v[2:17], v[64:67], v[60:63], v[2:17]
	ds_read_b128 v[60:63], v50 offset:53248
	s_waitcnt lgkmcnt(0)
	v_mfma_f32_32x32x16_f16 v[18:33], v[68:71], v[56:59], v[18:33]
	v_mfma_f32_32x32x16_f16 v[2:17], v[60:63], v[56:59], v[2:17]
	s_mov_b64 s[28:29], 0x580
	s_mov_b32 m0, s25
	v_lshl_add_u64 v[64:65], v[36:37], 0, s[28:29]
	s_waitcnt vmcnt(8)
	s_barrier
	global_load_lds_dwordx4 v[64:65], off
	v_lshl_add_u64 v[66:67], v[38:39], 0, s[28:29]
	s_mov_b32 m0, s23
	v_lshl_add_u64 v[68:69], v[40:41], 0, s[28:29]
	global_load_lds_dwordx4 v[66:67], off
	s_mov_b32 m0, s24
	v_lshl_add_u64 v[70:71], v[42:43], 0, s[28:29]
	global_load_lds_dwordx4 v[68:69], off
	s_mov_b32 m0, s26
	s_nop 0
	global_load_lds_dwordx4 v[70:71], off
	ds_read_b128 v[36:39], v49
	ds_read_b128 v[40:43], v51
	ds_read_b128 v[56:59], v49 offset:4096
	ds_read_b128 v[60:63], v48
	s_waitcnt lgkmcnt(0)
	v_mfma_f32_32x32x16_f16 v[18:33], v[36:39], v[40:43], v[18:33]
	ds_read_b128 v[36:39], v53
	v_mfma_f32_32x32x16_f16 v[2:17], v[56:59], v[40:43], v[2:17]
	ds_read_b128 v[40:43], v48 offset:4096
	s_waitcnt lgkmcnt(0)
	v_mfma_f32_32x32x16_f16 v[18:33], v[60:63], v[36:39], v[18:33]
	v_mfma_f32_32x32x16_f16 v[2:17], v[40:43], v[36:39], v[2:17]
	ds_read_b128 v[36:39], v52
	ds_read_b128 v[40:43], v54
	ds_read_b128 v[56:59], v52 offset:4096
	ds_read_b128 v[60:63], v50
	s_waitcnt lgkmcnt(0)
	v_mfma_f32_32x32x16_f16 v[18:33], v[36:39], v[40:43], v[18:33]
	ds_read_b128 v[36:39], v55
	v_mfma_f32_32x32x16_f16 v[2:17], v[56:59], v[40:43], v[2:17]
	ds_read_b128 v[40:43], v50 offset:4096
	s_waitcnt lgkmcnt(0)
	v_mfma_f32_32x32x16_f16 v[18:33], v[60:63], v[36:39], v[18:33]
	v_mfma_f32_32x32x16_f16 v[2:17], v[40:43], v[36:39], v[2:17]
	s_mov_b32 m0, s19
	s_waitcnt vmcnt(8)
	s_barrier
	global_load_lds_dwordx4 v[64:65], off
	s_mov_b32 m0, s20
	s_nop 0
	global_load_lds_dwordx4 v[66:67], off
	s_mov_b32 m0, s21
	s_nop 0
	global_load_lds_dwordx4 v[68:69], off
	s_mov_b32 m0, s22
	s_nop 0
	global_load_lds_dwordx4 v[70:71], off
	ds_read_b128 v[36:39], v49 offset:16384
	ds_read_b128 v[40:43], v51 offset:16384
	ds_read_b128 v[56:59], v49 offset:20480
	ds_read_b128 v[60:63], v48 offset:16384
	s_waitcnt lgkmcnt(0)
	v_mfma_f32_32x32x16_f16 v[18:33], v[36:39], v[40:43], v[18:33]
	ds_read_b128 v[36:39], v53 offset:16384
	v_mfma_f32_32x32x16_f16 v[2:17], v[56:59], v[40:43], v[2:17]
	ds_read_b128 v[40:43], v48 offset:20480
	s_waitcnt lgkmcnt(0)
	v_mfma_f32_32x32x16_f16 v[18:33], v[60:63], v[36:39], v[18:33]
	v_mfma_f32_32x32x16_f16 v[2:17], v[40:43], v[36:39], v[2:17]
	ds_read_b128 v[36:39], v52 offset:16384
	ds_read_b128 v[40:43], v54 offset:16384
	ds_read_b128 v[56:59], v52 offset:20480
	ds_read_b128 v[60:63], v50 offset:16384
	s_waitcnt lgkmcnt(0)
	v_mfma_f32_32x32x16_f16 v[18:33], v[36:39], v[40:43], v[18:33]
	ds_read_b128 v[36:39], v55 offset:16384
	v_mfma_f32_32x32x16_f16 v[2:17], v[56:59], v[40:43], v[2:17]
	ds_read_b128 v[40:43], v50 offset:20480
	s_waitcnt lgkmcnt(0)
	v_mfma_f32_32x32x16_f16 v[18:33], v[60:63], v[36:39], v[18:33]
	v_mfma_f32_32x32x16_f16 v[2:17], v[40:43], v[36:39], v[2:17]
	s_mov_b32 m0, s15
	s_waitcnt vmcnt(8)
	s_barrier
	global_load_lds_dwordx4 v[64:65], off
	s_mov_b32 m0, s16
	s_nop 0
	global_load_lds_dwordx4 v[66:67], off
	s_mov_b32 m0, s17
	s_nop 0
	global_load_lds_dwordx4 v[68:69], off
	s_mov_b32 m0, s18
	s_nop 0
	global_load_lds_dwordx4 v[70:71], off
	ds_read_b128 v[36:39], v49 offset:32768
	ds_read_b128 v[40:43], v51 offset:32768
	ds_read_b128 v[56:59], v49 offset:36864
	ds_read_b128 v[60:63], v48 offset:32768
	s_waitcnt lgkmcnt(0)
	v_mfma_f32_32x32x16_f16 v[18:33], v[36:39], v[40:43], v[18:33]
	ds_read_b128 v[36:39], v53 offset:32768
	v_mfma_f32_32x32x16_f16 v[2:17], v[56:59], v[40:43], v[2:17]
	ds_read_b128 v[40:43], v48 offset:36864
	s_waitcnt lgkmcnt(0)
	v_mfma_f32_32x32x16_f16 v[18:33], v[60:63], v[36:39], v[18:33]
	v_mfma_f32_32x32x16_f16 v[2:17], v[40:43], v[36:39], v[2:17]
	ds_read_b128 v[36:39], v52 offset:32768
	ds_read_b128 v[40:43], v54 offset:32768
	ds_read_b128 v[56:59], v52 offset:36864
	ds_read_b128 v[60:63], v50 offset:32768
	s_waitcnt lgkmcnt(0)
	v_mfma_f32_32x32x16_f16 v[18:33], v[36:39], v[40:43], v[18:33]
	ds_read_b128 v[36:39], v55 offset:32768
	v_mfma_f32_32x32x16_f16 v[2:17], v[56:59], v[40:43], v[2:17]
	ds_read_b128 v[40:43], v50 offset:36864
	s_waitcnt lgkmcnt(0)
	v_mfma_f32_32x32x16_f16 v[18:33], v[60:63], v[36:39], v[18:33]
	v_mfma_f32_32x32x16_f16 v[2:17], v[40:43], v[36:39], v[2:17]
	s_mov_b32 m0, s11
	s_waitcnt vmcnt(8)
	s_barrier
	global_load_lds_dwordx4 v[64:65], off
	s_mov_b32 m0, s12
	s_nop 0
	global_load_lds_dwordx4 v[66:67], off
	s_mov_b32 m0, s13
	s_nop 0
	global_load_lds_dwordx4 v[68:69], off
	s_mov_b32 m0, s14
	s_nop 0
	global_load_lds_dwordx4 v[70:71], off
	ds_read_b128 v[36:39], v49 offset:49152
	ds_read_b128 v[40:43], v51 offset:49152
	ds_read_b128 v[56:59], v49 offset:53248
	ds_read_b128 v[60:63], v48 offset:49152
	s_waitcnt lgkmcnt(0)
	v_mfma_f32_32x32x16_f16 v[18:33], v[36:39], v[40:43], v[18:33]
	ds_read_b128 v[36:39], v53 offset:49152
	v_mfma_f32_32x32x16_f16 v[2:17], v[56:59], v[40:43], v[2:17]
	ds_read_b128 v[40:43], v48 offset:53248
	s_waitcnt lgkmcnt(0)
	v_mfma_f32_32x32x16_f16 v[18:33], v[60:63], v[36:39], v[18:33]
	v_mfma_f32_32x32x16_f16 v[2:17], v[40:43], v[36:39], v[2:17]
	ds_read_b128 v[36:39], v52 offset:49152
	ds_read_b128 v[40:43], v54 offset:49152
	ds_read_b128 v[56:59], v52 offset:53248
	ds_read_b128 v[60:63], v50 offset:49152
	s_waitcnt lgkmcnt(0)
	v_mfma_f32_32x32x16_f16 v[18:33], v[36:39], v[40:43], v[18:33]
	ds_read_b128 v[36:39], v55 offset:49152
	v_mfma_f32_32x32x16_f16 v[2:17], v[56:59], v[40:43], v[2:17]
	ds_read_b128 v[40:43], v50 offset:53248
	s_waitcnt lgkmcnt(0)
	v_mfma_f32_32x32x16_f16 v[18:33], v[60:63], v[36:39], v[18:33]
	v_mfma_f32_32x32x16_f16 v[2:17], v[40:43], v[36:39], v[2:17]
	v_mul_u32_u24_e32 v56, 0x2400, v44
	v_lshl_or_b32 v36, v47, 2, v56
	s_movk_i32 s11, 0x240
	v_mad_u32_u24 v36, v46, s11, v36
	s_waitcnt vmcnt(8)
	s_barrier
	s_waitcnt vmcnt(0)
	s_waitcnt vmcnt(0)
	s_barrier
	s_nop 3
	ds_write2_b32 v36, v18, v19 offset1:36
	ds_write2_b32 v36, v20, v21 offset0:72 offset1:108
	v_add_u32_e32 v18, 0x400, v36
	ds_write2_b32 v18, v22, v23 offset0:32 offset1:68
	ds_write2_b32 v18, v24, v25 offset0:104 offset1:140
	v_add_u32_e32 v18, 0x800, v36
	ds_write2_b32 v18, v26, v27 offset0:64 offset1:100
	ds_write2_b32 v18, v28, v29 offset0:136 offset1:172
	v_add_u32_e32 v18, 0xc00, v36
	ds_write2_b32 v18, v30, v31 offset0:96 offset1:132
	ds_write2_b32 v18, v32, v33 offset0:168 offset1:204
	v_add_u32_e32 v18, 0x1000, v36
	ds_write2_b32 v18, v2, v3 offset0:128 offset1:164
	ds_write2_b32 v18, v4, v5 offset0:200 offset1:236
	v_add_u32_e32 v2, 0x1400, v36
	ds_write2_b32 v2, v6, v7 offset0:160 offset1:196
	v_add_u32_e32 v2, 0x1600, v36
	ds_write2_b32 v2, v8, v9 offset0:104 offset1:140
	v_add_u32_e32 v2, 0x1800, v36
	ds_write2_b32 v2, v10, v11 offset0:192 offset1:228
	v_add_u32_e32 v2, 0x1c00, v36
	ds_write2_b32 v2, v12, v13 offset0:8 offset1:44
	v_add_u32_e32 v2, 0x1e00, v36
	v_lshl_or_b32 v5, v45, 5, s10
	v_lshlrev_b32_e32 v6, 2, v0
	ds_write2_b32 v2, v14, v15 offset0:96 offset1:132
	v_add_u32_e32 v2, 0x2000, v36
	v_lshlrev_b32_e32 v4, 6, v34
	v_lshlrev_b32_e32 v34, 2, v5
	v_and_b32_e32 v6, 28, v6
	ds_write2_b32 v2, v16, v17 offset0:40 offset1:76
	v_lshl_add_u64 v[2:3], s[8:9], 0, v[34:35]
	v_lshlrev_b32_e32 v34, 2, v6
	v_lshl_add_u64 v[10:11], v[2:3], 0, v[34:35]
	v_or3_b32 v2, s3, v4, v1
	v_or_b32_e32 v3, v5, v6
	s_movk_i32 s3, 0x300
	v_mad_u32_u24 v36, v2, s3, v3
	v_add_u32_e32 v2, 0x4800, v36
	v_mov_b32_e32 v3, v35
	v_lshlrev_b64 v[40:41], 2, v[2:3]
	v_lshl_add_u64 v[12:13], s[6:7], 0, v[40:41]
	global_load_dwordx4 v[2:5], v[10:11], off
	global_load_dwordx4 v[6:9], v[12:13], off
	v_add_u32_e32 v10, 0x3000, v36
	v_mov_b32_e32 v11, v35
	v_lshlrev_b64 v[42:43], 2, v[10:11]
	v_lshl_add_u64 v[10:11], s[6:7], 0, v[42:43]
	global_load_dwordx4 v[10:13], v[10:11], off
	v_add_u32_e32 v14, 0x1800, v36
	v_mov_b32_e32 v15, v35
	v_lshlrev_b64 v[44:45], 2, v[14:15]
	v_lshl_add_u64 v[14:15], s[6:7], 0, v[44:45]
	v_mov_b32_e32 v37, v35
	global_load_dwordx4 v[14:17], v[14:15], off
	v_lshlrev_b64 v[46:47], 2, v[36:37]
	v_lshl_add_u64 v[18:19], s[6:7], 0, v[46:47]
	global_load_dwordx4 v[18:21], v[18:19], off
	v_add_u32_e32 v22, 0x6000, v36
	v_mov_b32_e32 v23, v35
	v_lshlrev_b64 v[48:49], 2, v[22:23]
	v_lshl_add_u64 v[22:23], s[6:7], 0, v[48:49]
	v_add_u32_e32 v26, 0x7800, v36
	v_mov_b32_e32 v27, v35
	global_load_dwordx4 v[22:25], v[22:23], off
	v_lshlrev_b64 v[50:51], 2, v[26:27]
	v_lshl_add_u64 v[26:27], s[6:7], 0, v[50:51]
	global_load_dwordx4 v[26:29], v[26:27], off
	v_add_u32_e32 v30, 0x9000, v36
	v_mov_b32_e32 v31, v35
	v_add_u32_e32 v36, 0xa800, v36
	v_lshlrev_b64 v[52:53], 2, v[30:31]
	v_lshlrev_b64 v[54:55], 2, v[36:37]
	v_lshl_add_u64 v[30:31], s[6:7], 0, v[52:53]
	v_lshl_add_u64 v[36:37], s[6:7], 0, v[54:55]
	global_load_dwordx4 v[30:33], v[30:31], off
	v_or_b32_e32 v34, v56, v34
	global_load_dwordx4 v[36:39], v[36:37], off
	s_movk_i32 s3, 0x90
	v_mad_u32_u24 v1, v1, s3, v34
	v_lshl_add_u64 v[58:59], s[4:5], 0, v[42:43]
	v_lshl_add_u64 v[60:61], s[4:5], 0, v[40:41]
	ds_read_b128 v[40:43], v1 offset:3456
	v_lshl_add_u64 v[34:35], s[4:5], 0, v[46:47]
	v_lshl_add_u64 v[56:57], s[4:5], 0, v[44:45]
	ds_read_b128 v[44:47], v1 offset:2304
	v_lshl_add_u64 v[48:49], s[4:5], 0, v[48:49]
	v_lshl_add_u64 v[50:51], s[4:5], 0, v[50:51]
	v_lshl_add_u64 v[52:53], s[4:5], 0, v[52:53]
	v_lshl_add_u64 v[54:55], s[4:5], 0, v[54:55]
	s_mov_b64 s[4:5], 0
	s_waitcnt vmcnt(8) lgkmcnt(1)
	v_pk_add_f32 v[40:41], v[2:3], v[40:41]
	s_waitcnt vmcnt(7)
	v_pk_add_f32 v[6:7], v[40:41], v[6:7]
	v_pk_add_f32 v[40:41], v[4:5], v[42:43]
	s_waitcnt lgkmcnt(0)
	v_pk_add_f32 v[44:45], v[2:3], v[44:45]
	v_pk_add_f32 v[8:9], v[40:41], v[8:9]
	ds_read_b128 v[40:43], v1 offset:1152
	s_waitcnt vmcnt(6)
	v_pk_add_f32 v[10:11], v[44:45], v[10:11]
	v_pk_add_f32 v[44:45], v[4:5], v[46:47]
	s_nop 0
	v_pk_add_f32 v[12:13], v[44:45], v[12:13]
	ds_read_b128 v[44:47], v1
	s_waitcnt lgkmcnt(1)
	v_pk_add_f32 v[40:41], v[2:3], v[40:41]
	s_waitcnt vmcnt(5)
	v_pk_add_f32 v[14:15], v[40:41], v[14:15]
	v_pk_add_f32 v[40:41], v[4:5], v[42:43]
	s_nop 0
	v_pk_add_f32 v[16:17], v[40:41], v[16:17]
	s_waitcnt lgkmcnt(0)
	v_pk_add_f32 v[40:41], v[2:3], v[44:45]
	s_waitcnt vmcnt(4)
	v_pk_add_f32 v[18:19], v[40:41], v[18:19]
	v_pk_add_f32 v[40:41], v[4:5], v[46:47]
	s_nop 0
	v_pk_add_f32 v[20:21], v[40:41], v[20:21]
	global_store_dwordx4 v[34:35], v[18:21], off
	ds_read_b128 v[18:21], v1 offset:4608
	global_store_dwordx4 v[56:57], v[14:17], off
	global_store_dwordx4 v[58:59], v[10:13], off
	global_store_dwordx4 v[60:61], v[6:9], off
	ds_read_b128 v[6:9], v1 offset:5760
	s_waitcnt lgkmcnt(1)
	v_pk_add_f32 v[10:11], v[2:3], v[18:19]
	v_pk_add_f32 v[12:13], v[4:5], v[20:21]
	s_waitcnt vmcnt(7)
	v_pk_add_f32 v[10:11], v[10:11], v[22:23]
	v_pk_add_f32 v[12:13], v[12:13], v[24:25]
	global_store_dwordx4 v[48:49], v[10:13], off
	ds_read_b128 v[10:13], v1 offset:6912
	s_waitcnt lgkmcnt(1)
	v_pk_add_f32 v[6:7], v[2:3], v[6:7]
	v_pk_add_f32 v[8:9], v[4:5], v[8:9]
	s_waitcnt vmcnt(7)
	v_pk_add_f32 v[6:7], v[6:7], v[26:27]
	v_pk_add_f32 v[8:9], v[8:9], v[28:29]
	global_store_dwordx4 v[50:51], v[6:9], off
	ds_read_b128 v[6:9], v1 offset:8064
	s_waitcnt lgkmcnt(1)
	v_pk_add_f32 v[10:11], v[2:3], v[10:11]
	v_pk_add_f32 v[12:13], v[4:5], v[12:13]
	s_waitcnt vmcnt(7)
	v_pk_add_f32 v[10:11], v[10:11], v[30:31]
	v_pk_add_f32 v[12:13], v[12:13], v[32:33]
	s_waitcnt lgkmcnt(0)
	v_pk_add_f32 v[2:3], v[2:3], v[6:7]
	v_pk_add_f32 v[4:5], v[4:5], v[8:9]
	s_waitcnt vmcnt(6)
	v_pk_add_f32 v[2:3], v[2:3], v[36:37]
	v_pk_add_f32 v[4:5], v[4:5], v[38:39]
	global_store_dwordx4 v[52:53], v[10:13], off
	global_store_dwordx4 v[54:55], v[2:5], off

.LBB12_14:
	s_endpgm
	s_nop 0
	s_nop 0
	s_nop 0
	s_nop 0
	s_nop 0
	s_nop 0
	s_nop 0
	s_nop 0
	s_nop 0
	s_nop 0
	s_nop 0
	s_nop 0
	s_nop 0
	s_nop 0
	s_nop 0
	s_nop 0
	s_nop 0
	s_nop 0
	s_nop 0
	s_nop 0
	s_nop 0
	s_nop 0
	s_nop 0
	s_nop 0
	s_nop 0
	s_nop 0
	s_nop 0
	s_nop 0
	s_nop 0
	s_nop 0
	s_nop 0
	s_nop 0
	s_nop 0
	s_nop 0
	s_nop 0
	s_nop 0
	s_nop 0
	s_nop 0
	s_nop 0
	s_nop 0
	s_nop 0
	s_nop 0
	s_nop 0
	s_nop 0
	s_nop 0
	s_nop 0
	s_nop 0
	s_nop 0
	s_nop 0
	s_nop 0
	s_nop 0
	s_nop 0
	s_nop 0
	s_endpgm

	.amdhsa_kernel _Z6gemm_kILi1ELi128ELi4ELi8EEv5GArgs
		.amdhsa_group_segment_fixed_size 131072
		.amdhsa_private_segment_fixed_size 0
		.amdhsa_kernarg_size 136
		.amdhsa_user_sgpr_count 2
		.amdhsa_user_sgpr_dispatch_ptr 0
		.amdhsa_user_sgpr_queue_ptr 0
		.amdhsa_user_sgpr_kernarg_segment_ptr 1
		.amdhsa_user_sgpr_dispatch_id 0
		.amdhsa_user_sgpr_kernarg_preload_length 0
		.amdhsa_user_sgpr_kernarg_preload_offset 0
		.amdhsa_user_sgpr_private_segment_size 0
		.amdhsa_uses_dynamic_stack 0
		.amdhsa_enable_private_segment 0
		.amdhsa_system_sgpr_workgroup_id_x 1
		.amdhsa_system_sgpr_workgroup_id_y 0
		.amdhsa_system_sgpr_workgroup_id_z 0
		.amdhsa_system_sgpr_workgroup_info 0
		.amdhsa_system_vgpr_workitem_id 0
		.amdhsa_next_free_vgpr 177
		.amdhsa_next_free_sgpr 96
		.amdhsa_accum_offset 180
		.amdhsa_reserve_vcc 1
		.amdhsa_float_round_mode_32 0
		.amdhsa_float_round_mode_16_64 0
		.amdhsa_float_denorm_mode_32 3
		.amdhsa_float_denorm_mode_16_64 3
		.amdhsa_dx10_clamp 1
		.amdhsa_ieee_mode 1
		.amdhsa_fp16_overflow 0
		.amdhsa_tg_split 0
		.amdhsa_exception_fp_ieee_invalid_op 0
		.amdhsa_exception_fp_denorm_src 0
		.amdhsa_exception_fp_ieee_div_zero 0
		.amdhsa_exception_fp_ieee_overflow 0
		.amdhsa_exception_fp_ieee_underflow 0
		.amdhsa_exception_fp_ieee_inexact 0
		.amdhsa_exception_int_div_zero 0
	.end_amdhsa_kernel

_Z6gemm_kILi2ELi128ELi2ELi4EEv5GArgs:
	v_lshlrev_b32_e32 v200, 4, v0
	s_getpc_b64 s[92:93]
	s_add_u32 s92, s92, 0x30f8
	s_addc_u32 s93, s93, 0x0
	global_load_dwordx4 v[196:199], v200, s[92:93]
	v_add_u32_e32 v200, 0x1000, v200
	global_load_dwordx4 v[196:199], v200, s[92:93]
	v_lshlrev_b32_e32 v200, 4, v0
	s_load_dwordx4 s[4:7], s[0:1], 0x38
	s_lshr_b32 s9, s2, 3
	s_and_b32 s3, s2, 7
	s_mul_hi_u32 s10, s9, 0x33333334
	s_mul_i32 s10, s10, 5
	s_waitcnt lgkmcnt(0)
	s_load_dword s8, s[6:7], 0x280
	s_sub_i32 s9, s9, s10
	s_waitcnt lgkmcnt(0)
	s_mul_i32 s3, s8, s3
	s_ashr_i32 s10, s3, 3
	s_add_i32 s3, s3, s8
	s_ashr_i32 s8, s3, 3
	s_add_i32 s3, s10, s9
	s_cmp_ge_i32 s3, s8
	s_cbranch_scc1 .LBB13_20
	s_lshl_b32 s8, s3, 2
	s_ashr_i32 s9, s8, 31
	s_lshl_b64 s[8:9], s[8:9], 2
	s_add_u32 s6, s6, s8
	s_addc_u32 s7, s7, s9
	s_load_dwordx4 s[12:15], s[6:7], 0x0
	s_mov_b32 s3, 0
	s_waitcnt lgkmcnt(0)
	s_cmp_lt_i32 s12, 0
	s_cbranch_scc1 .LBB13_20
	s_mov_b32 s8, s13
	s_mov_b32 s9, s14
	v_lshrrev_b32_e32 v1, 6, v0
	v_bfe_u32 v76, v0, 3, 3
	v_lshl_or_b32 v6, v1, 5, v76
	v_or_b32_e32 v44, 8, v6
	s_waitcnt lgkmcnt(0)
	s_add_i32 s6, s9, -1
	v_add_u32_e32 v4, s8, v6
	v_min_i32_e32 v2, s6, v4
	v_add_u32_e32 v4, 16, v4
	v_min_i32_e32 v4, s6, v4
	v_ashrrev_i32_e32 v3, 31, v2
	v_ashrrev_i32_e32 v5, 31, v4
	v_lshl_add_u64 v[2:3], v[2:3], 2, s[4:5]
	v_lshl_add_u64 v[4:5], v[4:5], 2, s[4:5]
	global_load_dword v7, v[2:3], off
	global_load_dword v8, v[4:5], off
	v_or_b32_e32 v4, 24, v6
	v_add_u32_e32 v2, s8, v4
	v_min_i32_e32 v2, s6, v2
	v_ashrrev_i32_e32 v3, 31, v2
	v_lshl_add_u64 v[2:3], v[2:3], 2, s[4:5]
	global_load_dword v9, v[2:3], off
	v_add_u32_e32 v2, s8, v44
	v_min_i32_e32 v2, s6, v2
	v_ashrrev_i32_e32 v3, 31, v2
	v_lshl_add_u64 v[2:3], v[2:3], 2, s[4:5]
	global_load_dword v45, v[2:3], off
	s_load_dwordx2 s[14:15], s[0:1], 0x0
	s_load_dwordx4 s[4:7], s[0:1], 0x10
	v_lshrrev_b32_e32 v4, 1, v4
	v_bfe_u32 v2, v0, 4, 2
	v_xor_b32_e32 v4, v4, v0
	s_mul_hi_u32 s10, s2, 0xcccccccd
	s_movk_i32 s2, 0x680
	v_bitop3_b32 v2, v2, v0, 7 bitop3:0x78
	s_waitcnt lgkmcnt(0)
	v_mov_b64_e32 v[36:37], s[14:15]
	v_lshlrev_b32_e32 v4, 3, v4
	v_mov_b32_e32 v3, 0
	v_bfe_u32 v77, v0, 5, 1
	s_lshl_b32 s10, s10, 2
	v_lshlrev_b32_e32 v2, 4, v2
	v_bitop3_b32 v11, v4, 8, 56 bitop3:0x6c
	s_mul_i32 s16, s12, 0x900000
	v_lshl_or_b32 v48, v1, 1, v77
	s_and_b32 s10, s10, 0xffffff80
	s_mul_hi_u32 s13, s12, 0x900000
	v_mul_u32_u24_e32 v10, 0x6000, v48
	s_add_u32 s4, s4, s16
	s_addc_u32 s5, s5, s13
	s_mov_b32 s11, s3
	v_and_b32_e32 v78, 31, v0
	s_movk_i32 s18, 0x3000
	s_movk_i32 s17, 0x6000
	s_mov_b32 s19, 0x9000
	s_mov_b32 s20, 0xc000
	s_mov_b32 s21, 0xf000
	s_mov_b32 s22, 0x12000
	v_lshlrev_b32_e32 v81, 12, v1
	v_or_b32_e32 v46, 0xc00, v81
	v_readfirstlane_b32 s13, v81
	s_mov_b32 m0, s13
	v_readfirstlane_b32 s16, v46
	v_lshlrev_b32_e32 v82, 9, v78
	s_load_dwordx2 s[0:1], s[0:1], 0x70
	v_lshrrev_b32_e32 v79, 7, v0
	v_bfe_u32 v80, v0, 6, 1
	v_lshlrev_b32_e32 v89, 13, v79
	v_lshlrev_b32_e32 v90, 7, v78
	v_lshlrev_b32_e32 v91, 13, v80
	s_mov_b32 s13, 0xc3000
	v_mov_b32_e32 v53, v3
	v_mov_b32_e32 v54, v3
	v_mov_b32_e32 v55, v3
	v_mov_b32_e32 v56, v3
	v_mov_b32_e32 v57, v3
	v_mov_b32_e32 v58, v3
	v_mov_b32_e32 v59, v3
	v_mov_b32_e32 v60, v3
	v_mov_b32_e32 v61, v3
	v_mov_b32_e32 v62, v3
	v_mov_b32_e32 v63, v3
	v_mov_b32_e32 v64, v3
	v_mov_b32_e32 v65, v3
	s_waitcnt vmcnt(3)
	v_mad_i64_i32 v[4:5], s[14:15], v7, s2, v[36:37]
	v_lshl_add_u64 v[66:67], v[4:5], 0, v[2:3]
	s_waitcnt vmcnt(2)
	v_mad_i64_i32 v[4:5], s[14:15], v8, s2, v[36:37]
	v_xor_b32_e32 v2, 16, v2
	v_lshl_add_u64 v[68:69], v[4:5], 0, v[2:3]
	s_waitcnt vmcnt(1)
	v_mad_i64_i32 v[6:7], s[14:15], v9, s2, v[36:37]
	v_lshlrev_b32_e32 v2, 1, v11
	v_lshl_add_u64 v[70:71], v[6:7], 0, v[2:3]
	v_lshlrev_b32_e32 v2, 2, v10
	v_lshl_add_u64 v[4:5], s[4:5], 0, v[2:3]
	v_lshlrev_b32_e32 v2, 4, v78
	v_lshl_add_u64 v[4:5], s[10:11], 2, v[4:5]
	v_lshl_add_u64 v[72:73], v[4:5], 0, v[2:3]
	v_add_co_u32_e32 v38, vcc, s18, v72
	s_mov_b32 s4, 0x15000
	s_nop 0
	v_addc_co_u32_e32 v39, vcc, 0, v73, vcc
	v_add_co_u32_e32 v40, vcc, s17, v72
	v_lshrrev_b32_e32 v2, 2, v0
	s_nop 0
	v_addc_co_u32_e32 v41, vcc, 0, v73, vcc
	v_add_co_u32_e32 v12, vcc, s19, v72
	s_mov_b32 s11, 1
	s_nop 0
	v_addc_co_u32_e32 v13, vcc, 0, v73, vcc
	v_add_co_u32_e32 v14, vcc, s20, v72
	s_mov_b32 s17, 0xcf000
	s_nop 0
	v_addc_co_u32_e32 v15, vcc, 0, v73, vcc
	v_add_co_u32_e32 v20, vcc, s21, v72
	global_load_dwordx4 v[4:7], v[12:13], off
	global_load_dwordx4 v[8:11], v[14:15], off
	v_addc_co_u32_e32 v21, vcc, 0, v73, vcc
	v_add_co_u32_e32 v22, vcc, s22, v72
	s_mov_b32 s18, 0xd2000
	s_nop 0
	v_addc_co_u32_e32 v23, vcc, 0, v73, vcc
	v_add_co_u32_e32 v42, vcc, s4, v72
	global_load_dwordx4 v[12:15], v[20:21], off
	global_load_dwordx4 v[16:19], v[22:23], off
	v_addc_co_u32_e32 v43, vcc, 0, v73, vcc
	global_load_dwordx4 v[20:23], v[42:43], off
	global_load_dwordx4 v[24:27], v[38:39], off
	global_load_dwordx4 v[28:31], v[40:41], off
	global_load_dwordx4 v[32:35], v[72:73], off
	v_lshlrev_b32_e32 v40, 1, v0
	v_bfe_u32 v38, v0, 2, 1
	v_lshlrev_b32_e32 v41, 2, v78
	v_and_b32_e32 v40, 6, v40
	v_bitop3_b32 v38, v38, v48, v40 bitop3:0x36
	v_or_b32_e32 v40, 2, v41
	v_or_b32_e32 v49, 3, v41
	v_lshrrev_b32_e32 v41, 1, v44
	v_lshlrev_b32_e32 v83, 4, v38
	v_bfe_u32 v38, v40, 1, 3
	v_lshlrev_b32_e32 v84, 7, v40
	v_xor_b32_e32 v40, v41, v0
	v_or_b32_e32 v42, 0x400, v81
	v_bitop3_b32 v38, v2, v38, 1 bitop3:0x6c
	v_lshlrev_b32_e32 v40, 4, v40
	v_mov_b32_e32 v39, v3
	v_or_b32_e32 v43, 0x800, v81
	v_readfirstlane_b32 s14, v42
	v_xor_b32_e32 v41, v38, v48
	v_and_b32_e32 v38, 0x70, v40
	s_waitcnt vmcnt(8)
	v_mad_i64_i32 v[36:37], s[4:5], v45, s2, v[36:37]
	v_readfirstlane_b32 s15, v43
	v_lshl_add_u64 v[74:75], v[36:37], 0, v[38:39]
	global_load_lds_dwordx4 v[66:67], off
	s_mov_b32 m0, s14
	v_bfe_u32 v50, v49, 1, 3
	global_load_lds_dwordx4 v[74:75], off
	s_mov_b32 m0, s15
	v_bitop3_b32 v2, v2, v50, 1 bitop3:0x6c
	global_load_lds_dwordx4 v[68:69], off
	s_mov_b32 m0, s16
	v_xor_b32_e32 v2, v2, v48
	global_load_lds_dwordx4 v[70:71], off
	v_readfirstlane_b32 s40, v81
	s_mov_b64 s[44:45], 0x3000
	s_mov_b64 s[46:47], 0x6000
	s_mov_b64 s[48:49], 0x9000
	s_mov_b64 s[50:51], 0xc000
	s_mov_b64 s[52:53], 0xf000
	s_mov_b64 s[54:55], 0x12000
	s_mov_b64 s[56:57], 0x15000
	s_mov_b32 s41, 0
	s_mov_b32 s42, 0x4000
	s_mov_b32 s43, 0x8000
	s_movk_i32 s2, 0x80
	s_add_i32 s23, s40, s42
	v_lshl_add_u64 v[144:145], v[66:67], 0, s[2:3]
	s_mov_b32 m0, s23
	s_add_i32 s23, s23, 0x400
	global_load_lds_dwordx4 v[144:145], off
	v_lshl_add_u64 v[144:145], v[74:75], 0, s[2:3]
	s_mov_b32 m0, s23
	s_add_i32 s23, s23, 0x400
	global_load_lds_dwordx4 v[144:145], off
	v_lshl_add_u64 v[144:145], v[68:69], 0, s[2:3]
	s_mov_b32 m0, s23
	s_add_i32 s23, s23, 0x400
	global_load_lds_dwordx4 v[144:145], off
	v_lshl_add_u64 v[144:145], v[70:71], 0, s[2:3]
	s_mov_b32 m0, s23
	s_nop 0
	global_load_lds_dwordx4 v[144:145], off
	s_mov_b32 s22, 0xc0000
	s_mov_b32 s23, 0
	v_lshl_add_u64 v[176:177], v[72:73], 0, s[22:23]
	v_lshl_add_u64 v[178:179], v[176:177], 0, s[44:45]
	v_lshl_add_u64 v[180:181], v[176:177], 0, s[46:47]
	v_lshl_add_u64 v[182:183], v[176:177], 0, s[48:49]
	v_lshl_add_u64 v[184:185], v[176:177], 0, s[50:51]
	v_lshl_add_u64 v[186:187], v[176:177], 0, s[52:53]
	v_lshl_add_u64 v[188:189], v[176:177], 0, s[54:55]
	v_lshl_add_u64 v[190:191], v[176:177], 0, s[56:57]
	global_load_dwordx4 v[144:147], v[176:177], off
	global_load_dwordx4 v[148:151], v[178:179], off
	global_load_dwordx4 v[152:155], v[180:181], off
	global_load_dwordx4 v[156:159], v[182:183], off
	global_load_dwordx4 v[160:163], v[184:185], off
	global_load_dwordx4 v[164:167], v[186:187], off
	global_load_dwordx4 v[168:171], v[188:189], off
	global_load_dwordx4 v[172:175], v[190:191], off
	v_lshlrev_b32_e32 v86, 4, v2
	v_lshlrev_b32_e32 v87, 7, v49
	v_or_b32_e32 v51, v82, v83
	v_lshlrev_b32_e32 v85, 4, v41
	v_add_u32_e32 v2, v87, v86
	v_add_u32_e32 v52, v84, v85
	s_mov_b64 s[4:5], 0x80
	s_mov_b32 s14, 0xc6000
	s_mov_b32 s15, 0xc9000
	s_mov_b32 s16, 0xcc000
	s_mov_b32 s19, 0xd5000
	s_mov_b32 s21, 0
	s_mov_b32 s20, 0
	v_mov_b32_e32 v48, v3
	v_mov_b32_e32 v49, v3
	v_mov_b32_e32 v50, v3
	s_waitcnt vmcnt(12)
	v_cvt_pk_f16_f32 v38, v8, v12
	v_cvt_pk_f16_f32 v39, v16, v20
	v_cvt_pk_f16_f32 v42, v9, v13
	v_cvt_pk_f16_f32 v37, v28, v4
	v_cvt_pk_f16_f32 v36, v32, v24
	v_cvt_pk_f16_f32 v45, v30, v6
	v_cvt_pk_f16_f32 v9, v19, v23
	v_cvt_pk_f16_f32 v8, v11, v15
	v_cvt_pk_f16_f32 v7, v31, v7
	v_cvt_pk_f16_f32 v6, v35, v27
	v_cvt_pk_f16_f32 v43, v17, v21
	v_cvt_pk_f16_f32 v41, v29, v5
	v_cvt_pk_f16_f32 v40, v33, v25
	v_cvt_pk_f16_f32 v47, v18, v22
	v_cvt_pk_f16_f32 v46, v10, v14
	v_cvt_pk_f16_f32 v44, v34, v26
	ds_write_b128 v51, v[36:39] offset:49152
	ds_write_b128 v51, v[40:43] offset:49280
	ds_write_b128 v52, v[44:47] offset:49152
	ds_write_b128 v2, v[6:9] offset:49152
	v_lshrrev_b32_e32 v2, 1, v0
	v_bfe_u32 v4, v0, 4, 1
	v_bitop3_b32 v2, v2, v4, 7 bitop3:0x6c
	v_xor_b32_e32 v4, v2, v77
	v_lshlrev_b32_e32 v88, 4, v4
	v_or_b32_e32 v4, 2, v77
	v_xor_b32_e32 v4, v2, v4
	v_lshlrev_b32_e32 v92, 4, v4
	v_or_b32_e32 v4, 4, v77
	v_xor_b32_e32 v4, v2, v4
	s_waitcnt vmcnt(12)
	v_lshlrev_b32_e32 v93, 4, v4
	v_or_b32_e32 v4, 6, v77
	v_xor_b32_e32 v2, v2, v4
	v_lshlrev_b32_e32 v94, 4, v2
	v_mov_b32_e32 v2, v3
	v_mov_b32_e32 v4, v3
	v_mov_b32_e32 v5, v3
	v_mov_b32_e32 v6, v3
	v_mov_b32_e32 v7, v3
	v_mov_b32_e32 v8, v3
	v_mov_b32_e32 v9, v3
	v_mov_b32_e32 v10, v3
	v_mov_b32_e32 v11, v3
	v_mov_b32_e32 v12, v3
	v_mov_b32_e32 v13, v3
	v_mov_b32_e32 v14, v3
	v_mov_b32_e32 v15, v3
	v_mov_b32_e32 v16, v3
	v_mov_b32_e32 v17, v3
	v_mov_b32_e32 v18, v3
	v_mov_b32_e32 v19, v3
	v_mov_b32_e32 v20, v3
	v_mov_b32_e32 v21, v3
	v_mov_b32_e32 v22, v3
	v_mov_b32_e32 v23, v3
	v_mov_b32_e32 v24, v3
	v_mov_b32_e32 v25, v3
	v_mov_b32_e32 v26, v3
	v_mov_b32_e32 v27, v3
	v_mov_b32_e32 v28, v3
	v_mov_b32_e32 v29, v3
	v_mov_b32_e32 v30, v3
	v_mov_b32_e32 v31, v3
	v_mov_b32_e32 v32, v3
	v_mov_b32_e32 v33, v3
	v_mov_b32_e32 v34, v3
	v_mov_b32_e32 v35, v3
	v_mov_b32_e32 v36, v3
	v_mov_b32_e32 v37, v3
	v_mov_b32_e32 v38, v3
	v_mov_b32_e32 v39, v3
	v_mov_b32_e32 v40, v3
	v_mov_b32_e32 v41, v3
	v_mov_b32_e32 v42, v3
	v_mov_b32_e32 v43, v3
	v_mov_b32_e32 v44, v3
	v_mov_b32_e32 v45, v3
	v_mov_b32_e32 v46, v3
	v_mov_b32_e32 v47, v3
	v_mov_b32_e32 v51, v3
	v_mov_b32_e32 v52, v3
	s_waitcnt lgkmcnt(0)
	s_barrier

.LBB13_20:
	s_endpgm
	s_endpgm

	.amdhsa_kernel _Z6gemm_kILi2ELi128ELi2ELi4EEv5GArgs
		.amdhsa_group_segment_fixed_size 81920
		.amdhsa_private_segment_fixed_size 0
		.amdhsa_kernarg_size 136
		.amdhsa_user_sgpr_count 2
		.amdhsa_user_sgpr_dispatch_ptr 0
		.amdhsa_user_sgpr_queue_ptr 0
		.amdhsa_user_sgpr_kernarg_segment_ptr 1
		.amdhsa_user_sgpr_dispatch_id 0
		.amdhsa_user_sgpr_kernarg_preload_length 0
		.amdhsa_user_sgpr_kernarg_preload_offset 0
		.amdhsa_user_sgpr_private_segment_size 0
		.amdhsa_uses_dynamic_stack 0
		.amdhsa_enable_private_segment 0
		.amdhsa_system_sgpr_workgroup_id_x 1
		.amdhsa_system_sgpr_workgroup_id_y 0
		.amdhsa_system_sgpr_workgroup_id_z 0
		.amdhsa_system_sgpr_workgroup_info 0
		.amdhsa_system_vgpr_workitem_id 0
		.amdhsa_next_free_vgpr 201
		.amdhsa_next_free_sgpr 96
		.amdhsa_accum_offset 204
		.amdhsa_reserve_vcc 1
		.amdhsa_float_round_mode_32 0
		.amdhsa_float_round_mode_16_64 0
		.amdhsa_float_denorm_mode_32 3
		.amdhsa_float_denorm_mode_16_64 3
		.amdhsa_dx10_clamp 1
		.amdhsa_ieee_mode 1
		.amdhsa_fp16_overflow 0
		.amdhsa_tg_split 0
		.amdhsa_exception_fp_ieee_invalid_op 0
		.amdhsa_exception_fp_denorm_src 0
		.amdhsa_exception_fp_ieee_div_zero 0
		.amdhsa_exception_fp_ieee_overflow 0
		.amdhsa_exception_fp_ieee_underflow 0
		.amdhsa_exception_fp_ieee_inexact 0
		.amdhsa_exception_int_div_zero 0
	.end_amdhsa_kernel

_Z7gemm2_kILi3ELi2ELi2EEv5GArgs:
	v_lshlrev_b32_e32 v176, 4, v0
	s_getpc_b64 s[92:93]
	s_add_u32 s92, s92, 0xfffedbf8
	s_addc_u32 s93, s93, 0xffffffff
	global_load_dwordx4 v[172:175], v176, s[92:93]
	s_load_dwordx4 s[8:11], s[0:1], 0x48
	s_load_dwordx2 s[20:21], s[0:1], 0x58
	s_cmpk_lt_u32 s2, 0xc0
	s_mov_b64 s[4:5], -1
	s_cbranch_scc0 .LBB14_39
	s_lshl_b32 s4, s2, 3
	s_lshl_b32 s3, s2, 8
	s_and_b32 s28, s4, 0x780
	s_load_dwordx4 s[12:15], s[0:1], 0x30
	s_load_dwordx2 s[22:23], s[0:1], 0x18
	s_load_dwordx4 s[16:19], s[0:1], 0x0
	s_and_b32 s3, s3, 0xf00
	s_add_i32 s29, s28, 0xfffffd00
	s_cmpk_gt_u32 s2, 0x5f
	v_lshrrev_b32_e32 v136, 6, v0
	s_cselect_b64 s[26:27], -1, 0
	v_bfe_u32 v131, v0, 3, 3
	v_lshl_or_b32 v16, v136, 5, v131
	s_and_b64 s[6:7], s[26:27], exec
	s_cselect_b32 s4, 0xc00, 0
	v_or_b32_e32 v12, s3, v16
	s_waitcnt lgkmcnt(0)
	s_add_u32 s6, s16, s4
	v_mul_u32_u24_e32 v2, 0xc40, v12
	v_bfe_u32 v24, v0, 4, 2
	s_addc_u32 s7, s17, 0
	v_lshlrev_b32_e32 v34, 1, v2
	v_mov_b32_e32 v35, 0
	v_bitop3_b32 v4, v24, v0, 7 bitop3:0x78
	v_lshl_add_u64 v[2:3], s[6:7], 0, v[34:35]
	v_lshlrev_b32_e32 v4, 4, v4
	v_mov_b32_e32 v5, v35
	v_lshl_add_u64 v[2:3], v[2:3], 0, v[4:5]
	v_or_b32_e32 v5, 8, v16
	v_or_b32_e32 v6, s3, v5
	v_lshrrev_b32_e32 v5, 1, v5
	v_mul_u32_u24_e32 v6, 0xc40, v6
	v_mov_b32_e32 v7, v35
	v_xor_b32_e32 v10, v5, v0
	v_lshlrev_b64 v[6:7], 1, v[6:7]
	v_lshlrev_b32_e32 v10, 4, v10
	v_lshl_add_u64 v[8:9], s[6:7], 0, v[6:7]
	v_and_b32_e32 v10, 0x70, v10
	v_mov_b32_e32 v11, v35
	v_lshl_add_u64 v[8:9], v[8:9], 0, v[10:11]
	v_or_b32_e32 v10, 16, v12
	v_mul_u32_u24_e32 v10, 0xc40, v10
	v_lshlrev_b64 v[10:11], 1, v[10:11]
	v_lshl_add_u64 v[12:13], s[6:7], 0, v[10:11]
	v_xor_b32_e32 v14, 16, v4
	v_mov_b32_e32 v15, v35
	v_or_b32_e32 v18, 24, v16
	v_lshl_add_u64 v[12:13], v[12:13], 0, v[14:15]
	v_or_b32_e32 v14, s3, v18
	v_lshrrev_b32_e32 v18, 1, v18
	v_mul_u32_u24_e32 v14, 0xc40, v14
	v_xor_b32_e32 v18, v18, v0
	v_lshlrev_b64 v[14:15], 1, v[14:15]
	v_lshlrev_b32_e32 v18, 3, v18
	s_cmpk_lt_u32 s2, 0x60
	v_lshl_add_u64 v[16:17], s[6:7], 0, v[14:15]
	v_bitop3_b32 v18, v18, 8, 56 bitop3:0x6c
	s_cselect_b64 s[6:7], -1, 0
	v_lshlrev_b32_e32 v18, 1, v18
	v_mov_b32_e32 v19, v35
	s_and_b64 s[24:25], s[6:7], exec
	v_lshlrev_b32_e32 v83, 12, v136
	v_and_b32_e32 v20, 7, v0
	v_lshl_add_u64 v[16:17], v[16:17], 0, v[18:19]
	s_cselect_b32 s24, s28, s29
	v_lshl_or_b32 v19, v136, 4, v131
	v_readfirstlane_b32 s25, v83
	v_bitop3_b32 v30, v136, v20, 1 bitop3:0x6c
	v_or_b32_e32 v20, s24, v19
	s_mov_b32 m0, s25
	s_add_u32 s28, s18, s4
	v_mul_i32_i24_e32 v20, 0xc40, v20
	v_mov_b32_e32 v21, v35
	global_load_lds_dwordx4 v[2:3], off
	v_or_b32_e32 v2, 0x400, v83
	s_addc_u32 s29, s19, 0
	v_lshlrev_b64 v[20:21], 1, v[20:21]
	v_xor_b32_e32 v24, v30, v24
	v_readfirstlane_b32 s25, v2
	v_or_b32_e32 v2, 0x800, v83
	v_lshl_add_u64 v[22:23], s[28:29], 0, v[20:21]
	v_lshlrev_b32_e32 v24, 4, v24
	v_mov_b32_e32 v25, v35
	v_or_b32_e32 v19, 8, v19
	s_mov_b32 m0, s25
	v_readfirstlane_b32 s25, v2
	v_or_b32_e32 v2, 0xc00, v83
	v_lshl_add_u64 v[22:23], v[22:23], 0, v[24:25]
	v_or_b32_e32 v25, s24, v19
	global_load_lds_dwordx4 v[8:9], off
	s_mov_b32 m0, s25
	v_readfirstlane_b32 s25, v2
	v_lshlrev_b32_e32 v2, 11, v136
	v_mul_i32_i24_e32 v26, 0xc40, v25
	v_mov_b32_e32 v27, v35
	v_bfe_u32 v19, v19, 1, 3
	v_or_b32_e32 v85, 0x10000, v2
	v_lshlrev_b64 v[26:27], 1, v[26:27]
	v_xor_b32_e32 v19, v30, v19
	global_load_lds_dwordx4 v[12:13], off
	s_mov_b32 m0, s25
	v_readfirstlane_b32 s25, v85
	v_or_b32_e32 v2, 0x10400, v2
	v_lshl_add_u64 v[28:29], s[28:29], 0, v[26:27]
	v_lshlrev_b32_e32 v30, 4, v19
	v_mov_b32_e32 v31, v35
	global_load_lds_dwordx4 v[16:17], off
	s_mov_b32 m0, s25
	v_readfirstlane_b32 s25, v2
	v_lshl_add_u64 v[28:29], v[28:29], 0, v[30:31]
	global_load_lds_dwordx4 v[22:23], off
	s_mov_b32 m0, s25
	v_bfe_u32 v138, v0, 5, 1
	global_load_lds_dwordx4 v[28:29], off
	v_lshrrev_b32_e32 v2, 1, v0
	v_bfe_u32 v3, v0, 4, 1
	v_bitop3_b32 v2, v2, v3, 7 bitop3:0x6c
	v_or_b32_e32 v8, 2, v138
	v_xor_b32_e32 v8, v8, v2
	v_lshlrev_b32_e32 v84, 4, v8
	v_or_b32_e32 v8, 4, v138
	v_xor_b32_e32 v8, v8, v2
	v_lshrrev_b32_e32 v1, 7, v0
	v_xor_b32_e32 v3, v2, v138
	v_lshlrev_b32_e32 v82, 4, v8
	v_or_b32_e32 v8, 6, v138
	v_bfe_u32 v126, v0, 6, 1
	v_and_b32_e32 v139, 31, v0
	v_lshlrev_b32_e32 v3, 4, v3
	v_lshlrev_b32_e32 v80, 13, v1
	v_xor_b32_e32 v2, v8, v2
	v_lshlrev_b32_e32 v78, 7, v139
	v_lshlrev_b32_e32 v79, 13, v126
	v_lshlrev_b32_e32 v81, 4, v2
	v_or_b32_e32 v2, v3, v80
	v_add_u32_e32 v86, v2, v78
	v_or3_b32 v2, v3, v79, v78
	v_add_u32_e32 v87, 0x10000, v2
	v_or_b32_e32 v2, s4, v4
	v_mov_b32_e32 v3, v35
	v_lshl_add_u64 v[2:3], v[2:3], 0, v[34:35]
	v_lshl_add_u64 v[2:3], s[16:17], 0, v[2:3]
	s_mov_b64 s[28:29], 0x80
	v_lshl_add_u64 v[66:67], v[2:3], 0, s[28:29]
	v_bitop3_b32 v2, v5, 7, v0 bitop3:0x48
	v_lshl_or_b32 v34, v2, 4, s4
	v_lshl_add_u64 v[2:3], v[34:35], 0, v[6:7]
	s_mov_b32 s5, 0
	v_lshl_add_u64 v[2:3], s[16:17], 0, v[2:3]
	v_lshl_add_u64 v[68:69], v[2:3], 0, s[28:29]
	v_lshl_add_u64 v[2:3], s[4:5], 0, v[10:11]
	v_bitop3_b32 v2, v2, v4, 16 bitop3:0xf6
	v_lshl_add_u64 v[2:3], s[16:17], 0, v[2:3]
	v_lshl_add_u64 v[70:71], v[2:3], 0, s[28:29]
	v_lshl_add_u64 v[2:3], s[4:5], 0, v[14:15]
	v_or_b32_e32 v2, v2, v18
	v_lshl_add_u64 v[2:3], s[16:17], 0, v[2:3]
	v_or_b32_e32 v34, s4, v24
	v_lshl_add_u64 v[72:73], v[2:3], 0, s[28:29]
	v_lshl_add_u64 v[2:3], v[34:35], 0, v[20:21]
	v_lshl_add_u64 v[2:3], s[18:19], 0, v[2:3]
	v_or_b32_e32 v34, s4, v30
	s_waitcnt vmcnt(0)
	v_lshl_add_u64 v[74:75], v[2:3], 0, s[28:29]
	v_lshl_add_u64 v[2:3], v[34:35], 0, v[26:27]
	v_lshl_add_u64 v[2:3], s[18:19], 0, v[2:3]
	v_lshl_add_u64 v[76:77], v[2:3], 0, s[28:29]
	s_mov_b64 s[16:17], 0
	v_mov_b32_e32 v88, 0x8000
	v_mov_b32_e32 v34, v35
	v_mov_b32_e32 v36, v35
	v_mov_b32_e32 v37, v35
	v_mov_b32_e32 v38, v35
	v_mov_b32_e32 v39, v35
	v_mov_b32_e32 v40, v35
	v_mov_b32_e32 v41, v35
	v_mov_b32_e32 v42, v35
	v_mov_b32_e32 v43, v35
	v_mov_b32_e32 v44, v35
	v_mov_b32_e32 v45, v35
	v_mov_b32_e32 v46, v35
	v_mov_b32_e32 v47, v35
	v_mov_b32_e32 v48, v35
	v_mov_b32_e32 v49, v35
	v_mov_b32_e32 v50, v35
	v_mov_b32_e32 v51, v35
	v_mov_b32_e32 v52, v35
	v_mov_b32_e32 v53, v35
	v_mov_b32_e32 v54, v35
	v_mov_b32_e32 v55, v35
	v_mov_b32_e32 v56, v35
	v_mov_b32_e32 v57, v35
	v_mov_b32_e32 v58, v35
	v_mov_b32_e32 v59, v35
	v_mov_b32_e32 v60, v35
	v_mov_b32_e32 v61, v35
	v_mov_b32_e32 v62, v35
	v_mov_b32_e32 v63, v35
	v_mov_b32_e32 v64, v35
	v_mov_b32_e32 v65, v35
	v_mov_b32_e32 v18, v35
	v_mov_b32_e32 v19, v35
	v_mov_b32_e32 v20, v35
	v_mov_b32_e32 v21, v35
	v_mov_b32_e32 v22, v35
	v_mov_b32_e32 v23, v35
	v_mov_b32_e32 v24, v35
	v_mov_b32_e32 v25, v35
	v_mov_b32_e32 v26, v35
	v_mov_b32_e32 v27, v35
	v_mov_b32_e32 v28, v35
	v_mov_b32_e32 v29, v35
	v_mov_b32_e32 v30, v35
	v_mov_b32_e32 v32, v35
	v_mov_b32_e32 v33, v35
	v_mov_b32_e32 v2, v35
	v_mov_b32_e32 v3, v35
	v_mov_b32_e32 v4, v35
	v_mov_b32_e32 v5, v35
	v_mov_b32_e32 v6, v35
	v_mov_b32_e32 v7, v35
	v_mov_b32_e32 v8, v35
	v_mov_b32_e32 v9, v35
	v_mov_b32_e32 v10, v35
	v_mov_b32_e32 v11, v35
	v_mov_b32_e32 v12, v35
	v_mov_b32_e32 v13, v35
	v_mov_b32_e32 v14, v35
	v_mov_b32_e32 v15, v35
	v_mov_b32_e32 v16, v35
	v_mov_b32_e32 v17, v35
	s_waitcnt vmcnt(0) lgkmcnt(0)
	s_barrier

.LBB14_51:
	s_endpgm
	s_nop 0
	s_nop 0
	s_nop 0
	s_nop 0
	s_nop 0
	s_nop 0
	s_nop 0
	s_nop 0
	s_nop 0
	s_nop 0
	s_nop 0
	s_nop 0
	s_nop 0
	s_nop 0
	s_nop 0
	s_nop 0
	s_nop 0
	s_nop 0
	s_nop 0
	s_nop 0
	s_nop 0
	s_nop 0
	s_nop 0
	s_nop 0
	s_nop 0
	s_nop 0
	s_nop 0
	s_nop 0
	s_nop 0
	s_nop 0
	s_nop 0
	s_nop 0
	s_nop 0
	s_nop 0
	s_nop 0
	s_nop 0
	s_nop 0
	s_nop 0
	s_nop 0
	s_nop 0
	s_nop 0
	s_nop 0
	s_nop 0
	s_nop 0
	s_nop 0
	s_nop 0
	s_nop 0
	s_nop 0
	s_nop 0
	s_nop 0
	s_nop 0
	s_nop 0
	s_nop 0
	s_nop 0
	s_nop 0
	s_nop 0
	s_endpgm

	.amdhsa_kernel _Z7gemm2_kILi3ELi2ELi2EEv5GArgs
		.amdhsa_group_segment_fixed_size 98304
		.amdhsa_private_segment_fixed_size 0
		.amdhsa_kernarg_size 136
		.amdhsa_user_sgpr_count 2
		.amdhsa_user_sgpr_dispatch_ptr 0
		.amdhsa_user_sgpr_queue_ptr 0
		.amdhsa_user_sgpr_kernarg_segment_ptr 1
		.amdhsa_user_sgpr_dispatch_id 0
		.amdhsa_user_sgpr_kernarg_preload_length 0
		.amdhsa_user_sgpr_kernarg_preload_offset 0
		.amdhsa_user_sgpr_private_segment_size 0
		.amdhsa_uses_dynamic_stack 0
		.amdhsa_enable_private_segment 0
		.amdhsa_system_sgpr_workgroup_id_x 1
		.amdhsa_system_sgpr_workgroup_id_y 0
		.amdhsa_system_sgpr_workgroup_id_z 0
		.amdhsa_system_sgpr_workgroup_info 0
		.amdhsa_system_vgpr_workitem_id 0
		.amdhsa_next_free_vgpr 177
		.amdhsa_next_free_sgpr 96
		.amdhsa_accum_offset 180
		.amdhsa_reserve_vcc 1
		.amdhsa_float_round_mode_32 0
		.amdhsa_float_round_mode_16_64 0
		.amdhsa_float_denorm_mode_32 3
		.amdhsa_float_denorm_mode_16_64 3
		.amdhsa_dx10_clamp 1
		.amdhsa_ieee_mode 1
		.amdhsa_fp16_overflow 0
		.amdhsa_tg_split 0
		.amdhsa_exception_fp_ieee_invalid_op 0
		.amdhsa_exception_fp_denorm_src 0
		.amdhsa_exception_fp_ieee_div_zero 0
		.amdhsa_exception_fp_ieee_overflow 0
		.amdhsa_exception_fp_ieee_underflow 0
		.amdhsa_exception_fp_ieee_inexact 0
		.amdhsa_exception_int_div_zero 0
	.end_amdhsa_kernel

_Z7gemv8_kILi192ELi3072EEvPKfS1_Pf:
	v_lshlrev_b32_e32 v132, 4, v0
	s_getpc_b64 s[92:93]
	s_add_u32 s92, s92, 0xffff38f8
	s_addc_u32 s93, s93, 0xffffffff
	global_load_dwordx4 v[128:131], v132, s[92:93]
	v_add_u32_e32 v132, 0x1000, v132
	global_load_dwordx4 v[128:131], v132, s[92:93]
	v_lshlrev_b32_e32 v132, 4, v0
	s_load_dwordx4 s[4:7], s[0:1], 0x0
	s_load_dwordx2 s[8:9], s[0:1], 0x10
	s_mul_i32 s0, s3, 0xc0
	s_ashr_i32 s1, s0, 31
	s_lshl_b64 s[10:11], s[0:1], 2
	s_waitcnt lgkmcnt(0)
	s_add_u32 s12, s4, s10
	s_addc_u32 s13, s5, s11
	s_mov_b64 s[4:5], 0
	s_mov_b32 s1, 0xaaab
	s_movk_i32 s10, 0x3000
	v_mov_b64_e32 v[2:3], s[12:13]
	v_mov_b32_e32 v5, 0
	s_movk_i32 s11, 0x300
	s_movk_i32 s12, 0x4ff
	v_mov_b32_e32 v1, v0

	.amdhsa_kernel _Z7gemv8_kILi192ELi3072EEvPKfS1_Pf
		.amdhsa_group_segment_fixed_size 38912
		.amdhsa_private_segment_fixed_size 0
		.amdhsa_kernarg_size 24
		.amdhsa_user_sgpr_count 2
		.amdhsa_user_sgpr_dispatch_ptr 0
		.amdhsa_user_sgpr_queue_ptr 0
		.amdhsa_user_sgpr_kernarg_segment_ptr 1
		.amdhsa_user_sgpr_dispatch_id 0
		.amdhsa_user_sgpr_kernarg_preload_length 0
		.amdhsa_user_sgpr_kernarg_preload_offset 0
		.amdhsa_user_sgpr_private_segment_size 0
		.amdhsa_uses_dynamic_stack 0
		.amdhsa_enable_private_segment 0
		.amdhsa_system_sgpr_workgroup_id_x 1
		.amdhsa_system_sgpr_workgroup_id_y 1
		.amdhsa_system_sgpr_workgroup_id_z 0
		.amdhsa_system_sgpr_workgroup_info 0
		.amdhsa_system_vgpr_workitem_id 0
		.amdhsa_next_free_vgpr 133
		.amdhsa_next_free_sgpr 96
		.amdhsa_accum_offset 136
		.amdhsa_reserve_vcc 1
		.amdhsa_float_round_mode_32 0
		.amdhsa_float_round_mode_16_64 0
		.amdhsa_float_denorm_mode_32 3
		.amdhsa_float_denorm_mode_16_64 3
		.amdhsa_dx10_clamp 1
		.amdhsa_ieee_mode 1
		.amdhsa_fp16_overflow 0
		.amdhsa_tg_split 0
		.amdhsa_exception_fp_ieee_invalid_op 0
		.amdhsa_exception_fp_denorm_src 0
		.amdhsa_exception_fp_ieee_div_zero 0
		.amdhsa_exception_fp_ieee_overflow 0
		.amdhsa_exception_fp_ieee_underflow 0
		.amdhsa_exception_fp_ieee_inexact 0
		.amdhsa_exception_int_div_zero 0
	.end_amdhsa_kernel

amdhsa.kernels:
  - .agpr_count:     0
    .args:
      - .address_space:  global
        .offset:         0
        .size:           8
        .value_kind:     global_buffer
    .group_segment_fixed_size: 0
    .kernarg_segment_align: 8
    .kernarg_segment_size: 8
    .language:       OpenCL C
    .language_version:
      - 2
      - 0
    .max_flat_workgroup_size: 1024
    .name:           _Z7empty_kPi
    .private_segment_fixed_size: 0
    .sgpr_count:     6
    .sgpr_spill_count: 0
    .symbol:         _Z7empty_kPi.kd
    .uniform_work_group_size: 1
    .uses_dynamic_stack: false
    .vgpr_count:     0
    .vgpr_spill_count: 0
    .wavefront_size: 64
  - .agpr_count:     0
    .args:
      - .actual_access:  read_only
        .address_space:  global
        .offset:         0
        .size:           8
        .value_kind:     global_buffer
      - .actual_access:  read_only
        .address_space:  global
        .offset:         8
        .size:           8
        .value_kind:     global_buffer
      - .actual_access:  read_only
        .address_space:  global
        .offset:         16
        .size:           8
        .value_kind:     global_buffer
      - .actual_access:  read_only
        .address_space:  global
        .offset:         24
        .size:           8
        .value_kind:     global_buffer
      - .actual_access:  write_only
        .address_space:  global
        .offset:         32
        .size:           8
        .value_kind:     global_buffer
      - .actual_access:  write_only
        .address_space:  global
        .offset:         40
        .size:           8
        .value_kind:     global_buffer
    .group_segment_fixed_size: 0
    .kernarg_segment_align: 8
    .kernarg_segment_size: 48
    .language:       OpenCL C
    .language_version:
      - 2
      - 0
    .max_flat_workgroup_size: 256
    .name:           _Z4ln_kPKfS0_S0_S0_PfPDF16_
    .private_segment_fixed_size: 0
    .sgpr_count:     102
    .sgpr_spill_count: 0
    .symbol:         _Z4ln_kPKfS0_S0_S0_PfPDF16_.kd
    .uniform_work_group_size: 1
    .uses_dynamic_stack: false
    .vgpr_count:     65
    .vgpr_spill_count: 0
    .wavefront_size: 64
  - .agpr_count:     0
    .args:
      - .actual_access:  read_only
        .address_space:  global
        .offset:         0
        .size:           8
        .value_kind:     global_buffer
      - .actual_access:  read_only
        .address_space:  global
        .offset:         8
        .size:           8
        .value_kind:     global_buffer
      - .actual_access:  read_only
        .address_space:  global
        .offset:         16
        .size:           8
        .value_kind:     global_buffer
      - .actual_access:  read_only
        .address_space:  global
        .offset:         24
        .size:           8
        .value_kind:     global_buffer
      - .actual_access:  read_only
        .address_space:  global
        .offset:         32
        .size:           8
        .value_kind:     global_buffer
      - .actual_access:  write_only
        .address_space:  global
        .offset:         40
        .size:           8
        .value_kind:     global_buffer
      - .actual_access:  write_only
        .address_space:  global
        .offset:         48
        .size:           8
        .value_kind:     global_buffer
      - .actual_access:  write_only
        .address_space:  global
        .offset:         56
        .size:           8
        .value_kind:     global_buffer
      - .actual_access:  write_only
        .address_space:  global
        .offset:         64
        .size:           8
        .value_kind:     global_buffer
      - .offset:         72
        .size:           4
        .value_kind:     by_value
    .group_segment_fixed_size: 24704
    .kernarg_segment_align: 8
    .kernarg_segment_size: 76
    .language:       OpenCL C
    .language_version:
      - 2
      - 0
    .max_flat_workgroup_size: 1024
    .name:           _Z11ln_router_kPKfS0_S0_S0_S0_PfPDF16_PiS1_i
    .private_segment_fixed_size: 0
    .sgpr_count:     102
    .sgpr_spill_count: 0
    .symbol:         _Z11ln_router_kPKfS0_S0_S0_S0_PfPDF16_PiS1_i.kd
    .uniform_work_group_size: 1
    .uses_dynamic_stack: false
    .vgpr_count:     61
    .vgpr_spill_count: 0
    .wavefront_size: 64
  - .agpr_count:     0
    .args:
      - .actual_access:  read_only
        .address_space:  global
        .offset:         0
        .size:           8
        .value_kind:     global_buffer
      - .actual_access:  write_only
        .address_space:  global
        .offset:         8
        .size:           8
        .value_kind:     global_buffer
      - .actual_access:  write_only
        .address_space:  global
        .offset:         16
        .size:           8
        .value_kind:     global_buffer
    .group_segment_fixed_size: 4176
    .kernarg_segment_align: 8
    .kernarg_segment_size: 24
    .language:       OpenCL C
    .language_version:
      - 2
      - 0
    .max_flat_workgroup_size: 1024
    .name:           _Z6sort_kPKiPiS1_
    .private_segment_fixed_size: 0
    .sgpr_count:     102
    .sgpr_spill_count: 0
    .symbol:         _Z6sort_kPKiPiS1_.kd
    .uniform_work_group_size: 1
    .uses_dynamic_stack: false
    .vgpr_count:     53
    .vgpr_spill_count: 0
    .wavefront_size: 64
  - .agpr_count:     0
    .args:
      - .offset:         0
        .size:           272
        .value_kind:     by_value
      - .actual_access:  read_only
        .address_space:  global
        .offset:         272
        .size:           8
        .value_kind:     global_buffer
      - .actual_access:  read_only
        .address_space:  global
        .offset:         280
        .size:           8
        .value_kind:     global_buffer
      - .actual_access:  read_only
        .address_space:  global
        .offset:         288
        .size:           8
        .value_kind:     global_buffer
      - .actual_access:  read_only
        .address_space:  global
        .offset:         296
        .size:           8
        .value_kind:     global_buffer
      - .actual_access:  read_only
        .address_space:  global
        .offset:         304
        .size:           8
        .value_kind:     global_buffer
      - .actual_access:  read_only
        .address_space:  global
        .offset:         312
        .size:           8
        .value_kind:     global_buffer
      - .actual_access:  read_only
        .address_space:  global
        .offset:         320
        .size:           8
        .value_kind:     global_buffer
      - .actual_access:  write_only
        .address_space:  global
        .offset:         328
        .size:           8
        .value_kind:     global_buffer
      - .actual_access:  write_only
        .address_space:  global
        .offset:         336
        .size:           8
        .value_kind:     global_buffer
      - .actual_access:  write_only
        .address_space:  global
        .offset:         344
        .size:           8
        .value_kind:     global_buffer
    .group_segment_fixed_size: 16640
    .kernarg_segment_align: 8
    .kernarg_segment_size: 352
    .language:       OpenCL C
    .language_version:
      - 2
      - 0
    .max_flat_workgroup_size: 256
    .name:           _Z5pre_k7CvtArgsPKiS1_PKfS3_S3_S3_S3_PfPDF16_S4_
    .private_segment_fixed_size: 0
    .sgpr_count:     102
    .sgpr_spill_count: 0
    .symbol:         _Z5pre_k7CvtArgsPKiS1_PKfS3_S3_S3_S3_PfPDF16_S4_.kd
    .uniform_work_group_size: 1
    .uses_dynamic_stack: false
    .vgpr_count:     73
    .vgpr_spill_count: 0
    .wavefront_size: 64
  - .agpr_count:     0
    .args:
      - .actual_access:  read_only
        .address_space:  global
        .offset:         0
        .size:           8
        .value_kind:     global_buffer
      - .actual_access:  read_only
        .address_space:  global
        .offset:         8
        .size:           8
        .value_kind:     global_buffer
      - .actual_access:  read_only
        .address_space:  global
        .offset:         16
        .size:           8
        .value_kind:     global_buffer
      - .actual_access:  read_only
        .address_space:  global
        .offset:         24
        .size:           8
        .value_kind:     global_buffer
      - .actual_access:  write_only
        .address_space:  global
        .offset:         32
        .size:           8
        .value_kind:     global_buffer
      - .actual_access:  read_only
        .address_space:  global
        .offset:         40
        .size:           8
        .value_kind:     global_buffer
      - .offset:         48
        .size:           4
        .value_kind:     by_value
      - .actual_access:  write_only
        .address_space:  global
        .offset:         56
        .size:           8
        .value_kind:     global_buffer
    .group_segment_fixed_size: 133120
    .kernarg_segment_align: 8
    .kernarg_segment_size: 64
    .language:       OpenCL C
    .language_version:
      - 2
      - 0
    .max_flat_workgroup_size: 512
    .name:           _Z6attn_kPKDF16_S0_S0_PKfPDF16_PK15HIP_vector_typeIfLj4EEiPf
    .private_segment_fixed_size: 0
    .sgpr_count:     102
    .sgpr_spill_count: 0
    .symbol:         _Z6attn_kPKDF16_S0_S0_PKfPDF16_PK15HIP_vector_typeIfLj4EEiPf.kd
    .uniform_work_group_size: 1
    .uses_dynamic_stack: false
    .vgpr_count:     177
    .vgpr_spill_count: 0
    .wavefront_size: 64
  - .agpr_count:     0
    .args:
      - .actual_access:  read_only
        .address_space:  global
        .offset:         0
        .size:           8
        .value_kind:     global_buffer
      - .actual_access:  read_only
        .address_space:  global
        .offset:         8
        .size:           8
        .value_kind:     global_buffer
      - .actual_access:  read_only
        .address_space:  global
        .offset:         16
        .size:           8
        .value_kind:     global_buffer
      - .actual_access:  read_only
        .address_space:  global
        .offset:         24
        .size:           8
        .value_kind:     global_buffer
      - .actual_access:  write_only
        .address_space:  global
        .offset:         32
        .size:           8
        .value_kind:     global_buffer
      - .actual_access:  read_only
        .address_space:  global
        .offset:         40
        .size:           8
        .value_kind:     global_buffer
      - .actual_access:  read_only
        .address_space:  global
        .offset:         48
        .size:           8
        .value_kind:     global_buffer
      - .actual_access:  write_only
        .address_space:  global
        .offset:         56
        .size:           8
        .value_kind:     global_buffer
      - .actual_access:  read_only
        .address_space:  global
        .offset:         64
        .size:           8
        .value_kind:     global_buffer
      - .offset:         72
        .size:           4
        .value_kind:     by_value
      - .actual_access:  read_only
        .address_space:  global
        .offset:         80
        .size:           8
        .value_kind:     global_buffer
      - .offset:         88
        .size:           4
        .value_kind:     by_value
      - .actual_access:  write_only
        .address_space:  global
        .offset:         96
        .size:           8
        .value_kind:     global_buffer
    .group_segment_fixed_size: 7168
    .kernarg_segment_align: 8
    .kernarg_segment_size: 104
    .language:       OpenCL C
    .language_version:
      - 2
      - 0
    .max_flat_workgroup_size: 256
    .name:           _Z9tail_up_kPKfPKiS0_S0_PfS0_S2_S3_PK15HIP_vector_typeIfLj4EEiS7_iS3_
    .private_segment_fixed_size: 0
    .sgpr_count:     102
    .sgpr_spill_count: 0
    .symbol:         _Z9tail_up_kPKfPKiS0_S0_PfS0_S2_S3_PK15HIP_vector_typeIfLj4EEiS7_iS3_.kd
    .uniform_work_group_size: 1
    .uses_dynamic_stack: false
    .vgpr_count:     117
    .vgpr_spill_count: 0
    .wavefront_size: 64
  - .agpr_count:     0
    .args:
      - .actual_access:  read_only
        .address_space:  global
        .offset:         0
        .size:           8
        .value_kind:     global_buffer
      - .offset:         8
        .size:           4
        .value_kind:     by_value
      - .actual_access:  read_only
        .address_space:  global
        .offset:         16
        .size:           8
        .value_kind:     global_buffer
      - .actual_access:  read_only
        .address_space:  global
        .offset:         24
        .size:           8
        .value_kind:     global_buffer
      - .actual_access:  read_only
        .address_space:  global
        .offset:         32
        .size:           8
        .value_kind:     global_buffer
      - .actual_access:  read_only
        .address_space:  global
        .offset:         40
        .size:           8
        .value_kind:     global_buffer
      - .actual_access:  write_only
        .address_space:  global
        .offset:         48
        .size:           8
        .value_kind:     global_buffer
    .group_segment_fixed_size: 0
    .kernarg_segment_align: 8
    .kernarg_segment_size: 56
    .language:       OpenCL C
    .language_version:
      - 2
      - 0
    .max_flat_workgroup_size: 512
    .name:           _Z9tail_ln_kPKfiS0_S0_S0_S0_Pf
    .private_segment_fixed_size: 0
    .sgpr_count:     22
    .sgpr_spill_count: 0
    .symbol:         _Z9tail_ln_kPKfiS0_S0_S0_S0_Pf.kd
    .uniform_work_group_size: 1
    .uses_dynamic_stack: false
    .vgpr_count:     48
    .vgpr_spill_count: 0
    .wavefront_size: 64
  - .agpr_count:     0
    .args:
      - .actual_access:  read_only
        .address_space:  global
        .offset:         0
        .size:           8
        .value_kind:     global_buffer
      - .actual_access:  read_only
        .address_space:  global
        .offset:         8
        .size:           8
        .value_kind:     global_buffer
      - .actual_access:  read_only
        .address_space:  global
        .offset:         16
        .size:           8
        .value_kind:     global_buffer
      - .actual_access:  read_only
        .address_space:  global
        .offset:         24
        .size:           8
        .value_kind:     global_buffer
      - .actual_access:  read_only
        .address_space:  global
        .offset:         32
        .size:           8
        .value_kind:     global_buffer
      - .actual_access:  read_only
        .address_space:  global
        .offset:         40
        .size:           8
        .value_kind:     global_buffer
      - .actual_access:  write_only
        .address_space:  global
        .offset:         48
        .size:           8
        .value_kind:     global_buffer
      - .actual_access:  write_only
        .address_space:  global
        .offset:         56
        .size:           8
        .value_kind:     global_buffer
    .group_segment_fixed_size: 47872
    .kernarg_segment_align: 8
    .kernarg_segment_size: 64
    .language:       OpenCL C
    .language_version:
      - 2
      - 0
    .max_flat_workgroup_size: 256
    .name:           _Z6pool_kPKfS0_S0_S0_S0_S0_PfS1_
    .private_segment_fixed_size: 0
    .sgpr_count:     102
    .sgpr_spill_count: 0
    .symbol:         _Z6pool_kPKfS0_S0_S0_S0_S0_PfS1_.kd
    .uniform_work_group_size: 1
    .uses_dynamic_stack: false
    .vgpr_count:     225
    .vgpr_spill_count: 0
    .wavefront_size: 64
  - .agpr_count:     0
    .args:
      - .actual_access:  read_only
        .address_space:  global
        .offset:         0
        .size:           8
        .value_kind:     global_buffer
      - .actual_access:  read_only
        .address_space:  global
        .offset:         8
        .size:           8
        .value_kind:     global_buffer
      - .actual_access:  read_only
        .address_space:  global
        .offset:         16
        .size:           8
        .value_kind:     global_buffer
      - .actual_access:  read_only
        .address_space:  global
        .offset:         24
        .size:           8
        .value_kind:     global_buffer
      - .actual_access:  read_only
        .address_space:  global
        .offset:         32
        .size:           8
        .value_kind:     global_buffer
      - .actual_access:  read_only
        .address_space:  global
        .offset:         40
        .size:           8
        .value_kind:     global_buffer
      - .actual_access:  write_only
        .address_space:  global
        .offset:         48
        .size:           8
        .value_kind:     global_buffer
    .group_segment_fixed_size: 16
    .kernarg_segment_align: 8
    .kernarg_segment_size: 56
    .language:       OpenCL C
    .language_version:
      - 2
      - 0
    .max_flat_workgroup_size: 256
    .name:           _Z8final2_kPKfS0_S0_S0_S0_S0_Pf
    .private_segment_fixed_size: 0
    .sgpr_count:     52
    .sgpr_spill_count: 0
    .symbol:         _Z8final2_kPKfS0_S0_S0_S0_S0_Pf.kd
    .uniform_work_group_size: 1
    .uses_dynamic_stack: false
    .vgpr_count:     67
    .vgpr_spill_count: 0
    .wavefront_size: 64
  - .agpr_count:     0
    .args:
      - .actual_access:  read_only
        .address_space:  global
        .offset:         0
        .size:           8
        .value_kind:     global_buffer
      - .offset:         8
        .size:           4
        .value_kind:     by_value
      - .actual_access:  read_only
        .address_space:  global
        .offset:         16
        .size:           8
        .value_kind:     global_buffer
      - .actual_access:  read_only
        .address_space:  global
        .offset:         24
        .size:           8
        .value_kind:     global_buffer
      - .actual_access:  read_only
        .address_space:  global
        .offset:         32
        .size:           8
        .value_kind:     global_buffer
      - .actual_access:  read_only
        .address_space:  global
        .offset:         40
        .size:           8
        .value_kind:     global_buffer
      - .actual_access:  write_only
        .address_space:  global
        .offset:         48
        .size:           8
        .value_kind:     global_buffer
    .group_segment_fixed_size: 0
    .kernarg_segment_align: 8
    .kernarg_segment_size: 56
    .language:       OpenCL C
    .language_version:
      - 2
      - 0
    .max_flat_workgroup_size: 512
    .name:           _Z7final_kPKfiS0_S0_S0_S0_Pf
    .private_segment_fixed_size: 0
    .sgpr_count:     36
    .sgpr_spill_count: 0
    .symbol:         _Z7final_kPKfiS0_S0_S0_S0_Pf.kd
    .uniform_work_group_size: 1
    .uses_dynamic_stack: false
    .vgpr_count:     20
    .vgpr_spill_count: 0
    .wavefront_size: 64
  - .agpr_count:     0
    .args:
      - .offset:         0
        .size:           136
        .value_kind:     by_value
    .group_segment_fixed_size: 114688
    .kernarg_segment_align: 8
    .kernarg_segment_size: 136
    .language:       OpenCL C
    .language_version:
      - 2
      - 0
    .max_flat_workgroup_size: 512
    .name:           _Z7gemm2_kILi0ELi3ELi1EEv5GArgs
    .private_segment_fixed_size: 0
    .sgpr_count:     102
    .sgpr_spill_count: 0
    .symbol:         _Z7gemm2_kILi0ELi3ELi1EEv5GArgs.kd
    .uniform_work_group_size: 1
    .uses_dynamic_stack: false
    .vgpr_count:     193
    .vgpr_spill_count: 0
    .wavefront_size: 64
  - .agpr_count:     0
    .args:
      - .offset:         0
        .size:           136
        .value_kind:     by_value
    .group_segment_fixed_size: 131072
    .kernarg_segment_align: 8
    .kernarg_segment_size: 136
    .language:       OpenCL C
    .language_version:
      - 2
      - 0
    .max_flat_workgroup_size: 512
    .name:           _Z6gemm_kILi1ELi128ELi4ELi8EEv5GArgs
    .private_segment_fixed_size: 0
    .sgpr_count:     102
    .sgpr_spill_count: 0
    .symbol:         _Z6gemm_kILi1ELi128ELi4ELi8EEv5GArgs.kd
    .uniform_work_group_size: 1
    .uses_dynamic_stack: false
    .vgpr_count:     177
    .vgpr_spill_count: 0
    .wavefront_size: 64
  - .agpr_count:     0
    .args:
      - .offset:         0
        .size:           136
        .value_kind:     by_value
    .group_segment_fixed_size: 81920
    .kernarg_segment_align: 8
    .kernarg_segment_size: 136
    .language:       OpenCL C
    .language_version:
      - 2
      - 0
    .max_flat_workgroup_size: 256
    .name:           _Z6gemm_kILi2ELi128ELi2ELi4EEv5GArgs
    .private_segment_fixed_size: 0
    .sgpr_count:     102
    .sgpr_spill_count: 0
    .symbol:         _Z6gemm_kILi2ELi128ELi2ELi4EEv5GArgs.kd
    .uniform_work_group_size: 1
    .uses_dynamic_stack: false
    .vgpr_count:     201
    .vgpr_spill_count: 0
    .wavefront_size: 64
  - .agpr_count:     0
    .args:
      - .offset:         0
        .size:           136
        .value_kind:     by_value
    .group_segment_fixed_size: 98304
    .kernarg_segment_align: 8
    .kernarg_segment_size: 136
    .language:       OpenCL C
    .language_version:
      - 2
      - 0
    .max_flat_workgroup_size: 512
    .name:           _Z7gemm2_kILi3ELi2ELi2EEv5GArgs
    .private_segment_fixed_size: 0
    .sgpr_count:     102
    .sgpr_spill_count: 0
    .symbol:         _Z7gemm2_kILi3ELi2ELi2EEv5GArgs.kd
    .uniform_work_group_size: 1
    .uses_dynamic_stack: false
    .vgpr_count:     177
    .vgpr_spill_count: 0
    .wavefront_size: 64
  - .agpr_count:     0
    .args:
      - .actual_access:  read_only
        .address_space:  global
        .offset:         0
        .size:           8
        .value_kind:     global_buffer
      - .actual_access:  read_only
        .address_space:  global
        .offset:         8
        .size:           8
        .value_kind:     global_buffer
      - .actual_access:  write_only
        .address_space:  global
        .offset:         16
        .size:           8
        .value_kind:     global_buffer
    .group_segment_fixed_size: 38912
    .kernarg_segment_align: 8
    .kernarg_segment_size: 24
    .language:       OpenCL C
    .language_version:
      - 2
      - 0
    .max_flat_workgroup_size: 256
    .name:           _Z7gemv8_kILi192ELi3072EEvPKfS1_Pf
    .private_segment_fixed_size: 0
    .sgpr_count:     102
    .sgpr_spill_count: 0
    .symbol:         _Z7gemv8_kILi192ELi3072EEvPKfS1_Pf.kd
    .uniform_work_group_size: 1
    .uses_dynamic_stack: false
    .vgpr_count:     133
    .vgpr_spill_count: 0
    .wavefront_size: 64
